# baseline (speedup 1.0000x reference)
_Z5gemm8ILi192ELi2ELi3ELi0ELi1ELi16EEvPKDF16_S1_iiiPDF16_PfPKf:
	v_readfirstlane_b32 s28, v0
	s_nop 3
	s_bitcmp1_b32 s28, 8
	s_cbranch_scc0 .Lprio_skip0
	s_setprio 1
.Lprio_skip0:
	s_load_dword s3, s[0:1], 0x38
	s_load_dwordx4 s[4:7], s[0:1], 0x0
	s_and_b32 s13, s2, 7
	s_waitcnt lgkmcnt(0)
	s_cmpk_lg_i32 s3, 0x200
	s_cbranch_scc0 .LBB4_2
	s_lshl_b32 s3, s13, 1
	s_and_b32 s3, s3, 12
	s_bfe_u32 s8, s2, 0x20003
	s_or_b32 s3, s3, s8
	s_lshl_b32 s8, s2, 3
	s_and_b32 s8, s8, 8
	s_lshr_b32 s9, s2, 5
	s_add_i32 s12, s8, s9
	s_load_dwordx2 s[8:9], s[0:1], 0x20
	s_cbranch_execz .LBB4_3
	s_branch .LBB4_4

.LBB4_4:
	s_load_dword s2, s[0:1], 0x18
	v_lshrrev_b32_e32 v6, 4, v0
	v_xor_b32_e32 v1, v6, v0
	v_lshlrev_b32_e32 v1, 3, v1
	v_and_b32_e32 v2, 56, v1
	v_lshrrev_b32_e32 v1, 3, v0
	s_waitcnt lgkmcnt(0)
	v_mad_u64_u32 v[4:5], s[0:1], v1, s2, v[2:3]
	v_or_b32_e32 v3, 0x200, v0
	v_lshrrev_b32_e32 v3, 3, v3
	s_lshl_b32 s10, s12, 7
	s_ashr_i32 s13, s2, 31
	v_mul_lo_u32 v3, v3, s2
	s_lshl_b32 s0, s2, 7
	v_add_lshl_u32 v2, v3, v2, 1
	v_add_lshl_u32 v3, v4, s0, 1
	s_mul_i32 s0, s10, s13
	s_mul_hi_u32 s1, s10, s2
	s_add_i32 s1, s1, s0
	s_mul_i32 s0, s10, s2
	s_mul_i32 s11, s3, 0xc0
	s_lshl_b64 s[0:1], s[0:1], 1
	v_lshlrev_b32_e32 v122, 4, v0
	v_lshlrev_b32_e32 v1, 1, v4
	s_add_u32 s0, s4, s0
	s_mul_i32 s3, s11, s13
	s_mul_hi_u32 s4, s11, s2
	v_add_u32_e32 v4, 0, v122
	s_addc_u32 s1, s5, s1
	s_add_i32 s3, s4, s3
	s_mul_i32 s2, s11, s2
	v_readfirstlane_b32 s13, v4
	v_add_u32_e32 v5, 0x2000, v4
	s_lshl_b64 s[2:3], s[2:3], 1
	s_mov_b32 m0, s13
	v_readfirstlane_b32 s4, v5
	v_add_u32_e32 v5, 0x4000, v4
	s_add_u32 s2, s6, s2
	global_load_lds_dwordx4 v1, s[0:1]
	s_mov_b32 m0, s4
	v_readfirstlane_b32 s5, v5
	v_add_u32_e32 v5, 0x6000, v4
	s_addc_u32 s3, s7, s3
	global_load_lds_dwordx4 v2, s[0:1]
	s_mov_b32 m0, s5
	v_readfirstlane_b32 s6, v5
	v_add_u32_e32 v5, 0x8000, v4
	global_load_lds_dwordx4 v1, s[2:3]
	s_mov_b32 m0, s6
	v_readfirstlane_b32 s7, v5
	v_add_u32_e32 v5, 0xa000, v4
	global_load_lds_dwordx4 v2, s[2:3]
	s_mov_b32 m0, s7
	s_add_u32 s16, s0, 0x80
	v_readfirstlane_b32 s18, v5
	v_add_u32_e32 v5, 0xc000, v4
	global_load_lds_dwordx4 v3, s[2:3]
	s_addc_u32 s17, s1, 0
	s_mov_b32 m0, s18
	v_readfirstlane_b32 s14, v5
	v_add_u32_e32 v5, 0xe000, v4
	s_add_u32 s20, s2, 0x80
	global_load_lds_dwordx4 v1, s[16:17]
	s_mov_b32 m0, s14
	v_readfirstlane_b32 s15, v5
	v_add_u32_e32 v5, 0x10000, v4
	s_addc_u32 s21, s3, 0
	global_load_lds_dwordx4 v2, s[16:17]
	s_mov_b32 m0, s15
	v_readfirstlane_b32 s16, v5
	v_add_u32_e32 v5, 0x12000, v4
	global_load_lds_dwordx4 v1, s[20:21]
	s_mov_b32 m0, s16
	v_readfirstlane_b32 s17, v5
	global_load_lds_dwordx4 v2, s[20:21]
	s_mov_b32 m0, s17
	v_add_u32_e32 v5, 0x14000, v4
	global_load_lds_dwordx4 v3, s[20:21]
	s_add_u32 s20, s0, 0x100
	v_readfirstlane_b32 s19, v5
	v_add_u32_e32 v5, 0x16000, v4
	s_addc_u32 s21, s1, 0
	s_mov_b32 m0, s19
	v_readfirstlane_b32 s19, v5
	v_add_u32_e32 v5, 0x18000, v4
	s_add_u32 s22, s2, 0x100
	global_load_lds_dwordx4 v1, s[20:21]
	s_mov_b32 m0, s19
	v_readfirstlane_b32 s19, v5
	v_add_u32_e32 v5, 0x1a000, v4
	s_addc_u32 s23, s3, 0
	global_load_lds_dwordx4 v2, s[20:21]
	s_mov_b32 m0, s19
	v_readfirstlane_b32 s19, v5
	v_add_u32_e32 v4, 0x1c000, v4
	global_load_lds_dwordx4 v1, s[22:23]
	s_mov_b32 m0, s19
	v_readfirstlane_b32 s19, v4
	global_load_lds_dwordx4 v2, s[22:23]
	s_mov_b32 m0, s19
	v_and_b32_e32 v8, 15, v0
	global_load_lds_dwordx4 v3, s[22:23]
	v_lshrrev_b32_e32 v11, 2, v0
	v_bfe_u32 v9, v0, 6, 2
	v_bfe_u32 v5, v0, 1, 3
	v_and_or_b32 v4, v11, 64, v8
	v_lshlrev_b32_e32 v123, 7, v4
	v_bitop3_b32 v4, v6, v5, 3 bitop3:0x6c
	v_mul_u32_u24_e32 v10, 48, v9
	v_lshlrev_b32_e32 v6, 4, v4
	v_or_b32_e32 v4, v10, v8
	v_lshlrev_b32_e32 v7, 7, v4
	v_add_u32_e32 v13, 0, v7
	s_waitcnt vmcnt(10)
	s_barrier
	v_add_u32_e32 v4, v13, v6
	ds_read_b128 v[14:17], v4 offset:16384
	v_add_u32_e32 v50, 0, v123
	v_add_u32_e32 v6, v50, v6
	ds_read_b128 v[18:21], v6
	ds_read_b128 v[22:25], v4 offset:18432
	ds_read_b128 v[26:29], v6 offset:2048
	ds_read_b128 v[30:33], v4 offset:20480
	ds_read_b128 v[42:45], v6 offset:4096
	ds_read_b128 v[46:49], v6 offset:6144
	v_bfe_u32 v12, v0, 4, 2
	v_bitop3_b32 v0, v12, v5, 4 bitop3:0x36
	v_lshlrev_b32_e32 v5, 4, v0
	s_add_i32 s19, 0, 0x14000
	v_add_u32_e32 v124, s19, v5
	s_waitcnt lgkmcnt(0)
	v_mfma_f32_16x16x32_f16 v[34:37], v[14:17], v[18:21], 0
	v_add_u32_e32 v7, v7, v124
	v_mfma_f32_16x16x32_f16 v[38:41], v[22:25], v[18:21], 0
	v_mfma_f32_16x16x32_f16 v[18:21], v[30:33], v[18:21], 0
	v_add_u32_e32 v0, v50, v5
	ds_read_b128 v[50:53], v0
	ds_read_b128 v[54:57], v0 offset:2048
	ds_read_b128 v[58:61], v0 offset:4096
	ds_read_b128 v[62:65], v0 offset:6144
	v_add_u32_e32 v5, v13, v5
	ds_read_b128 v[66:69], v5 offset:16384
	ds_read_b128 v[70:73], v5 offset:18432
	ds_read_b128 v[74:77], v5 offset:20480
	v_mfma_f32_16x16x32_f16 v[78:81], v[14:17], v[26:29], 0
	v_mfma_f32_16x16x32_f16 v[82:85], v[22:25], v[26:29], 0
	v_mfma_f32_16x16x32_f16 v[26:29], v[30:33], v[26:29], 0
	v_mfma_f32_16x16x32_f16 v[86:89], v[14:17], v[42:45], 0
	v_mfma_f32_16x16x32_f16 v[90:93], v[22:25], v[42:45], 0
	v_mfma_f32_16x16x32_f16 v[42:45], v[30:33], v[42:45], 0
	v_mfma_f32_16x16x32_f16 v[14:17], v[14:17], v[46:49], 0
	v_mfma_f32_16x16x32_f16 v[22:25], v[22:25], v[46:49], 0
	v_mfma_f32_16x16x32_f16 v[30:33], v[30:33], v[46:49], 0
	s_add_u32 s20, s0, 0x180
	s_mov_b32 m0, s13
	s_waitcnt vmcnt(5) lgkmcnt(0)
	s_barrier
	s_addc_u32 s21, s1, 0
	s_add_u32 s22, s2, 0x180
	global_load_lds_dwordx4 v1, s[20:21]
	s_mov_b32 m0, s4
	s_addc_u32 s23, s3, 0
	global_load_lds_dwordx4 v2, s[20:21]
	s_mov_b32 m0, s5
	s_nop 0
	global_load_lds_dwordx4 v1, s[22:23]
	s_mov_b32 m0, s6
	s_nop 0
	global_load_lds_dwordx4 v2, s[22:23]
	s_mov_b32 m0, s7
	s_nop 0
	global_load_lds_dwordx4 v3, s[22:23]
	s_waitcnt lgkmcnt(0)
	v_mfma_f32_16x16x32_f16 v[34:37], v[66:69], v[50:53], v[34:37]
	v_mfma_f32_16x16x32_f16 v[38:41], v[70:73], v[50:53], v[38:41]
	v_mfma_f32_16x16x32_f16 v[18:21], v[74:77], v[50:53], v[18:21]
	ds_read_b128 v[46:49], v6 offset:40960
	ds_read_b128 v[50:53], v6 offset:43008
	ds_read_b128 v[94:97], v6 offset:45056
	ds_read_b128 v[98:101], v6 offset:47104
	ds_read_b128 v[102:105], v4 offset:57344
	ds_read_b128 v[106:109], v4 offset:59392
	ds_read_b128 v[110:113], v4 offset:61440
	v_mfma_f32_16x16x32_f16 v[78:81], v[66:69], v[54:57], v[78:81]
	v_mfma_f32_16x16x32_f16 v[82:85], v[70:73], v[54:57], v[82:85]
	v_mfma_f32_16x16x32_f16 v[26:29], v[74:77], v[54:57], v[26:29]
	v_mfma_f32_16x16x32_f16 v[54:57], v[66:69], v[58:61], v[86:89]
	v_mfma_f32_16x16x32_f16 v[86:89], v[70:73], v[58:61], v[90:93]
	v_mfma_f32_16x16x32_f16 v[42:45], v[74:77], v[58:61], v[42:45]
	v_mfma_f32_16x16x32_f16 v[14:17], v[66:69], v[62:65], v[14:17]
	v_mfma_f32_16x16x32_f16 v[22:25], v[70:73], v[62:65], v[22:25]
	v_mfma_f32_16x16x32_f16 v[30:33], v[74:77], v[62:65], v[30:33]
	s_waitcnt lgkmcnt(0)
	v_mfma_f32_16x16x32_f16 v[34:37], v[102:105], v[46:49], v[34:37]
	v_mfma_f32_16x16x32_f16 v[38:41], v[106:109], v[46:49], v[38:41]
	v_mfma_f32_16x16x32_f16 v[18:21], v[110:113], v[46:49], v[18:21]
	ds_read_b128 v[46:49], v0 offset:40960
	ds_read_b128 v[58:61], v0 offset:43008
	ds_read_b128 v[62:65], v0 offset:45056
	ds_read_b128 v[66:69], v0 offset:47104
	ds_read_b128 v[70:73], v5 offset:57344
	ds_read_b128 v[74:77], v5 offset:59392
	ds_read_b128 v[90:93], v5 offset:61440
	v_mfma_f32_16x16x32_f16 v[78:81], v[102:105], v[50:53], v[78:81]
	v_mfma_f32_16x16x32_f16 v[82:85], v[106:109], v[50:53], v[82:85]
	v_mfma_f32_16x16x32_f16 v[26:29], v[110:113], v[50:53], v[26:29]
	v_mfma_f32_16x16x32_f16 v[50:53], v[102:105], v[94:97], v[54:57]
	v_mfma_f32_16x16x32_f16 v[54:57], v[106:109], v[94:97], v[86:89]
	v_mfma_f32_16x16x32_f16 v[42:45], v[110:113], v[94:97], v[42:45]
	v_mfma_f32_16x16x32_f16 v[86:89], v[102:105], v[98:101], v[14:17]
	v_mfma_f32_16x16x32_f16 v[22:25], v[106:109], v[98:101], v[22:25]
	v_mfma_f32_16x16x32_f16 v[30:33], v[110:113], v[98:101], v[30:33]
	s_add_u32 s20, s0, 0x200
	s_mov_b32 m0, s18
	s_waitcnt vmcnt(5) lgkmcnt(0)
	s_barrier
	s_addc_u32 s21, s1, 0
	s_add_u32 s22, s2, 0x200
	global_load_lds_dwordx4 v1, s[20:21]
	s_mov_b32 m0, s14
	s_addc_u32 s23, s3, 0
	global_load_lds_dwordx4 v2, s[20:21]
	s_mov_b32 m0, s15
	s_nop 0
	global_load_lds_dwordx4 v1, s[22:23]
	s_mov_b32 m0, s16
	s_nop 0
	global_load_lds_dwordx4 v2, s[22:23]
	s_mov_b32 m0, s17
	s_nop 0
	global_load_lds_dwordx4 v3, s[22:23]
	s_waitcnt lgkmcnt(0)
	v_mfma_f32_16x16x32_f16 v[34:37], v[70:73], v[46:49], v[34:37]
	v_mfma_f32_16x16x32_f16 v[38:41], v[74:77], v[46:49], v[38:41]
	v_mfma_f32_16x16x32_f16 v[46:49], v[90:93], v[46:49], v[18:21]
	v_add_u32_e32 v13, 0x14000, v6
	v_add_u32_e32 v15, 0x15000, v6
	s_nop 0
	v_add_u32_e32 v18, 0x18000, v4
	v_add_u32_e32 v14, 0x14800, v6
	ds_read_b128 v[94:97], v13
	ds_read_b128 v[98:101], v14
	v_add_u32_e32 v16, 0x15800, v6
	ds_read_b128 v[102:105], v15
	ds_read_b128 v[106:109], v16
	v_add_u32_e32 v19, 0x18800, v4
	ds_read_b128 v[110:113], v18
	ds_read_b128 v[114:117], v19
	v_add_u32_e32 v20, 0x19000, v4
	ds_read_b128 v[118:121], v20
	v_mfma_f32_16x16x32_f16 v[78:81], v[70:73], v[58:61], v[78:81]
	v_mfma_f32_16x16x32_f16 v[82:85], v[74:77], v[58:61], v[82:85]
	v_mfma_f32_16x16x32_f16 v[26:29], v[90:93], v[58:61], v[26:29]
	v_mfma_f32_16x16x32_f16 v[50:53], v[70:73], v[62:65], v[50:53]
	v_mfma_f32_16x16x32_f16 v[54:57], v[74:77], v[62:65], v[54:57]
	v_mfma_f32_16x16x32_f16 v[42:45], v[90:93], v[62:65], v[42:45]
	v_mfma_f32_16x16x32_f16 v[58:61], v[70:73], v[66:69], v[86:89]
	v_mfma_f32_16x16x32_f16 v[22:25], v[74:77], v[66:69], v[22:25]
	v_mfma_f32_16x16x32_f16 v[30:33], v[90:93], v[66:69], v[30:33]
	s_waitcnt lgkmcnt(0)
	v_mfma_f32_16x16x32_f16 v[34:37], v[110:113], v[94:97], v[34:37]
	v_mfma_f32_16x16x32_f16 v[38:41], v[114:117], v[94:97], v[38:41]
	v_mfma_f32_16x16x32_f16 v[46:49], v[118:121], v[94:97], v[46:49]
	v_add_u32_e32 v17, v124, v123
	ds_read_b128 v[62:65], v17 offset:2048
	ds_read_b128 v[66:69], v17 offset:4096
	ds_read_b128 v[70:73], v17 offset:6144
	ds_read_b128 v[74:77], v7 offset:16384
	ds_read_b128 v[86:89], v7 offset:18432
	ds_read_b128 v[90:93], v17
	ds_read_b128 v[94:97], v7 offset:20480
	v_mfma_f32_16x16x32_f16 v[78:81], v[110:113], v[98:101], v[78:81]
	v_mfma_f32_16x16x32_f16 v[82:85], v[114:117], v[98:101], v[82:85]
	v_mfma_f32_16x16x32_f16 v[26:29], v[118:121], v[98:101], v[26:29]
	v_mfma_f32_16x16x32_f16 v[50:53], v[110:113], v[102:105], v[50:53]
	v_mfma_f32_16x16x32_f16 v[54:57], v[114:117], v[102:105], v[54:57]
	v_mfma_f32_16x16x32_f16 v[42:45], v[118:121], v[102:105], v[42:45]
	v_mfma_f32_16x16x32_f16 v[58:61], v[110:113], v[106:109], v[58:61]
	v_mfma_f32_16x16x32_f16 v[22:25], v[114:117], v[106:109], v[22:25]
	v_mfma_f32_16x16x32_f16 v[30:33], v[118:121], v[106:109], v[30:33]
	v_add_u32_e32 v21, s19, v122
	s_add_u32 s20, s0, 0x280
	v_readfirstlane_b32 s23, v21
	v_add_u32_e32 v98, 0x2000, v21
	s_waitcnt vmcnt(5) lgkmcnt(0)
	s_barrier
	s_addc_u32 s21, s1, 0
	s_mov_b32 m0, s23
	v_readfirstlane_b32 s19, v98
	global_load_lds_dwordx4 v1, s[20:21]
	s_mov_b32 m0, s19
	v_add_u32_e32 v98, 0x4000, v21
	s_add_u32 s24, s2, 0x280
	global_load_lds_dwordx4 v2, s[20:21]
	v_readfirstlane_b32 s20, v98
	v_add_u32_e32 v98, 0x6000, v21
	s_addc_u32 s25, s3, 0
	s_mov_b32 m0, s20
	v_readfirstlane_b32 s21, v98
	v_add_u32_e32 v21, 0x8000, v21
	global_load_lds_dwordx4 v1, s[24:25]
	s_mov_b32 m0, s21
	v_readfirstlane_b32 s22, v21
	global_load_lds_dwordx4 v2, s[24:25]
	s_mov_b32 m0, s22
	s_nop 0
	global_load_lds_dwordx4 v3, s[24:25]
	s_waitcnt lgkmcnt(0)
	v_mfma_f32_16x16x32_f16 v[34:37], v[74:77], v[90:93], v[34:37]
	v_mfma_f32_16x16x32_f16 v[38:41], v[86:89], v[90:93], v[38:41]
	v_mfma_f32_16x16x32_f16 v[46:49], v[94:97], v[90:93], v[46:49]
	ds_read_b128 v[90:93], v6
	ds_read_b128 v[98:101], v6 offset:2048
	ds_read_b128 v[102:105], v6 offset:4096
	ds_read_b128 v[106:109], v6 offset:6144
	ds_read_b128 v[110:113], v4 offset:16384
	ds_read_b128 v[114:117], v4 offset:18432
	ds_read_b128 v[118:121], v4 offset:20480
	v_mfma_f32_16x16x32_f16 v[78:81], v[74:77], v[62:65], v[78:81]
	v_mfma_f32_16x16x32_f16 v[82:85], v[86:89], v[62:65], v[82:85]
	v_mfma_f32_16x16x32_f16 v[26:29], v[94:97], v[62:65], v[26:29]
	v_mfma_f32_16x16x32_f16 v[50:53], v[74:77], v[66:69], v[50:53]
	v_mfma_f32_16x16x32_f16 v[54:57], v[86:89], v[66:69], v[54:57]
	v_mfma_f32_16x16x32_f16 v[42:45], v[94:97], v[66:69], v[42:45]
	v_mfma_f32_16x16x32_f16 v[58:61], v[74:77], v[70:73], v[58:61]
	v_mfma_f32_16x16x32_f16 v[22:25], v[86:89], v[70:73], v[22:25]
	v_mfma_f32_16x16x32_f16 v[30:33], v[94:97], v[70:73], v[30:33]
	s_waitcnt lgkmcnt(0)
	v_mfma_f32_16x16x32_f16 v[34:37], v[110:113], v[90:93], v[34:37]
	v_mfma_f32_16x16x32_f16 v[38:41], v[114:117], v[90:93], v[38:41]
	v_mfma_f32_16x16x32_f16 v[46:49], v[118:121], v[90:93], v[46:49]
	ds_read_b128 v[62:65], v0
	ds_read_b128 v[66:69], v0 offset:2048
	ds_read_b128 v[70:73], v0 offset:4096
	ds_read_b128 v[74:77], v0 offset:6144
	ds_read_b128 v[86:89], v5 offset:16384
	ds_read_b128 v[90:93], v5 offset:18432
	ds_read_b128 v[94:97], v5 offset:20480
	v_mfma_f32_16x16x32_f16 v[78:81], v[110:113], v[98:101], v[78:81]
	v_mfma_f32_16x16x32_f16 v[82:85], v[114:117], v[98:101], v[82:85]
	v_mfma_f32_16x16x32_f16 v[26:29], v[118:121], v[98:101], v[26:29]
	v_mfma_f32_16x16x32_f16 v[50:53], v[110:113], v[102:105], v[50:53]
	v_mfma_f32_16x16x32_f16 v[54:57], v[114:117], v[102:105], v[54:57]
	v_mfma_f32_16x16x32_f16 v[42:45], v[118:121], v[102:105], v[42:45]
	v_mfma_f32_16x16x32_f16 v[58:61], v[110:113], v[106:109], v[58:61]
	v_mfma_f32_16x16x32_f16 v[22:25], v[114:117], v[106:109], v[22:25]
	v_mfma_f32_16x16x32_f16 v[30:33], v[118:121], v[106:109], v[30:33]
	s_add_u32 s24, s0, 0x300
	s_mov_b32 m0, s13
	s_waitcnt vmcnt(5) lgkmcnt(0)
	s_barrier
	s_addc_u32 s25, s1, 0
	s_add_u32 s26, s2, 0x300
	global_load_lds_dwordx4 v1, s[24:25]
	s_mov_b32 m0, s4
	s_addc_u32 s27, s3, 0
	global_load_lds_dwordx4 v2, s[24:25]
	s_mov_b32 m0, s5
	s_nop 0
	global_load_lds_dwordx4 v1, s[26:27]
	s_mov_b32 m0, s6
	s_nop 0
	global_load_lds_dwordx4 v2, s[26:27]
	s_mov_b32 m0, s7
	s_nop 0
	global_load_lds_dwordx4 v3, s[26:27]
	s_waitcnt lgkmcnt(0)
	v_mfma_f32_16x16x32_f16 v[34:37], v[86:89], v[62:65], v[34:37]
	v_mfma_f32_16x16x32_f16 v[38:41], v[90:93], v[62:65], v[38:41]
	v_mfma_f32_16x16x32_f16 v[46:49], v[94:97], v[62:65], v[46:49]
	ds_read_b128 v[62:65], v6 offset:40960
	ds_read_b128 v[98:101], v6 offset:43008
	ds_read_b128 v[102:105], v6 offset:45056
	ds_read_b128 v[106:109], v6 offset:47104
	ds_read_b128 v[110:113], v4 offset:57344
	ds_read_b128 v[114:117], v4 offset:59392
	ds_read_b128 v[118:121], v4 offset:61440
	v_mfma_f32_16x16x32_f16 v[78:81], v[86:89], v[66:69], v[78:81]
	v_mfma_f32_16x16x32_f16 v[82:85], v[90:93], v[66:69], v[82:85]
	v_mfma_f32_16x16x32_f16 v[26:29], v[94:97], v[66:69], v[26:29]
	v_mfma_f32_16x16x32_f16 v[50:53], v[86:89], v[70:73], v[50:53]
	v_mfma_f32_16x16x32_f16 v[54:57], v[90:93], v[70:73], v[54:57]
	v_mfma_f32_16x16x32_f16 v[42:45], v[94:97], v[70:73], v[42:45]
	v_mfma_f32_16x16x32_f16 v[58:61], v[86:89], v[74:77], v[58:61]
	v_mfma_f32_16x16x32_f16 v[22:25], v[90:93], v[74:77], v[22:25]
	v_mfma_f32_16x16x32_f16 v[30:33], v[94:97], v[74:77], v[30:33]
	s_waitcnt lgkmcnt(0)
	v_mfma_f32_16x16x32_f16 v[34:37], v[110:113], v[62:65], v[34:37]
	v_mfma_f32_16x16x32_f16 v[38:41], v[114:117], v[62:65], v[38:41]
	v_mfma_f32_16x16x32_f16 v[46:49], v[118:121], v[62:65], v[46:49]
	ds_read_b128 v[62:65], v0 offset:40960
	ds_read_b128 v[66:69], v0 offset:43008
	ds_read_b128 v[70:73], v0 offset:45056
	ds_read_b128 v[74:77], v0 offset:47104
	ds_read_b128 v[86:89], v5 offset:57344
	ds_read_b128 v[90:93], v5 offset:59392
	ds_read_b128 v[94:97], v5 offset:61440
	v_mfma_f32_16x16x32_f16 v[78:81], v[110:113], v[98:101], v[78:81]
	v_mfma_f32_16x16x32_f16 v[82:85], v[114:117], v[98:101], v[82:85]
	v_mfma_f32_16x16x32_f16 v[26:29], v[118:121], v[98:101], v[26:29]
	v_mfma_f32_16x16x32_f16 v[50:53], v[110:113], v[102:105], v[50:53]
	v_mfma_f32_16x16x32_f16 v[54:57], v[114:117], v[102:105], v[54:57]
	v_mfma_f32_16x16x32_f16 v[42:45], v[118:121], v[102:105], v[42:45]
	v_mfma_f32_16x16x32_f16 v[58:61], v[110:113], v[106:109], v[58:61]
	v_mfma_f32_16x16x32_f16 v[22:25], v[114:117], v[106:109], v[22:25]
	v_mfma_f32_16x16x32_f16 v[30:33], v[118:121], v[106:109], v[30:33]
	s_add_u32 s24, s0, 0x380
	s_mov_b32 m0, s18
	s_waitcnt vmcnt(5) lgkmcnt(0)
	s_barrier
	s_addc_u32 s25, s1, 0
	s_add_u32 s26, s2, 0x380
	global_load_lds_dwordx4 v1, s[24:25]
	s_mov_b32 m0, s14
	s_addc_u32 s27, s3, 0
	global_load_lds_dwordx4 v2, s[24:25]
	s_mov_b32 m0, s15
	s_nop 0
	global_load_lds_dwordx4 v1, s[26:27]
	s_mov_b32 m0, s16
	s_nop 0
	global_load_lds_dwordx4 v2, s[26:27]
	s_mov_b32 m0, s17
	s_nop 0
	global_load_lds_dwordx4 v3, s[26:27]
	s_waitcnt lgkmcnt(0)
	v_mfma_f32_16x16x32_f16 v[34:37], v[86:89], v[62:65], v[34:37]
	v_mfma_f32_16x16x32_f16 v[38:41], v[90:93], v[62:65], v[38:41]
	v_mfma_f32_16x16x32_f16 v[46:49], v[94:97], v[62:65], v[46:49]
	ds_read_b128 v[62:65], v13
	ds_read_b128 v[98:101], v14
	ds_read_b128 v[102:105], v15
	ds_read_b128 v[106:109], v16
	ds_read_b128 v[110:113], v18
	ds_read_b128 v[114:117], v19
	ds_read_b128 v[118:121], v20
	v_mfma_f32_16x16x32_f16 v[78:81], v[86:89], v[66:69], v[78:81]
	v_mfma_f32_16x16x32_f16 v[82:85], v[90:93], v[66:69], v[82:85]
	v_mfma_f32_16x16x32_f16 v[26:29], v[94:97], v[66:69], v[26:29]
	v_mfma_f32_16x16x32_f16 v[50:53], v[86:89], v[70:73], v[50:53]
	v_mfma_f32_16x16x32_f16 v[54:57], v[90:93], v[70:73], v[54:57]
	v_mfma_f32_16x16x32_f16 v[42:45], v[94:97], v[70:73], v[42:45]
	v_mfma_f32_16x16x32_f16 v[58:61], v[86:89], v[74:77], v[58:61]
	v_mfma_f32_16x16x32_f16 v[22:25], v[90:93], v[74:77], v[22:25]
	v_mfma_f32_16x16x32_f16 v[30:33], v[94:97], v[74:77], v[30:33]
	s_waitcnt lgkmcnt(0)
	v_mfma_f32_16x16x32_f16 v[34:37], v[110:113], v[62:65], v[34:37]
	v_mfma_f32_16x16x32_f16 v[38:41], v[114:117], v[62:65], v[38:41]
	v_mfma_f32_16x16x32_f16 v[46:49], v[118:121], v[62:65], v[46:49]
	ds_read_b128 v[62:65], v17 offset:2048
	ds_read_b128 v[66:69], v17 offset:4096
	ds_read_b128 v[70:73], v17 offset:6144
	ds_read_b128 v[74:77], v7 offset:16384
	ds_read_b128 v[86:89], v7 offset:18432
	ds_read_b128 v[90:93], v17
	ds_read_b128 v[94:97], v7 offset:20480
	v_mfma_f32_16x16x32_f16 v[78:81], v[110:113], v[98:101], v[78:81]
	v_mfma_f32_16x16x32_f16 v[82:85], v[114:117], v[98:101], v[82:85]
	v_mfma_f32_16x16x32_f16 v[26:29], v[118:121], v[98:101], v[26:29]
	v_mfma_f32_16x16x32_f16 v[50:53], v[110:113], v[102:105], v[50:53]
	v_mfma_f32_16x16x32_f16 v[54:57], v[114:117], v[102:105], v[54:57]
	v_mfma_f32_16x16x32_f16 v[42:45], v[118:121], v[102:105], v[42:45]
	v_mfma_f32_16x16x32_f16 v[58:61], v[110:113], v[106:109], v[58:61]
	v_mfma_f32_16x16x32_f16 v[22:25], v[114:117], v[106:109], v[22:25]
	v_mfma_f32_16x16x32_f16 v[30:33], v[118:121], v[106:109], v[30:33]
	s_add_u32 s24, s0, 0x400
	s_mov_b32 m0, s23
	s_waitcnt vmcnt(5) lgkmcnt(0)
	s_barrier
	s_addc_u32 s25, s1, 0
	s_add_u32 s26, s2, 0x400
	global_load_lds_dwordx4 v1, s[24:25]
	s_mov_b32 m0, s19
	s_addc_u32 s27, s3, 0
	global_load_lds_dwordx4 v2, s[24:25]
	s_mov_b32 m0, s20
	s_nop 0
	global_load_lds_dwordx4 v1, s[26:27]
	s_mov_b32 m0, s21
	s_nop 0
	global_load_lds_dwordx4 v2, s[26:27]
	s_mov_b32 m0, s22
	s_nop 0
	global_load_lds_dwordx4 v3, s[26:27]
	s_waitcnt lgkmcnt(0)
	v_mfma_f32_16x16x32_f16 v[34:37], v[74:77], v[90:93], v[34:37]
	v_mfma_f32_16x16x32_f16 v[38:41], v[86:89], v[90:93], v[38:41]
	v_mfma_f32_16x16x32_f16 v[46:49], v[94:97], v[90:93], v[46:49]
	ds_read_b128 v[90:93], v6
	ds_read_b128 v[98:101], v6 offset:2048
	ds_read_b128 v[102:105], v6 offset:4096
	ds_read_b128 v[106:109], v6 offset:6144
	ds_read_b128 v[110:113], v4 offset:16384
	ds_read_b128 v[114:117], v4 offset:18432
	ds_read_b128 v[118:121], v4 offset:20480
	v_mfma_f32_16x16x32_f16 v[78:81], v[74:77], v[62:65], v[78:81]
	v_mfma_f32_16x16x32_f16 v[82:85], v[86:89], v[62:65], v[82:85]
	v_mfma_f32_16x16x32_f16 v[26:29], v[94:97], v[62:65], v[26:29]
	v_mfma_f32_16x16x32_f16 v[50:53], v[74:77], v[66:69], v[50:53]
	v_mfma_f32_16x16x32_f16 v[54:57], v[86:89], v[66:69], v[54:57]
	v_mfma_f32_16x16x32_f16 v[42:45], v[94:97], v[66:69], v[42:45]
	v_mfma_f32_16x16x32_f16 v[58:61], v[74:77], v[70:73], v[58:61]
	v_mfma_f32_16x16x32_f16 v[22:25], v[86:89], v[70:73], v[22:25]
	v_mfma_f32_16x16x32_f16 v[30:33], v[94:97], v[70:73], v[30:33]
	s_waitcnt lgkmcnt(0)
	v_mfma_f32_16x16x32_f16 v[34:37], v[110:113], v[90:93], v[34:37]
	v_mfma_f32_16x16x32_f16 v[38:41], v[114:117], v[90:93], v[38:41]
	v_mfma_f32_16x16x32_f16 v[46:49], v[118:121], v[90:93], v[46:49]
	ds_read_b128 v[62:65], v0
	ds_read_b128 v[66:69], v0 offset:2048
	ds_read_b128 v[70:73], v0 offset:4096
	ds_read_b128 v[74:77], v0 offset:6144
	ds_read_b128 v[86:89], v5 offset:16384
	ds_read_b128 v[90:93], v5 offset:18432
	ds_read_b128 v[94:97], v5 offset:20480
	v_mfma_f32_16x16x32_f16 v[78:81], v[110:113], v[98:101], v[78:81]
	v_mfma_f32_16x16x32_f16 v[82:85], v[114:117], v[98:101], v[82:85]
	v_mfma_f32_16x16x32_f16 v[26:29], v[118:121], v[98:101], v[26:29]
	v_mfma_f32_16x16x32_f16 v[50:53], v[110:113], v[102:105], v[50:53]
	v_mfma_f32_16x16x32_f16 v[54:57], v[114:117], v[102:105], v[54:57]
	v_mfma_f32_16x16x32_f16 v[42:45], v[118:121], v[102:105], v[42:45]
	v_mfma_f32_16x16x32_f16 v[58:61], v[110:113], v[106:109], v[58:61]
	v_mfma_f32_16x16x32_f16 v[22:25], v[114:117], v[106:109], v[22:25]
	v_mfma_f32_16x16x32_f16 v[30:33], v[118:121], v[106:109], v[30:33]
	s_add_u32 s24, s0, 0x480
	s_mov_b32 m0, s13
	s_waitcnt vmcnt(5) lgkmcnt(0)
	s_barrier
	s_addc_u32 s25, s1, 0
	s_add_u32 s26, s2, 0x480
	global_load_lds_dwordx4 v1, s[24:25]
	s_mov_b32 m0, s4
	s_addc_u32 s27, s3, 0
	global_load_lds_dwordx4 v2, s[24:25]
	s_mov_b32 m0, s5
	s_nop 0
	global_load_lds_dwordx4 v1, s[26:27]
	s_mov_b32 m0, s6
	s_nop 0
	global_load_lds_dwordx4 v2, s[26:27]
	s_mov_b32 m0, s7
	s_nop 0
	global_load_lds_dwordx4 v3, s[26:27]
	s_waitcnt lgkmcnt(0)
	v_mfma_f32_16x16x32_f16 v[34:37], v[86:89], v[62:65], v[34:37]
	v_mfma_f32_16x16x32_f16 v[38:41], v[90:93], v[62:65], v[38:41]
	v_mfma_f32_16x16x32_f16 v[46:49], v[94:97], v[62:65], v[46:49]
	ds_read_b128 v[62:65], v6 offset:40960
	ds_read_b128 v[98:101], v6 offset:43008
	ds_read_b128 v[102:105], v6 offset:45056
	ds_read_b128 v[106:109], v6 offset:47104
	ds_read_b128 v[110:113], v4 offset:57344
	ds_read_b128 v[114:117], v4 offset:59392
	ds_read_b128 v[118:121], v4 offset:61440
	v_mfma_f32_16x16x32_f16 v[78:81], v[86:89], v[66:69], v[78:81]
	v_mfma_f32_16x16x32_f16 v[82:85], v[90:93], v[66:69], v[82:85]
	v_mfma_f32_16x16x32_f16 v[26:29], v[94:97], v[66:69], v[26:29]
	v_mfma_f32_16x16x32_f16 v[50:53], v[86:89], v[70:73], v[50:53]
	v_mfma_f32_16x16x32_f16 v[54:57], v[90:93], v[70:73], v[54:57]
	v_mfma_f32_16x16x32_f16 v[42:45], v[94:97], v[70:73], v[42:45]
	v_mfma_f32_16x16x32_f16 v[58:61], v[86:89], v[74:77], v[58:61]
	v_mfma_f32_16x16x32_f16 v[22:25], v[90:93], v[74:77], v[22:25]
	v_mfma_f32_16x16x32_f16 v[30:33], v[94:97], v[74:77], v[30:33]
	s_waitcnt lgkmcnt(0)
	v_mfma_f32_16x16x32_f16 v[34:37], v[110:113], v[62:65], v[34:37]
	v_mfma_f32_16x16x32_f16 v[38:41], v[114:117], v[62:65], v[38:41]
	v_mfma_f32_16x16x32_f16 v[46:49], v[118:121], v[62:65], v[46:49]
	ds_read_b128 v[62:65], v0 offset:40960
	ds_read_b128 v[66:69], v0 offset:43008
	ds_read_b128 v[70:73], v0 offset:45056
	ds_read_b128 v[74:77], v0 offset:47104
	ds_read_b128 v[86:89], v5 offset:57344
	ds_read_b128 v[90:93], v5 offset:59392
	ds_read_b128 v[94:97], v5 offset:61440
	v_mfma_f32_16x16x32_f16 v[78:81], v[110:113], v[98:101], v[78:81]
	v_mfma_f32_16x16x32_f16 v[82:85], v[114:117], v[98:101], v[82:85]
	v_mfma_f32_16x16x32_f16 v[26:29], v[118:121], v[98:101], v[26:29]
	v_mfma_f32_16x16x32_f16 v[50:53], v[110:113], v[102:105], v[50:53]
	v_mfma_f32_16x16x32_f16 v[54:57], v[114:117], v[102:105], v[54:57]
	v_mfma_f32_16x16x32_f16 v[42:45], v[118:121], v[102:105], v[42:45]
	v_mfma_f32_16x16x32_f16 v[58:61], v[110:113], v[106:109], v[58:61]
	v_mfma_f32_16x16x32_f16 v[22:25], v[114:117], v[106:109], v[22:25]
	v_mfma_f32_16x16x32_f16 v[30:33], v[118:121], v[106:109], v[30:33]
	s_add_u32 s24, s0, 0x500
	s_mov_b32 m0, s18
	s_waitcnt vmcnt(5) lgkmcnt(0)
	s_barrier
	s_addc_u32 s25, s1, 0
	s_add_u32 s26, s2, 0x500
	global_load_lds_dwordx4 v1, s[24:25]
	s_mov_b32 m0, s14
	s_addc_u32 s27, s3, 0
	global_load_lds_dwordx4 v2, s[24:25]
	s_mov_b32 m0, s15
	s_nop 0
	global_load_lds_dwordx4 v1, s[26:27]
	s_mov_b32 m0, s16
	s_nop 0
	global_load_lds_dwordx4 v2, s[26:27]
	s_mov_b32 m0, s17
	s_nop 0
	global_load_lds_dwordx4 v3, s[26:27]
	s_waitcnt lgkmcnt(0)
	v_mfma_f32_16x16x32_f16 v[34:37], v[86:89], v[62:65], v[34:37]
	v_mfma_f32_16x16x32_f16 v[38:41], v[90:93], v[62:65], v[38:41]
	v_mfma_f32_16x16x32_f16 v[46:49], v[94:97], v[62:65], v[46:49]
	ds_read_b128 v[62:65], v13
	ds_read_b128 v[98:101], v14
	ds_read_b128 v[102:105], v15
	ds_read_b128 v[106:109], v16
	ds_read_b128 v[110:113], v18
	ds_read_b128 v[114:117], v19
	ds_read_b128 v[118:121], v20
	v_mfma_f32_16x16x32_f16 v[78:81], v[86:89], v[66:69], v[78:81]
	v_mfma_f32_16x16x32_f16 v[82:85], v[90:93], v[66:69], v[82:85]
	v_mfma_f32_16x16x32_f16 v[26:29], v[94:97], v[66:69], v[26:29]
	v_mfma_f32_16x16x32_f16 v[50:53], v[86:89], v[70:73], v[50:53]
	v_mfma_f32_16x16x32_f16 v[54:57], v[90:93], v[70:73], v[54:57]
	v_mfma_f32_16x16x32_f16 v[42:45], v[94:97], v[70:73], v[42:45]
	v_mfma_f32_16x16x32_f16 v[58:61], v[86:89], v[74:77], v[58:61]
	v_mfma_f32_16x16x32_f16 v[22:25], v[90:93], v[74:77], v[22:25]
	v_mfma_f32_16x16x32_f16 v[30:33], v[94:97], v[74:77], v[30:33]
	s_waitcnt lgkmcnt(0)
	v_mfma_f32_16x16x32_f16 v[34:37], v[110:113], v[62:65], v[34:37]
	v_mfma_f32_16x16x32_f16 v[38:41], v[114:117], v[62:65], v[38:41]
	v_mfma_f32_16x16x32_f16 v[46:49], v[118:121], v[62:65], v[46:49]
	ds_read_b128 v[62:65], v17 offset:2048
	ds_read_b128 v[66:69], v17 offset:4096
	ds_read_b128 v[70:73], v17 offset:6144
	ds_read_b128 v[74:77], v7 offset:16384
	ds_read_b128 v[86:89], v7 offset:18432
	ds_read_b128 v[90:93], v17
	ds_read_b128 v[94:97], v7 offset:20480
	v_mfma_f32_16x16x32_f16 v[78:81], v[110:113], v[98:101], v[78:81]
	v_mfma_f32_16x16x32_f16 v[82:85], v[114:117], v[98:101], v[82:85]
	v_mfma_f32_16x16x32_f16 v[26:29], v[118:121], v[98:101], v[26:29]
	v_mfma_f32_16x16x32_f16 v[50:53], v[110:113], v[102:105], v[50:53]
	v_mfma_f32_16x16x32_f16 v[54:57], v[114:117], v[102:105], v[54:57]
	v_mfma_f32_16x16x32_f16 v[42:45], v[118:121], v[102:105], v[42:45]
	v_mfma_f32_16x16x32_f16 v[58:61], v[110:113], v[106:109], v[58:61]
	v_mfma_f32_16x16x32_f16 v[22:25], v[114:117], v[106:109], v[22:25]
	v_mfma_f32_16x16x32_f16 v[30:33], v[118:121], v[106:109], v[30:33]
	s_add_u32 s24, s0, 0x580
	s_mov_b32 m0, s23
	s_waitcnt vmcnt(5) lgkmcnt(0)
	s_barrier
	s_addc_u32 s25, s1, 0
	s_add_u32 s26, s2, 0x580
	global_load_lds_dwordx4 v1, s[24:25]
	s_mov_b32 m0, s19
	s_addc_u32 s27, s3, 0
	global_load_lds_dwordx4 v2, s[24:25]
	s_mov_b32 m0, s20
	s_nop 0
	global_load_lds_dwordx4 v1, s[26:27]
	s_mov_b32 m0, s21
	s_nop 0
	global_load_lds_dwordx4 v2, s[26:27]
	s_mov_b32 m0, s22
	s_nop 0
	global_load_lds_dwordx4 v3, s[26:27]
	s_waitcnt lgkmcnt(0)
	v_mfma_f32_16x16x32_f16 v[34:37], v[74:77], v[90:93], v[34:37]
	v_mfma_f32_16x16x32_f16 v[38:41], v[86:89], v[90:93], v[38:41]
	v_mfma_f32_16x16x32_f16 v[46:49], v[94:97], v[90:93], v[46:49]
	ds_read_b128 v[90:93], v6
	ds_read_b128 v[98:101], v6 offset:2048
	ds_read_b128 v[102:105], v6 offset:4096
	ds_read_b128 v[106:109], v6 offset:6144
	ds_read_b128 v[110:113], v4 offset:16384
	ds_read_b128 v[114:117], v4 offset:18432
	ds_read_b128 v[118:121], v4 offset:20480
	v_mfma_f32_16x16x32_f16 v[78:81], v[74:77], v[62:65], v[78:81]
	v_mfma_f32_16x16x32_f16 v[82:85], v[86:89], v[62:65], v[82:85]
	v_mfma_f32_16x16x32_f16 v[26:29], v[94:97], v[62:65], v[26:29]
	v_mfma_f32_16x16x32_f16 v[50:53], v[74:77], v[66:69], v[50:53]
	v_mfma_f32_16x16x32_f16 v[54:57], v[86:89], v[66:69], v[54:57]
	v_mfma_f32_16x16x32_f16 v[42:45], v[94:97], v[66:69], v[42:45]
	v_mfma_f32_16x16x32_f16 v[58:61], v[74:77], v[70:73], v[58:61]
	v_mfma_f32_16x16x32_f16 v[22:25], v[86:89], v[70:73], v[22:25]
	v_mfma_f32_16x16x32_f16 v[30:33], v[94:97], v[70:73], v[30:33]
	s_waitcnt lgkmcnt(0)
	v_mfma_f32_16x16x32_f16 v[34:37], v[110:113], v[90:93], v[34:37]
	v_mfma_f32_16x16x32_f16 v[38:41], v[114:117], v[90:93], v[38:41]
	v_mfma_f32_16x16x32_f16 v[46:49], v[118:121], v[90:93], v[46:49]
	ds_read_b128 v[62:65], v0
	ds_read_b128 v[66:69], v0 offset:2048
	ds_read_b128 v[70:73], v0 offset:4096
	ds_read_b128 v[74:77], v0 offset:6144
	ds_read_b128 v[86:89], v5 offset:16384
	ds_read_b128 v[90:93], v5 offset:18432
	ds_read_b128 v[94:97], v5 offset:20480
	v_mfma_f32_16x16x32_f16 v[78:81], v[110:113], v[98:101], v[78:81]
	v_mfma_f32_16x16x32_f16 v[82:85], v[114:117], v[98:101], v[82:85]
	v_mfma_f32_16x16x32_f16 v[26:29], v[118:121], v[98:101], v[26:29]
	v_mfma_f32_16x16x32_f16 v[50:53], v[110:113], v[102:105], v[50:53]
	v_mfma_f32_16x16x32_f16 v[54:57], v[114:117], v[102:105], v[54:57]
	v_mfma_f32_16x16x32_f16 v[42:45], v[118:121], v[102:105], v[42:45]
	v_mfma_f32_16x16x32_f16 v[58:61], v[110:113], v[106:109], v[58:61]
	v_mfma_f32_16x16x32_f16 v[22:25], v[114:117], v[106:109], v[22:25]
	v_mfma_f32_16x16x32_f16 v[30:33], v[118:121], v[106:109], v[30:33]
	s_add_u32 s24, s0, 0x600
	s_mov_b32 m0, s13
	s_waitcnt vmcnt(5) lgkmcnt(0)
	s_barrier
	s_addc_u32 s25, s1, 0
	s_add_u32 s26, s2, 0x600
	global_load_lds_dwordx4 v1, s[24:25]
	s_mov_b32 m0, s4
	s_addc_u32 s27, s3, 0
	global_load_lds_dwordx4 v2, s[24:25]
	s_mov_b32 m0, s5
	s_nop 0
	global_load_lds_dwordx4 v1, s[26:27]
	s_mov_b32 m0, s6
	s_nop 0
	global_load_lds_dwordx4 v2, s[26:27]
	s_mov_b32 m0, s7
	s_nop 0
	global_load_lds_dwordx4 v3, s[26:27]
	s_waitcnt lgkmcnt(0)
	v_mfma_f32_16x16x32_f16 v[34:37], v[86:89], v[62:65], v[34:37]
	v_mfma_f32_16x16x32_f16 v[38:41], v[90:93], v[62:65], v[38:41]
	v_mfma_f32_16x16x32_f16 v[46:49], v[94:97], v[62:65], v[46:49]
	ds_read_b128 v[62:65], v6 offset:40960
	ds_read_b128 v[98:101], v6 offset:43008
	ds_read_b128 v[102:105], v6 offset:45056
	ds_read_b128 v[106:109], v6 offset:47104
	ds_read_b128 v[110:113], v4 offset:57344
	ds_read_b128 v[114:117], v4 offset:59392
	ds_read_b128 v[118:121], v4 offset:61440
	v_mfma_f32_16x16x32_f16 v[78:81], v[86:89], v[66:69], v[78:81]
	v_mfma_f32_16x16x32_f16 v[82:85], v[90:93], v[66:69], v[82:85]
	v_mfma_f32_16x16x32_f16 v[26:29], v[94:97], v[66:69], v[26:29]
	v_mfma_f32_16x16x32_f16 v[50:53], v[86:89], v[70:73], v[50:53]
	v_mfma_f32_16x16x32_f16 v[54:57], v[90:93], v[70:73], v[54:57]
	v_mfma_f32_16x16x32_f16 v[42:45], v[94:97], v[70:73], v[42:45]
	v_mfma_f32_16x16x32_f16 v[58:61], v[86:89], v[74:77], v[58:61]
	v_mfma_f32_16x16x32_f16 v[22:25], v[90:93], v[74:77], v[22:25]
	v_mfma_f32_16x16x32_f16 v[30:33], v[94:97], v[74:77], v[30:33]
	s_waitcnt lgkmcnt(0)
	v_mfma_f32_16x16x32_f16 v[34:37], v[110:113], v[62:65], v[34:37]
	v_mfma_f32_16x16x32_f16 v[38:41], v[114:117], v[62:65], v[38:41]
	v_mfma_f32_16x16x32_f16 v[46:49], v[118:121], v[62:65], v[46:49]
	ds_read_b128 v[62:65], v0 offset:40960
	ds_read_b128 v[66:69], v0 offset:43008
	ds_read_b128 v[70:73], v0 offset:45056
	ds_read_b128 v[74:77], v0 offset:47104
	ds_read_b128 v[86:89], v5 offset:57344
	ds_read_b128 v[90:93], v5 offset:59392
	ds_read_b128 v[94:97], v5 offset:61440
	v_mfma_f32_16x16x32_f16 v[78:81], v[110:113], v[98:101], v[78:81]
	v_mfma_f32_16x16x32_f16 v[82:85], v[114:117], v[98:101], v[82:85]
	v_mfma_f32_16x16x32_f16 v[26:29], v[118:121], v[98:101], v[26:29]
	v_mfma_f32_16x16x32_f16 v[50:53], v[110:113], v[102:105], v[50:53]
	v_mfma_f32_16x16x32_f16 v[54:57], v[114:117], v[102:105], v[54:57]
	v_mfma_f32_16x16x32_f16 v[42:45], v[118:121], v[102:105], v[42:45]
	v_mfma_f32_16x16x32_f16 v[58:61], v[110:113], v[106:109], v[58:61]
	v_mfma_f32_16x16x32_f16 v[22:25], v[114:117], v[106:109], v[22:25]
	v_mfma_f32_16x16x32_f16 v[30:33], v[118:121], v[106:109], v[30:33]
	s_add_u32 s24, s0, 0x680
	s_mov_b32 m0, s18
	s_waitcnt vmcnt(5) lgkmcnt(0)
	s_barrier
	s_addc_u32 s25, s1, 0
	s_add_u32 s26, s2, 0x680
	global_load_lds_dwordx4 v1, s[24:25]
	s_mov_b32 m0, s14
	s_addc_u32 s27, s3, 0
	global_load_lds_dwordx4 v2, s[24:25]
	s_mov_b32 m0, s15
	s_nop 0
	global_load_lds_dwordx4 v1, s[26:27]
	s_mov_b32 m0, s16
	s_nop 0
	global_load_lds_dwordx4 v2, s[26:27]
	s_mov_b32 m0, s17
	s_nop 0
	global_load_lds_dwordx4 v3, s[26:27]
	s_waitcnt lgkmcnt(0)
	v_mfma_f32_16x16x32_f16 v[34:37], v[86:89], v[62:65], v[34:37]
	v_mfma_f32_16x16x32_f16 v[38:41], v[90:93], v[62:65], v[38:41]
	v_mfma_f32_16x16x32_f16 v[46:49], v[94:97], v[62:65], v[46:49]
	ds_read_b128 v[62:65], v13
	ds_read_b128 v[98:101], v14
	ds_read_b128 v[102:105], v15
	ds_read_b128 v[106:109], v16
	ds_read_b128 v[110:113], v18
	ds_read_b128 v[114:117], v19
	ds_read_b128 v[118:121], v20
	v_mfma_f32_16x16x32_f16 v[78:81], v[86:89], v[66:69], v[78:81]
	v_mfma_f32_16x16x32_f16 v[82:85], v[90:93], v[66:69], v[82:85]
	v_mfma_f32_16x16x32_f16 v[26:29], v[94:97], v[66:69], v[26:29]
	v_mfma_f32_16x16x32_f16 v[50:53], v[86:89], v[70:73], v[50:53]
	v_mfma_f32_16x16x32_f16 v[54:57], v[90:93], v[70:73], v[54:57]
	v_mfma_f32_16x16x32_f16 v[42:45], v[94:97], v[70:73], v[42:45]
	v_mfma_f32_16x16x32_f16 v[58:61], v[86:89], v[74:77], v[58:61]
	v_mfma_f32_16x16x32_f16 v[22:25], v[90:93], v[74:77], v[22:25]
	v_mfma_f32_16x16x32_f16 v[30:33], v[94:97], v[74:77], v[30:33]
	s_waitcnt lgkmcnt(0)
	v_mfma_f32_16x16x32_f16 v[34:37], v[110:113], v[62:65], v[34:37]
	v_mfma_f32_16x16x32_f16 v[38:41], v[114:117], v[62:65], v[38:41]
	v_mfma_f32_16x16x32_f16 v[46:49], v[118:121], v[62:65], v[46:49]
	ds_read_b128 v[62:65], v17 offset:2048
	ds_read_b128 v[66:69], v17 offset:4096
	ds_read_b128 v[70:73], v17 offset:6144
	ds_read_b128 v[74:77], v7 offset:16384
	ds_read_b128 v[86:89], v7 offset:18432
	ds_read_b128 v[90:93], v17
	ds_read_b128 v[94:97], v7 offset:20480
	v_mfma_f32_16x16x32_f16 v[78:81], v[110:113], v[98:101], v[78:81]
	v_mfma_f32_16x16x32_f16 v[82:85], v[114:117], v[98:101], v[82:85]
	v_mfma_f32_16x16x32_f16 v[26:29], v[118:121], v[98:101], v[26:29]
	v_mfma_f32_16x16x32_f16 v[50:53], v[110:113], v[102:105], v[50:53]
	v_mfma_f32_16x16x32_f16 v[54:57], v[114:117], v[102:105], v[54:57]
	v_mfma_f32_16x16x32_f16 v[42:45], v[118:121], v[102:105], v[42:45]
	v_mfma_f32_16x16x32_f16 v[58:61], v[110:113], v[106:109], v[58:61]
	v_mfma_f32_16x16x32_f16 v[22:25], v[114:117], v[106:109], v[22:25]
	v_mfma_f32_16x16x32_f16 v[30:33], v[118:121], v[106:109], v[30:33]
	s_add_u32 s14, s0, 0x700
	s_mov_b32 m0, s23
	s_waitcnt vmcnt(5) lgkmcnt(0)
	s_barrier
	s_addc_u32 s15, s1, 0
	s_add_u32 s16, s2, 0x700
	global_load_lds_dwordx4 v1, s[14:15]
	s_mov_b32 m0, s19
	s_addc_u32 s17, s3, 0
	global_load_lds_dwordx4 v2, s[14:15]
	s_mov_b32 m0, s20
	s_nop 0
	global_load_lds_dwordx4 v1, s[16:17]
	s_mov_b32 m0, s21
	s_nop 0
	global_load_lds_dwordx4 v2, s[16:17]
	s_mov_b32 m0, s22
	s_nop 0
	global_load_lds_dwordx4 v3, s[16:17]
	s_waitcnt lgkmcnt(0)
	v_mfma_f32_16x16x32_f16 v[34:37], v[74:77], v[90:93], v[34:37]
	v_mfma_f32_16x16x32_f16 v[38:41], v[86:89], v[90:93], v[38:41]
	v_mfma_f32_16x16x32_f16 v[46:49], v[94:97], v[90:93], v[46:49]
	ds_read_b128 v[90:93], v6
	ds_read_b128 v[98:101], v6 offset:2048
	ds_read_b128 v[102:105], v6 offset:4096
	ds_read_b128 v[106:109], v6 offset:6144
	ds_read_b128 v[110:113], v4 offset:16384
	ds_read_b128 v[114:117], v4 offset:18432
	ds_read_b128 v[118:121], v4 offset:20480
	v_mfma_f32_16x16x32_f16 v[78:81], v[74:77], v[62:65], v[78:81]
	v_mfma_f32_16x16x32_f16 v[82:85], v[86:89], v[62:65], v[82:85]
	v_mfma_f32_16x16x32_f16 v[26:29], v[94:97], v[62:65], v[26:29]
	v_mfma_f32_16x16x32_f16 v[50:53], v[74:77], v[66:69], v[50:53]
	v_mfma_f32_16x16x32_f16 v[54:57], v[86:89], v[66:69], v[54:57]
	v_mfma_f32_16x16x32_f16 v[42:45], v[94:97], v[66:69], v[42:45]
	v_mfma_f32_16x16x32_f16 v[58:61], v[74:77], v[70:73], v[58:61]
	v_mfma_f32_16x16x32_f16 v[22:25], v[86:89], v[70:73], v[22:25]
	v_mfma_f32_16x16x32_f16 v[30:33], v[94:97], v[70:73], v[30:33]
	s_waitcnt lgkmcnt(0)
	v_mfma_f32_16x16x32_f16 v[34:37], v[110:113], v[90:93], v[34:37]
	v_mfma_f32_16x16x32_f16 v[38:41], v[114:117], v[90:93], v[38:41]
	v_mfma_f32_16x16x32_f16 v[46:49], v[118:121], v[90:93], v[46:49]
	ds_read_b128 v[62:65], v0
	ds_read_b128 v[66:69], v0 offset:2048
	ds_read_b128 v[70:73], v0 offset:4096
	ds_read_b128 v[74:77], v0 offset:6144
	ds_read_b128 v[86:89], v5 offset:16384
	ds_read_b128 v[90:93], v5 offset:18432
	ds_read_b128 v[94:97], v5 offset:20480
	v_mfma_f32_16x16x32_f16 v[78:81], v[110:113], v[98:101], v[78:81]
	v_mfma_f32_16x16x32_f16 v[82:85], v[114:117], v[98:101], v[82:85]
	v_mfma_f32_16x16x32_f16 v[26:29], v[118:121], v[98:101], v[26:29]
	v_mfma_f32_16x16x32_f16 v[50:53], v[110:113], v[102:105], v[50:53]
	v_mfma_f32_16x16x32_f16 v[54:57], v[114:117], v[102:105], v[54:57]
	v_mfma_f32_16x16x32_f16 v[42:45], v[118:121], v[102:105], v[42:45]
	v_mfma_f32_16x16x32_f16 v[58:61], v[110:113], v[106:109], v[58:61]
	v_mfma_f32_16x16x32_f16 v[22:25], v[114:117], v[106:109], v[22:25]
	v_mfma_f32_16x16x32_f16 v[30:33], v[118:121], v[106:109], v[30:33]
	s_add_u32 s0, s0, 0x780
	s_mov_b32 m0, s13
	s_waitcnt vmcnt(5) lgkmcnt(0)
	s_barrier
	s_addc_u32 s1, s1, 0
	s_add_u32 s2, s2, 0x780
	global_load_lds_dwordx4 v1, s[0:1]
	s_mov_b32 m0, s4
	s_addc_u32 s3, s3, 0
	global_load_lds_dwordx4 v2, s[0:1]
	s_mov_b32 m0, s5
	s_nop 0
	global_load_lds_dwordx4 v1, s[2:3]
	s_mov_b32 m0, s6
	s_nop 0
	global_load_lds_dwordx4 v2, s[2:3]
	s_mov_b32 m0, s7
	s_nop 0
	global_load_lds_dwordx4 v3, s[2:3]
	s_waitcnt lgkmcnt(0)
	v_mfma_f32_16x16x32_f16 v[34:37], v[86:89], v[62:65], v[34:37]
	v_mfma_f32_16x16x32_f16 v[38:41], v[90:93], v[62:65], v[38:41]
	v_mfma_f32_16x16x32_f16 v[46:49], v[94:97], v[62:65], v[46:49]
	ds_read_b128 v[62:65], v6 offset:40960
	ds_read_b128 v[98:101], v6 offset:43008
	ds_read_b128 v[102:105], v6 offset:45056
	ds_read_b128 v[106:109], v6 offset:47104
	ds_read_b128 v[110:113], v4 offset:57344
	ds_read_b128 v[114:117], v4 offset:59392
	ds_read_b128 v[118:121], v4 offset:61440
	v_mfma_f32_16x16x32_f16 v[78:81], v[86:89], v[66:69], v[78:81]
	v_mfma_f32_16x16x32_f16 v[82:85], v[90:93], v[66:69], v[82:85]
	v_mfma_f32_16x16x32_f16 v[26:29], v[94:97], v[66:69], v[26:29]
	v_mfma_f32_16x16x32_f16 v[50:53], v[86:89], v[70:73], v[50:53]
	v_mfma_f32_16x16x32_f16 v[54:57], v[90:93], v[70:73], v[54:57]
	v_mfma_f32_16x16x32_f16 v[42:45], v[94:97], v[70:73], v[42:45]
	v_mfma_f32_16x16x32_f16 v[58:61], v[86:89], v[74:77], v[58:61]
	v_mfma_f32_16x16x32_f16 v[22:25], v[90:93], v[74:77], v[22:25]
	v_mfma_f32_16x16x32_f16 v[30:33], v[94:97], v[74:77], v[30:33]
	s_waitcnt lgkmcnt(0)
	v_mfma_f32_16x16x32_f16 v[34:37], v[110:113], v[62:65], v[34:37]
	v_mfma_f32_16x16x32_f16 v[38:41], v[114:117], v[62:65], v[38:41]
	v_mfma_f32_16x16x32_f16 v[46:49], v[118:121], v[62:65], v[46:49]
	ds_read_b128 v[62:65], v0 offset:40960
	ds_read_b128 v[66:69], v0 offset:43008
	ds_read_b128 v[70:73], v0 offset:45056
	ds_read_b128 v[74:77], v0 offset:47104
	ds_read_b128 v[86:89], v5 offset:57344
	ds_read_b128 v[90:93], v5 offset:59392
	ds_read_b128 v[94:97], v5 offset:61440
	v_mfma_f32_16x16x32_f16 v[78:81], v[110:113], v[98:101], v[78:81]
	v_mfma_f32_16x16x32_f16 v[82:85], v[114:117], v[98:101], v[82:85]
	v_mfma_f32_16x16x32_f16 v[26:29], v[118:121], v[98:101], v[26:29]
	v_mfma_f32_16x16x32_f16 v[50:53], v[110:113], v[102:105], v[50:53]
	v_mfma_f32_16x16x32_f16 v[54:57], v[114:117], v[102:105], v[54:57]
	v_mfma_f32_16x16x32_f16 v[42:45], v[118:121], v[102:105], v[42:45]
	v_mfma_f32_16x16x32_f16 v[58:61], v[110:113], v[106:109], v[58:61]
	v_mfma_f32_16x16x32_f16 v[22:25], v[114:117], v[106:109], v[22:25]
	v_mfma_f32_16x16x32_f16 v[30:33], v[118:121], v[106:109], v[30:33]
	s_waitcnt vmcnt(5) lgkmcnt(0)
	s_barrier
	s_waitcnt lgkmcnt(0)
	v_mfma_f32_16x16x32_f16 v[34:37], v[86:89], v[62:65], v[34:37]
	v_mfma_f32_16x16x32_f16 v[38:41], v[90:93], v[62:65], v[38:41]
	v_mfma_f32_16x16x32_f16 v[46:49], v[94:97], v[62:65], v[46:49]
	ds_read_b128 v[62:65], v13
	ds_read_b128 v[98:101], v14
	ds_read_b128 v[102:105], v15
	ds_read_b128 v[106:109], v16
	ds_read_b128 v[110:113], v18
	ds_read_b128 v[114:117], v19
	ds_read_b128 v[18:21], v20
	v_mfma_f32_16x16x32_f16 v[78:81], v[86:89], v[66:69], v[78:81]
	v_mfma_f32_16x16x32_f16 v[82:85], v[90:93], v[66:69], v[82:85]
	v_mfma_f32_16x16x32_f16 v[26:29], v[94:97], v[66:69], v[26:29]
	v_mfma_f32_16x16x32_f16 v[50:53], v[86:89], v[70:73], v[50:53]
	v_mfma_f32_16x16x32_f16 v[54:57], v[90:93], v[70:73], v[54:57]
	v_mfma_f32_16x16x32_f16 v[42:45], v[94:97], v[70:73], v[42:45]
	v_mfma_f32_16x16x32_f16 v[58:61], v[86:89], v[74:77], v[58:61]
	v_mfma_f32_16x16x32_f16 v[22:25], v[90:93], v[74:77], v[22:25]
	v_mfma_f32_16x16x32_f16 v[30:33], v[94:97], v[74:77], v[30:33]
	s_waitcnt lgkmcnt(0)
	v_mfma_f32_16x16x32_f16 v[34:37], v[110:113], v[62:65], v[34:37]
	v_mfma_f32_16x16x32_f16 v[38:41], v[114:117], v[62:65], v[38:41]
	v_mfma_f32_16x16x32_f16 v[46:49], v[18:21], v[62:65], v[46:49]
	ds_read_b128 v[62:65], v17 offset:2048
	ds_read_b128 v[66:69], v17 offset:4096
	ds_read_b128 v[70:73], v17 offset:6144
	ds_read_b128 v[74:77], v7 offset:16384
	ds_read_b128 v[86:89], v7 offset:18432
	ds_read_b128 v[14:17], v17
	ds_read_b128 v[90:93], v7 offset:20480
	v_mfma_f32_16x16x32_f16 v[78:81], v[110:113], v[98:101], v[78:81]
	v_mfma_f32_16x16x32_f16 v[82:85], v[114:117], v[98:101], v[82:85]
	v_mfma_f32_16x16x32_f16 v[26:29], v[18:21], v[98:101], v[26:29]
	v_mfma_f32_16x16x32_f16 v[50:53], v[110:113], v[102:105], v[50:53]
	v_mfma_f32_16x16x32_f16 v[54:57], v[114:117], v[102:105], v[54:57]
	v_mfma_f32_16x16x32_f16 v[42:45], v[18:21], v[102:105], v[42:45]
	v_mfma_f32_16x16x32_f16 v[58:61], v[110:113], v[106:109], v[58:61]
	v_mfma_f32_16x16x32_f16 v[22:25], v[114:117], v[106:109], v[22:25]
	v_mfma_f32_16x16x32_f16 v[18:21], v[18:21], v[106:109], v[30:33]
	s_waitcnt vmcnt(0) lgkmcnt(0)
	s_barrier
	s_waitcnt lgkmcnt(0)
	v_mfma_f32_16x16x32_f16 v[30:33], v[74:77], v[14:17], v[34:37]
	v_mfma_f32_16x16x32_f16 v[34:37], v[86:89], v[14:17], v[38:41]
	v_mfma_f32_16x16x32_f16 v[14:17], v[90:93], v[14:17], v[46:49]
	s_nop 1
	ds_read_b128 v[38:41], v6
	ds_read_b128 v[46:49], v6 offset:2048
	ds_read_b128 v[94:97], v6 offset:4096
	ds_read_b128 v[98:101], v6 offset:6144
	ds_read_b128 v[102:105], v4 offset:16384
	ds_read_b128 v[106:109], v4 offset:18432
	ds_read_b128 v[110:113], v4 offset:20480
	v_mfma_f32_16x16x32_f16 v[78:81], v[74:77], v[62:65], v[78:81]
	v_mfma_f32_16x16x32_f16 v[82:85], v[86:89], v[62:65], v[82:85]
	v_mfma_f32_16x16x32_f16 v[26:29], v[90:93], v[62:65], v[26:29]
	v_mfma_f32_16x16x32_f16 v[50:53], v[74:77], v[66:69], v[50:53]
	v_mfma_f32_16x16x32_f16 v[54:57], v[86:89], v[66:69], v[54:57]
	v_mfma_f32_16x16x32_f16 v[42:45], v[90:93], v[66:69], v[42:45]
	v_mfma_f32_16x16x32_f16 v[58:61], v[74:77], v[70:73], v[58:61]
	v_mfma_f32_16x16x32_f16 v[22:25], v[86:89], v[70:73], v[22:25]
	v_mfma_f32_16x16x32_f16 v[18:21], v[90:93], v[70:73], v[18:21]
	s_waitcnt lgkmcnt(0)
	v_mfma_f32_16x16x32_f16 v[30:33], v[102:105], v[38:41], v[30:33]
	v_mfma_f32_16x16x32_f16 v[34:37], v[106:109], v[38:41], v[34:37]
	v_mfma_f32_16x16x32_f16 v[14:17], v[110:113], v[38:41], v[14:17]
	ds_read_b128 v[38:41], v0
	ds_read_b128 v[62:65], v0 offset:2048
	ds_read_b128 v[66:69], v0 offset:4096
	ds_read_b128 v[0:3], v0 offset:6144
	ds_read_b128 v[70:73], v5 offset:16384
	ds_read_b128 v[74:77], v5 offset:18432
	ds_read_b128 v[86:89], v5 offset:20480
	v_mfma_f32_16x16x32_f16 v[4:7], v[102:105], v[46:49], v[78:81]
	v_mfma_f32_16x16x32_f16 v[78:81], v[106:109], v[46:49], v[82:85]
	v_mfma_f32_16x16x32_f16 v[26:29], v[110:113], v[46:49], v[26:29]
	v_mfma_f32_16x16x32_f16 v[46:49], v[102:105], v[94:97], v[50:53]
	v_mfma_f32_16x16x32_f16 v[50:53], v[106:109], v[94:97], v[54:57]
	v_mfma_f32_16x16x32_f16 v[42:45], v[110:113], v[94:97], v[42:45]
	v_mfma_f32_16x16x32_f16 v[54:57], v[102:105], v[98:101], v[58:61]
	v_mfma_f32_16x16x32_f16 v[22:25], v[106:109], v[98:101], v[22:25]
	v_mfma_f32_16x16x32_f16 v[18:21], v[110:113], v[98:101], v[18:21]
	s_waitcnt lgkmcnt(0)
	v_mfma_f32_16x16x32_f16 v[30:33], v[70:73], v[38:41], v[30:33]
	v_mfma_f32_16x16x32_f16 v[34:37], v[74:77], v[38:41], v[34:37]
	v_mfma_f32_16x16x32_f16 v[14:17], v[86:89], v[38:41], v[14:17]
	v_mfma_f32_16x16x32_f16 v[38:41], v[70:73], v[62:65], v[4:7]
	v_mfma_f32_16x16x32_f16 v[58:61], v[74:77], v[62:65], v[78:81]
	v_mfma_f32_16x16x32_f16 v[26:29], v[86:89], v[62:65], v[26:29]
	v_mfma_f32_16x16x32_f16 v[46:49], v[70:73], v[66:69], v[46:49]
	v_mfma_f32_16x16x32_f16 v[50:53], v[74:77], v[66:69], v[50:53]
	v_mfma_f32_16x16x32_f16 v[42:45], v[86:89], v[66:69], v[42:45]
	v_mfma_f32_16x16x32_f16 v[54:57], v[70:73], v[0:3], v[54:57]
	v_mfma_f32_16x16x32_f16 v[4:7], v[74:77], v[0:3], v[22:25]
	v_mfma_f32_16x16x32_f16 v[0:3], v[86:89], v[0:3], v[18:21]
	s_lshl_b32 s0, s12, 1
	v_or_b32_e32 v11, s10, v11
	s_and_b32 s5, s0, 0x3fffff0
	s_movk_i32 s0, 0x3c0
	v_mad_u32_u24 v62, v9, 48, s11
	v_lshlrev_b32_e32 v24, 2, v12
	v_and_or_b32 v63, v11, s0, v8
	s_movk_i32 s0, 0x400
	s_mov_b32 s4, 0x3e38aa3b
	v_and_or_b32 v20, v10, 48, v24
	v_pk_mul_f32 v[10:11], v[32:33], s[4:5] op_sel_hi:[1,0]
	v_cmp_gt_u32_e32 vcc, s0, v62
	v_pk_mul_f32 v[12:13], v[30:31], s[4:5] op_sel_hi:[1,0]
	v_lshrrev_b32_e32 v8, 10, v62
	v_cndmask_b32_e32 v9, v33, v11, vcc
	v_cndmask_b32_e32 v11, v32, v10, vcc
	v_lshrrev_b32_e32 v18, 6, v62
	v_cndmask_b32_e32 v10, v31, v13, vcc
	v_cndmask_b32_e32 v12, v30, v12, vcc
	v_cvt_pk_f16_f32 v11, v11, v9
	v_mov_b32_e32 v9, 0
	v_cvt_pk_f16_f32 v10, v12, v10
	v_lshlrev_b64 v[12:13], 22, v[8:9]
	v_and_or_b32 v8, v18, 15, s5
	v_lshlrev_b32_e32 v30, 10, v8
	v_or_b32_e32 v8, v30, v63
	v_lshl_add_u64 v[12:13], s[8:9], 0, v[12:13]
	v_lshlrev_b64 v[18:19], 7, v[8:9]
	v_lshl_add_u64 v[18:19], v[12:13], 0, v[18:19]
	v_lshlrev_b32_e32 v8, 1, v20
	v_lshl_add_u64 v[18:19], v[18:19], 0, v[8:9]
	s_movk_i32 s0, 0x3f0
	global_store_dwordx2 v[18:19], v[10:11], off
	v_add_u32_e32 v11, 16, v62
	v_pk_mul_f32 v[18:19], v[36:37], s[4:5] op_sel_hi:[1,0]
	v_pk_mul_f32 v[20:21], v[34:35], s[4:5] op_sel_hi:[1,0]
	v_cmp_gt_u32_e64 s[0:1], s0, v62
	v_lshrrev_b32_e32 v10, 10, v11
	v_and_or_b32 v23, v11, 48, v24
	v_cndmask_b32_e64 v22, v36, v18, s[0:1]
	v_cndmask_b32_e64 v18, v35, v21, s[0:1]
	v_cndmask_b32_e64 v20, v34, v20, s[0:1]
	v_lshrrev_b32_e32 v21, 6, v11
	v_cvt_pk_f16_f32 v18, v20, v18
	v_and_or_b32 v20, v21, 15, s5
	v_mov_b32_e32 v11, v9
	v_lshlrev_b32_e32 v31, 10, v20
	v_lshlrev_b64 v[10:11], 22, v[10:11]
	v_or_b32_e32 v20, v31, v63
	v_mov_b32_e32 v21, v9
	v_cndmask_b32_e64 v19, v37, v19, s[0:1]
	v_lshl_add_u64 v[10:11], s[8:9], 0, v[10:11]
	v_lshlrev_b64 v[20:21], 7, v[20:21]
	v_cvt_pk_f16_f32 v19, v22, v19
	v_lshl_add_u64 v[20:21], v[10:11], 0, v[20:21]
	v_lshlrev_b32_e32 v22, 1, v23
	v_mov_b32_e32 v23, v9
	v_lshl_add_u64 v[20:21], v[20:21], 0, v[22:23]
	global_store_dwordx2 v[20:21], v[18:19], off
	v_add_u32_e32 v19, 32, v62
	s_movk_i32 s2, 0x3e0
	v_and_or_b32 v33, v19, 48, v24
	v_pk_mul_f32 v[20:21], v[16:17], s[4:5] op_sel_hi:[1,0]
	v_pk_mul_f32 v[24:25], v[14:15], s[4:5] op_sel_hi:[1,0]
	v_cmp_gt_u32_e64 s[2:3], s2, v62
	v_lshrrev_b32_e32 v18, 10, v19
	v_lshrrev_b32_e32 v32, 6, v19
	v_cndmask_b32_e64 v17, v17, v21, s[2:3]
	v_cndmask_b32_e64 v16, v16, v20, s[2:3]
	v_cndmask_b32_e64 v15, v15, v25, s[2:3]
	v_cndmask_b32_e64 v14, v14, v24, s[2:3]
	v_mov_b32_e32 v19, v9
	v_cvt_pk_f16_f32 v14, v14, v15
	v_cvt_pk_f16_f32 v15, v16, v17
	v_lshlrev_b64 v[16:17], 22, v[18:19]
	v_and_or_b32 v18, v32, 15, s5
	v_lshlrev_b32_e32 v24, 10, v18
	v_or_b32_e32 v18, v24, v63
	v_lshl_add_u64 v[16:17], s[8:9], 0, v[16:17]
	v_lshlrev_b64 v[18:19], 7, v[18:19]
	v_lshl_add_u64 v[18:19], v[16:17], 0, v[18:19]
	v_lshlrev_b32_e32 v20, 1, v33
	v_mov_b32_e32 v21, v9
	v_lshl_add_u64 v[18:19], v[18:19], 0, v[20:21]
	global_store_dwordx2 v[18:19], v[14:15], off
	v_pk_mul_f32 v[14:15], v[40:41], s[4:5] op_sel_hi:[1,0]
	v_pk_mul_f32 v[18:19], v[38:39], s[4:5] op_sel_hi:[1,0]
	v_or_b32_e32 v25, 16, v63
	v_cndmask_b32_e32 v32, v40, v14, vcc
	v_cndmask_b32_e32 v14, v39, v19, vcc
	v_cndmask_b32_e32 v18, v38, v18, vcc
	v_cvt_pk_f16_f32 v14, v18, v14
	v_or_b32_e32 v18, v30, v25
	v_mov_b32_e32 v19, v9
	v_lshlrev_b64 v[18:19], 7, v[18:19]
	v_cndmask_b32_e32 v15, v41, v15, vcc
	v_lshl_add_u64 v[18:19], v[12:13], 0, v[18:19]
	v_cvt_pk_f16_f32 v15, v32, v15
	v_lshl_add_u64 v[18:19], v[18:19], 0, v[8:9]
	global_store_dwordx2 v[18:19], v[14:15], off
	v_pk_mul_f32 v[14:15], v[60:61], s[4:5] op_sel_hi:[1,0]
	v_pk_mul_f32 v[18:19], v[58:59], s[4:5] op_sel_hi:[1,0]
	v_cndmask_b32_e64 v32, v60, v14, s[0:1]
	v_cndmask_b32_e64 v14, v59, v19, s[0:1]
	v_cndmask_b32_e64 v18, v58, v18, s[0:1]
	v_cvt_pk_f16_f32 v14, v18, v14
	v_or_b32_e32 v18, v31, v25
	v_mov_b32_e32 v19, v9
	v_lshlrev_b64 v[18:19], 7, v[18:19]
	v_cndmask_b32_e64 v15, v61, v15, s[0:1]
	v_lshl_add_u64 v[18:19], v[10:11], 0, v[18:19]
	v_cvt_pk_f16_f32 v15, v32, v15
	v_lshl_add_u64 v[18:19], v[18:19], 0, v[22:23]
	global_store_dwordx2 v[18:19], v[14:15], off
	v_pk_mul_f32 v[14:15], v[28:29], s[4:5] op_sel_hi:[1,0]
	v_pk_mul_f32 v[18:19], v[26:27], s[4:5] op_sel_hi:[1,0]
	v_cndmask_b32_e64 v28, v28, v14, s[2:3]
	v_cndmask_b32_e64 v14, v27, v19, s[2:3]
	v_cndmask_b32_e64 v18, v26, v18, s[2:3]
	v_cvt_pk_f16_f32 v14, v18, v14
	v_or_b32_e32 v18, v24, v25
	v_mov_b32_e32 v19, v9
	v_lshlrev_b64 v[18:19], 7, v[18:19]
	v_cndmask_b32_e64 v15, v29, v15, s[2:3]
	v_lshl_add_u64 v[18:19], v[16:17], 0, v[18:19]
	v_cvt_pk_f16_f32 v15, v28, v15
	v_lshl_add_u64 v[18:19], v[18:19], 0, v[20:21]
	global_store_dwordx2 v[18:19], v[14:15], off
	v_pk_mul_f32 v[14:15], v[48:49], s[4:5] op_sel_hi:[1,0]
	v_pk_mul_f32 v[18:19], v[46:47], s[4:5] op_sel_hi:[1,0]
	v_or_b32_e32 v25, 32, v63
	v_cndmask_b32_e32 v26, v48, v14, vcc
	v_cndmask_b32_e32 v14, v47, v19, vcc
	v_cndmask_b32_e32 v18, v46, v18, vcc
	v_cvt_pk_f16_f32 v14, v18, v14
	v_or_b32_e32 v18, v30, v25
	v_mov_b32_e32 v19, v9
	v_lshlrev_b64 v[18:19], 7, v[18:19]
	v_cndmask_b32_e32 v15, v49, v15, vcc
	v_lshl_add_u64 v[18:19], v[12:13], 0, v[18:19]
	v_cvt_pk_f16_f32 v15, v26, v15
	v_lshl_add_u64 v[18:19], v[18:19], 0, v[8:9]
	global_store_dwordx2 v[18:19], v[14:15], off
	v_pk_mul_f32 v[14:15], v[52:53], s[4:5] op_sel_hi:[1,0]
	v_pk_mul_f32 v[18:19], v[50:51], s[4:5] op_sel_hi:[1,0]
	v_cndmask_b32_e64 v26, v52, v14, s[0:1]
	v_cndmask_b32_e64 v14, v51, v19, s[0:1]
	v_cndmask_b32_e64 v18, v50, v18, s[0:1]
	v_cvt_pk_f16_f32 v14, v18, v14
	v_or_b32_e32 v18, v31, v25
	v_mov_b32_e32 v19, v9
	v_lshlrev_b64 v[18:19], 7, v[18:19]
	v_cndmask_b32_e64 v15, v53, v15, s[0:1]
	v_lshl_add_u64 v[18:19], v[10:11], 0, v[18:19]
	v_cvt_pk_f16_f32 v15, v26, v15
	v_lshl_add_u64 v[18:19], v[18:19], 0, v[22:23]
	global_store_dwordx2 v[18:19], v[14:15], off
	v_pk_mul_f32 v[14:15], v[44:45], s[4:5] op_sel_hi:[1,0]
	v_pk_mul_f32 v[18:19], v[42:43], s[4:5] op_sel_hi:[1,0]
	v_cndmask_b32_e64 v26, v44, v14, s[2:3]
	v_cndmask_b32_e64 v14, v43, v19, s[2:3]
	v_cndmask_b32_e64 v18, v42, v18, s[2:3]
	v_cvt_pk_f16_f32 v14, v18, v14
	v_or_b32_e32 v18, v24, v25
	v_mov_b32_e32 v19, v9
	v_lshlrev_b64 v[18:19], 7, v[18:19]
	v_cndmask_b32_e64 v15, v45, v15, s[2:3]
	v_lshl_add_u64 v[18:19], v[16:17], 0, v[18:19]
	v_cvt_pk_f16_f32 v15, v26, v15
	v_lshl_add_u64 v[18:19], v[18:19], 0, v[20:21]
	global_store_dwordx2 v[18:19], v[14:15], off
	v_pk_mul_f32 v[14:15], v[56:57], s[4:5] op_sel_hi:[1,0]
	v_pk_mul_f32 v[18:19], v[54:55], s[4:5] op_sel_hi:[1,0]
	v_or_b32_e32 v25, 48, v63
	v_cndmask_b32_e32 v26, v56, v14, vcc
	v_cndmask_b32_e32 v14, v55, v19, vcc
	v_cndmask_b32_e32 v18, v54, v18, vcc
	v_cvt_pk_f16_f32 v14, v18, v14
	v_or_b32_e32 v18, v30, v25
	v_mov_b32_e32 v19, v9
	v_lshlrev_b64 v[18:19], 7, v[18:19]
	v_cndmask_b32_e32 v15, v57, v15, vcc
	v_lshl_add_u64 v[12:13], v[12:13], 0, v[18:19]
	v_cvt_pk_f16_f32 v15, v26, v15
	v_lshl_add_u64 v[12:13], v[12:13], 0, v[8:9]
	global_store_dwordx2 v[12:13], v[14:15], off
	v_pk_mul_f32 v[12:13], v[6:7], s[4:5] op_sel_hi:[1,0]
	v_pk_mul_f32 v[14:15], v[4:5], s[4:5] op_sel_hi:[1,0]
	v_cndmask_b32_e64 v7, v7, v13, s[0:1]
	v_cndmask_b32_e64 v6, v6, v12, s[0:1]
	v_cndmask_b32_e64 v5, v5, v15, s[0:1]
	v_cndmask_b32_e64 v4, v4, v14, s[0:1]
	v_or_b32_e32 v8, v31, v25
	v_cvt_pk_f16_f32 v4, v4, v5
	v_cvt_pk_f16_f32 v5, v6, v7
	v_lshlrev_b64 v[6:7], 7, v[8:9]
	v_lshl_add_u64 v[6:7], v[10:11], 0, v[6:7]
	v_lshl_add_u64 v[6:7], v[6:7], 0, v[22:23]
	global_store_dwordx2 v[6:7], v[4:5], off
	v_pk_mul_f32 v[4:5], v[2:3], s[4:5] op_sel_hi:[1,0]
	v_pk_mul_f32 v[6:7], v[0:1], s[4:5] op_sel_hi:[1,0]
	v_cndmask_b32_e64 v3, v3, v5, s[2:3]
	v_cndmask_b32_e64 v2, v2, v4, s[2:3]
	v_cndmask_b32_e64 v1, v1, v7, s[2:3]
	v_cndmask_b32_e64 v0, v0, v6, s[2:3]
	v_or_b32_e32 v8, v24, v25
	v_cvt_pk_f16_f32 v0, v0, v1
	v_cvt_pk_f16_f32 v1, v2, v3
	v_lshlrev_b64 v[2:3], 7, v[8:9]
	v_lshl_add_u64 v[2:3], v[16:17], 0, v[2:3]
	v_lshl_add_u64 v[2:3], v[2:3], 0, v[20:21]
	global_store_dwordx2 v[2:3], v[0:1], off
	s_endpgm
	s_endpgm
	s_endpgm
	s_endpgm
	s_endpgm
	s_endpgm
	s_endpgm
	s_endpgm
	s_endpgm
	s_endpgm
	s_endpgm
	s_endpgm
	s_endpgm
	s_endpgm
	s_endpgm
	s_endpgm
	s_endpgm
	s_endpgm
	s_endpgm
	s_endpgm
	s_endpgm
	s_endpgm
	s_endpgm
	s_endpgm
	s_endpgm
	s_endpgm
	s_endpgm
	s_endpgm
	s_endpgm
	s_endpgm
	s_endpgm
	s_endpgm
	s_endpgm
	s_endpgm
	s_endpgm
	s_endpgm
	s_endpgm
	s_endpgm
	s_endpgm
	s_endpgm
	s_endpgm
	s_endpgm
	s_endpgm
	s_endpgm
	s_endpgm
	s_endpgm
	s_endpgm
	s_endpgm
	s_endpgm
	s_endpgm
	s_endpgm
	s_endpgm
	s_endpgm
	.section	.rodata,"a",@progbits
	.p2align	6, 0x0
	.amdhsa_kernel _Z5gemm8ILi192ELi2ELi3ELi0ELi1ELi16EEvPKDF16_S1_iiiPDF16_PfPKf
		.amdhsa_group_segment_fixed_size 0
		.amdhsa_private_segment_fixed_size 0
		.amdhsa_kernarg_size 312
		.amdhsa_user_sgpr_count 2
		.amdhsa_user_sgpr_dispatch_ptr 0
		.amdhsa_user_sgpr_queue_ptr 0
		.amdhsa_user_sgpr_kernarg_segment_ptr 1
		.amdhsa_user_sgpr_dispatch_id 0
		.amdhsa_user_sgpr_kernarg_preload_length 0
		.amdhsa_user_sgpr_kernarg_preload_offset 0
		.amdhsa_user_sgpr_private_segment_size 0
		.amdhsa_uses_dynamic_stack 0
		.amdhsa_enable_private_segment 0
		.amdhsa_system_sgpr_workgroup_id_x 1
		.amdhsa_system_sgpr_workgroup_id_y 0
		.amdhsa_system_sgpr_workgroup_id_z 0
		.amdhsa_system_sgpr_workgroup_info 0
		.amdhsa_system_vgpr_workitem_id 0
		.amdhsa_next_free_vgpr 125
		.amdhsa_next_free_sgpr 32
		.amdhsa_accum_offset 128
		.amdhsa_reserve_vcc 1
		.amdhsa_float_round_mode_32 0
		.amdhsa_float_round_mode_16_64 0
		.amdhsa_float_denorm_mode_32 3
		.amdhsa_float_denorm_mode_16_64 3
		.amdhsa_dx10_clamp 1
		.amdhsa_ieee_mode 1
		.amdhsa_fp16_overflow 0
		.amdhsa_tg_split 0
		.amdhsa_exception_fp_ieee_invalid_op 0
		.amdhsa_exception_fp_denorm_src 0
		.amdhsa_exception_fp_ieee_div_zero 0
		.amdhsa_exception_fp_ieee_overflow 0
		.amdhsa_exception_fp_ieee_underflow 0
		.amdhsa_exception_fp_ieee_inexact 0
		.amdhsa_exception_int_div_zero 0
	.end_amdhsa_kernel

_Z5gemm8ILi128ELi2ELi2ELi2ELi1ELi16EEvPKDF16_S1_iiiPDF16_PfPKf:
	v_readfirstlane_b32 s24, v0
	s_nop 3
	s_bitcmp1_b32 s24, 8
	s_cbranch_scc0 .Lprio_skip1
	s_setprio 1
.Lprio_skip1:
	s_load_dwordx2 s[10:11], s[0:1], 0x30
	s_load_dword s12, s[0:1], 0x38
	s_load_dwordx4 s[4:7], s[0:1], 0x0
	s_load_dwordx2 s[8:9], s[0:1], 0x20
	s_and_b32 s3, s2, 7
	s_waitcnt lgkmcnt(0)
	s_cmpk_lg_i32 s12, 0x200
	s_cbranch_scc0 .LBB5_2
	s_lshl_b32 s12, s3, 1
	s_and_b32 s12, s12, 12
	s_bfe_u32 s13, s2, 0x20003
	s_or_b32 s14, s12, s13
	s_lshl_b32 s12, s2, 3
	s_and_b32 s12, s12, 8
	s_lshr_b32 s13, s2, 5
	s_add_i32 s15, s12, s13
	s_cbranch_execz .LBB5_3
	s_branch .LBB5_4

.LBB5_4:
	s_load_dwordx2 s[2:3], s[0:1], 0x14
	v_lshrrev_b32_e32 v3, 4, v0
	s_lshl_b32 s12, s15, 7
	s_lshl_b32 s13, s14, 7
	v_xor_b32_e32 v1, v3, v0
	s_waitcnt lgkmcnt(0)
	s_ashr_i32 s14, s3, 31
	s_mul_i32 s0, s12, s14
	s_mul_hi_u32 s1, s12, s3
	v_lshlrev_b32_e32 v1, 3, v1
	v_or_b32_e32 v4, 0x200, v0
	s_add_i32 s1, s1, s0
	s_mul_i32 s0, s12, s3
	v_and_b32_e32 v2, 56, v1
	v_lshrrev_b32_e32 v1, 3, v0
	v_lshrrev_b32_e32 v4, 3, v4
	s_lshl_b64 s[0:1], s[0:1], 1
	v_mul_lo_u32 v1, v1, s3
	v_mul_lo_u32 v4, v4, s3
	s_add_u32 s0, s4, s0
	v_add_lshl_u32 v1, v1, v2, 1
	v_add_lshl_u32 v2, v4, v2, 1
	s_addc_u32 s1, s5, s1
	s_mul_i32 s4, s13, s14
	s_mul_hi_u32 s5, s13, s3
	v_lshl_add_u32 v4, v0, 4, 0
	s_add_i32 s5, s5, s4
	s_mul_i32 s4, s13, s3
	v_readfirstlane_b32 s18, v4
	v_add_u32_e32 v5, 0x2000, v4
	s_lshl_b64 s[4:5], s[4:5], 1
	s_mov_b32 m0, s18
	v_readfirstlane_b32 s15, v5
	v_add_u32_e32 v5, 0x4000, v4
	s_add_u32 s4, s6, s4
	global_load_lds_dwordx4 v1, s[0:1]
	s_mov_b32 m0, s15
	v_readfirstlane_b32 s16, v5
	v_add_u32_e32 v5, 0x6000, v4
	s_addc_u32 s5, s7, s5
	global_load_lds_dwordx4 v2, s[0:1]
	s_mov_b32 m0, s16
	v_readfirstlane_b32 s17, v5
	v_add_u32_e32 v5, 0x8000, v4
	global_load_lds_dwordx4 v1, s[4:5]
	s_mov_b32 m0, s17
	s_add_u32 s6, s0, 0x80
	v_readfirstlane_b32 s14, v5
	v_add_u32_e32 v5, 0xa000, v4
	global_load_lds_dwordx4 v2, s[4:5]
	s_addc_u32 s7, s1, 0
	s_mov_b32 m0, s14
	v_readfirstlane_b32 s3, v5
	global_load_lds_dwordx4 v1, s[6:7]
	s_mov_b32 m0, s3
	v_add_u32_e32 v5, 0xc000, v4
	s_add_u32 s20, s4, 0x80
	global_load_lds_dwordx4 v2, s[6:7]
	v_readfirstlane_b32 s6, v5
	v_add_u32_e32 v4, 0xe000, v4
	s_addc_u32 s21, s5, 0
	s_mov_b32 m0, s6
	v_readfirstlane_b32 s7, v4
	global_load_lds_dwordx4 v1, s[20:21]
	s_mov_b32 m0, s7
	v_lshrrev_b32_e32 v5, 1, v0
	global_load_lds_dwordx4 v2, s[20:21]
	v_bfe_u32 v6, v0, 1, 3
	v_and_b32_e32 v4, 15, v0
	v_lshrrev_b32_e32 v7, 2, v0
	v_bitop3_b32 v3, v3, v6, 3 bitop3:0x6c
	v_and_b32_e32 v8, 0x60, v5
	v_and_or_b32 v32, v7, 64, v4
	v_lshlrev_b32_e32 v7, 4, v3
	v_or_b32_e32 v3, v8, v4
	v_lshl_add_u32 v4, v3, 7, 0
	s_waitcnt vmcnt(4)
	s_barrier
	v_add_u32_e32 v3, v4, v7
	ds_read_b128 v[10:13], v3 offset:16384
	v_lshl_add_u32 v30, v32, 7, 0
	v_add_u32_e32 v5, v30, v7
	ds_read_b128 v[14:17], v5
	ds_read_b128 v[18:21], v3 offset:18432
	ds_read_b128 v[22:25], v5 offset:2048
	ds_read_b128 v[34:37], v5 offset:4096
	ds_read_b128 v[38:41], v5 offset:6144
	v_bfe_u32 v9, v0, 4, 2
	v_bitop3_b32 v0, v9, v6, 4 bitop3:0x36
	s_waitcnt lgkmcnt(0)
	v_mfma_f32_16x16x32_f16 v[26:29], v[10:13], v[14:17], 0
	v_lshlrev_b32_e32 v6, 4, v0
	v_mfma_f32_16x16x32_f16 v[14:17], v[18:21], v[14:17], 0
	v_add_u32_e32 v0, v30, v6
	ds_read_b128 v[42:45], v0
	ds_read_b128 v[46:49], v0 offset:2048
	ds_read_b128 v[50:53], v0 offset:4096
	ds_read_b128 v[54:57], v0 offset:6144
	v_add_u32_e32 v4, v4, v6
	ds_read_b128 v[58:61], v4 offset:16384
	ds_read_b128 v[62:65], v4 offset:18432
	v_mfma_f32_16x16x32_f16 v[66:69], v[10:13], v[22:25], 0
	v_mfma_f32_16x16x32_f16 v[22:25], v[18:21], v[22:25], 0
	v_mfma_f32_16x16x32_f16 v[70:73], v[10:13], v[34:37], 0
	v_mfma_f32_16x16x32_f16 v[34:37], v[18:21], v[34:37], 0
	v_mfma_f32_16x16x32_f16 v[10:13], v[10:13], v[38:41], 0
	v_mfma_f32_16x16x32_f16 v[18:21], v[18:21], v[38:41], 0
	s_add_u32 s20, s0, 0x100
	s_mov_b32 m0, s18
	s_waitcnt vmcnt(0) lgkmcnt(0)
	s_barrier
	s_addc_u32 s21, s1, 0
	s_add_u32 s22, s4, 0x100
	global_load_lds_dwordx4 v1, s[20:21]
	s_mov_b32 m0, s15
	s_addc_u32 s23, s5, 0
	global_load_lds_dwordx4 v2, s[20:21]
	s_mov_b32 m0, s16
	s_nop 0
	global_load_lds_dwordx4 v1, s[22:23]
	s_mov_b32 m0, s17
	s_nop 0
	global_load_lds_dwordx4 v2, s[22:23]
	s_waitcnt lgkmcnt(0)
	v_mfma_f32_16x16x32_f16 v[26:29], v[58:61], v[42:45], v[26:29]
	v_mfma_f32_16x16x32_f16 v[14:17], v[62:65], v[42:45], v[14:17]
	ds_read_b128 v[38:41], v5 offset:32768
	ds_read_b128 v[42:45], v5 offset:34816
	ds_read_b128 v[74:77], v5 offset:36864
	ds_read_b128 v[78:81], v5 offset:38912
	ds_read_b128 v[82:85], v3 offset:49152
	ds_read_b128 v[86:89], v3 offset:51200
	v_mfma_f32_16x16x32_f16 v[66:69], v[58:61], v[46:49], v[66:69]
	v_mfma_f32_16x16x32_f16 v[22:25], v[62:65], v[46:49], v[22:25]
	v_mfma_f32_16x16x32_f16 v[46:49], v[58:61], v[50:53], v[70:73]
	v_mfma_f32_16x16x32_f16 v[34:37], v[62:65], v[50:53], v[34:37]
	v_mfma_f32_16x16x32_f16 v[10:13], v[58:61], v[54:57], v[10:13]
	v_mfma_f32_16x16x32_f16 v[18:21], v[62:65], v[54:57], v[18:21]
	s_waitcnt lgkmcnt(0)
	v_mfma_f32_16x16x32_f16 v[26:29], v[82:85], v[38:41], v[26:29]
	v_mfma_f32_16x16x32_f16 v[14:17], v[86:89], v[38:41], v[14:17]
	ds_read_b128 v[38:41], v0 offset:32768
	ds_read_b128 v[50:53], v0 offset:34816
	ds_read_b128 v[54:57], v0 offset:36864
	ds_read_b128 v[58:61], v0 offset:38912
	ds_read_b128 v[62:65], v4 offset:49152
	ds_read_b128 v[70:73], v4 offset:51200
	v_mfma_f32_16x16x32_f16 v[66:69], v[82:85], v[42:45], v[66:69]
	v_mfma_f32_16x16x32_f16 v[22:25], v[86:89], v[42:45], v[22:25]
	v_mfma_f32_16x16x32_f16 v[42:45], v[82:85], v[74:77], v[46:49]
	v_mfma_f32_16x16x32_f16 v[34:37], v[86:89], v[74:77], v[34:37]
	v_mfma_f32_16x16x32_f16 v[10:13], v[82:85], v[78:81], v[10:13]
	v_mfma_f32_16x16x32_f16 v[18:21], v[86:89], v[78:81], v[18:21]
	s_add_u32 s20, s0, 0x180
	s_mov_b32 m0, s14
	s_waitcnt vmcnt(0) lgkmcnt(0)
	s_barrier
	s_addc_u32 s21, s1, 0
	s_add_u32 s22, s4, 0x180
	global_load_lds_dwordx4 v1, s[20:21]
	s_mov_b32 m0, s3
	s_addc_u32 s23, s5, 0
	global_load_lds_dwordx4 v2, s[20:21]
	s_mov_b32 m0, s6
	s_nop 0
	global_load_lds_dwordx4 v1, s[22:23]
	s_mov_b32 m0, s7
	s_nop 0
	global_load_lds_dwordx4 v2, s[22:23]
	s_waitcnt lgkmcnt(0)
	v_mfma_f32_16x16x32_f16 v[26:29], v[62:65], v[38:41], v[26:29]
	v_mfma_f32_16x16x32_f16 v[14:17], v[70:73], v[38:41], v[14:17]
	ds_read_b128 v[38:41], v5
	ds_read_b128 v[46:49], v5 offset:2048
	ds_read_b128 v[74:77], v5 offset:4096
	ds_read_b128 v[78:81], v5 offset:6144
	ds_read_b128 v[82:85], v3 offset:16384
	ds_read_b128 v[86:89], v3 offset:18432
	v_mfma_f32_16x16x32_f16 v[66:69], v[62:65], v[50:53], v[66:69]
	v_mfma_f32_16x16x32_f16 v[22:25], v[70:73], v[50:53], v[22:25]
	v_mfma_f32_16x16x32_f16 v[42:45], v[62:65], v[54:57], v[42:45]
	v_mfma_f32_16x16x32_f16 v[34:37], v[70:73], v[54:57], v[34:37]
	v_mfma_f32_16x16x32_f16 v[10:13], v[62:65], v[58:61], v[10:13]
	v_mfma_f32_16x16x32_f16 v[18:21], v[70:73], v[58:61], v[18:21]
	s_waitcnt lgkmcnt(0)
	v_mfma_f32_16x16x32_f16 v[26:29], v[82:85], v[38:41], v[26:29]
	v_mfma_f32_16x16x32_f16 v[14:17], v[86:89], v[38:41], v[14:17]
	ds_read_b128 v[38:41], v0
	ds_read_b128 v[50:53], v0 offset:2048
	ds_read_b128 v[54:57], v0 offset:4096
	ds_read_b128 v[58:61], v0 offset:6144
	ds_read_b128 v[62:65], v4 offset:16384
	ds_read_b128 v[70:73], v4 offset:18432
	v_mfma_f32_16x16x32_f16 v[66:69], v[82:85], v[46:49], v[66:69]
	v_mfma_f32_16x16x32_f16 v[22:25], v[86:89], v[46:49], v[22:25]
	v_mfma_f32_16x16x32_f16 v[42:45], v[82:85], v[74:77], v[42:45]
	v_mfma_f32_16x16x32_f16 v[34:37], v[86:89], v[74:77], v[34:37]
	v_mfma_f32_16x16x32_f16 v[10:13], v[82:85], v[78:81], v[10:13]
	v_mfma_f32_16x16x32_f16 v[18:21], v[86:89], v[78:81], v[18:21]
	s_add_u32 s20, s0, 0x200
	s_mov_b32 m0, s18
	s_waitcnt vmcnt(0) lgkmcnt(0)
	s_barrier
	s_addc_u32 s21, s1, 0
	s_add_u32 s22, s4, 0x200
	global_load_lds_dwordx4 v1, s[20:21]
	s_mov_b32 m0, s15
	s_addc_u32 s23, s5, 0
	global_load_lds_dwordx4 v2, s[20:21]
	s_mov_b32 m0, s16
	s_nop 0
	global_load_lds_dwordx4 v1, s[22:23]
	s_mov_b32 m0, s17
	s_nop 0
	global_load_lds_dwordx4 v2, s[22:23]
	s_waitcnt lgkmcnt(0)
	v_mfma_f32_16x16x32_f16 v[26:29], v[62:65], v[38:41], v[26:29]
	v_mfma_f32_16x16x32_f16 v[14:17], v[70:73], v[38:41], v[14:17]
	ds_read_b128 v[38:41], v5 offset:32768
	ds_read_b128 v[46:49], v5 offset:34816
	ds_read_b128 v[74:77], v5 offset:36864
	ds_read_b128 v[78:81], v5 offset:38912
	ds_read_b128 v[82:85], v3 offset:49152
	ds_read_b128 v[86:89], v3 offset:51200
	v_mfma_f32_16x16x32_f16 v[66:69], v[62:65], v[50:53], v[66:69]
	v_mfma_f32_16x16x32_f16 v[22:25], v[70:73], v[50:53], v[22:25]
	v_mfma_f32_16x16x32_f16 v[42:45], v[62:65], v[54:57], v[42:45]
	v_mfma_f32_16x16x32_f16 v[34:37], v[70:73], v[54:57], v[34:37]
	v_mfma_f32_16x16x32_f16 v[10:13], v[62:65], v[58:61], v[10:13]
	v_mfma_f32_16x16x32_f16 v[18:21], v[70:73], v[58:61], v[18:21]
	s_waitcnt lgkmcnt(0)
	v_mfma_f32_16x16x32_f16 v[26:29], v[82:85], v[38:41], v[26:29]
	v_mfma_f32_16x16x32_f16 v[14:17], v[86:89], v[38:41], v[14:17]
	ds_read_b128 v[38:41], v0 offset:32768
	ds_read_b128 v[50:53], v0 offset:34816
	ds_read_b128 v[54:57], v0 offset:36864
	ds_read_b128 v[58:61], v0 offset:38912
	ds_read_b128 v[62:65], v4 offset:49152
	ds_read_b128 v[70:73], v4 offset:51200
	v_mfma_f32_16x16x32_f16 v[66:69], v[82:85], v[46:49], v[66:69]
	v_mfma_f32_16x16x32_f16 v[22:25], v[86:89], v[46:49], v[22:25]
	v_mfma_f32_16x16x32_f16 v[42:45], v[82:85], v[74:77], v[42:45]
	v_mfma_f32_16x16x32_f16 v[34:37], v[86:89], v[74:77], v[34:37]
	v_mfma_f32_16x16x32_f16 v[10:13], v[82:85], v[78:81], v[10:13]
	v_mfma_f32_16x16x32_f16 v[18:21], v[86:89], v[78:81], v[18:21]
	s_add_u32 s20, s0, 0x280
	s_mov_b32 m0, s14
	s_waitcnt vmcnt(0) lgkmcnt(0)
	s_barrier
	s_addc_u32 s21, s1, 0
	s_add_u32 s22, s4, 0x280
	global_load_lds_dwordx4 v1, s[20:21]
	s_mov_b32 m0, s3
	s_addc_u32 s23, s5, 0
	global_load_lds_dwordx4 v2, s[20:21]
	s_mov_b32 m0, s6
	s_nop 0
	global_load_lds_dwordx4 v1, s[22:23]
	s_mov_b32 m0, s7
	s_nop 0
	global_load_lds_dwordx4 v2, s[22:23]
	s_waitcnt lgkmcnt(0)
	v_mfma_f32_16x16x32_f16 v[26:29], v[62:65], v[38:41], v[26:29]
	v_mfma_f32_16x16x32_f16 v[14:17], v[70:73], v[38:41], v[14:17]
	ds_read_b128 v[38:41], v5
	ds_read_b128 v[46:49], v5 offset:2048
	ds_read_b128 v[74:77], v5 offset:4096
	ds_read_b128 v[78:81], v5 offset:6144
	ds_read_b128 v[82:85], v3 offset:16384
	ds_read_b128 v[86:89], v3 offset:18432
	v_mfma_f32_16x16x32_f16 v[66:69], v[62:65], v[50:53], v[66:69]
	v_mfma_f32_16x16x32_f16 v[22:25], v[70:73], v[50:53], v[22:25]
	v_mfma_f32_16x16x32_f16 v[42:45], v[62:65], v[54:57], v[42:45]
	v_mfma_f32_16x16x32_f16 v[34:37], v[70:73], v[54:57], v[34:37]
	v_mfma_f32_16x16x32_f16 v[10:13], v[62:65], v[58:61], v[10:13]
	v_mfma_f32_16x16x32_f16 v[18:21], v[70:73], v[58:61], v[18:21]
	s_waitcnt lgkmcnt(0)
	v_mfma_f32_16x16x32_f16 v[26:29], v[82:85], v[38:41], v[26:29]
	v_mfma_f32_16x16x32_f16 v[14:17], v[86:89], v[38:41], v[14:17]
	ds_read_b128 v[38:41], v0
	ds_read_b128 v[50:53], v0 offset:2048
	ds_read_b128 v[54:57], v0 offset:4096
	ds_read_b128 v[58:61], v0 offset:6144
	ds_read_b128 v[62:65], v4 offset:16384
	ds_read_b128 v[70:73], v4 offset:18432
	v_mfma_f32_16x16x32_f16 v[66:69], v[82:85], v[46:49], v[66:69]
	v_mfma_f32_16x16x32_f16 v[22:25], v[86:89], v[46:49], v[22:25]
	v_mfma_f32_16x16x32_f16 v[42:45], v[82:85], v[74:77], v[42:45]
	v_mfma_f32_16x16x32_f16 v[34:37], v[86:89], v[74:77], v[34:37]
	v_mfma_f32_16x16x32_f16 v[10:13], v[82:85], v[78:81], v[10:13]
	v_mfma_f32_16x16x32_f16 v[18:21], v[86:89], v[78:81], v[18:21]
	s_add_u32 s20, s0, 0x300
	s_mov_b32 m0, s18
	s_waitcnt vmcnt(0) lgkmcnt(0)
	s_barrier
	s_addc_u32 s21, s1, 0
	s_add_u32 s22, s4, 0x300
	global_load_lds_dwordx4 v1, s[20:21]
	s_mov_b32 m0, s15
	s_addc_u32 s23, s5, 0
	global_load_lds_dwordx4 v2, s[20:21]
	s_mov_b32 m0, s16
	s_nop 0
	global_load_lds_dwordx4 v1, s[22:23]
	s_mov_b32 m0, s17
	s_nop 0
	global_load_lds_dwordx4 v2, s[22:23]
	s_waitcnt lgkmcnt(0)
	v_mfma_f32_16x16x32_f16 v[26:29], v[62:65], v[38:41], v[26:29]
	v_mfma_f32_16x16x32_f16 v[14:17], v[70:73], v[38:41], v[14:17]
	ds_read_b128 v[38:41], v5 offset:32768
	ds_read_b128 v[46:49], v5 offset:34816
	ds_read_b128 v[74:77], v5 offset:36864
	ds_read_b128 v[78:81], v5 offset:38912
	ds_read_b128 v[82:85], v3 offset:49152
	ds_read_b128 v[86:89], v3 offset:51200
	v_mfma_f32_16x16x32_f16 v[66:69], v[62:65], v[50:53], v[66:69]
	v_mfma_f32_16x16x32_f16 v[22:25], v[70:73], v[50:53], v[22:25]
	v_mfma_f32_16x16x32_f16 v[42:45], v[62:65], v[54:57], v[42:45]
	v_mfma_f32_16x16x32_f16 v[34:37], v[70:73], v[54:57], v[34:37]
	v_mfma_f32_16x16x32_f16 v[10:13], v[62:65], v[58:61], v[10:13]
	v_mfma_f32_16x16x32_f16 v[18:21], v[70:73], v[58:61], v[18:21]
	s_waitcnt lgkmcnt(0)
	v_mfma_f32_16x16x32_f16 v[26:29], v[82:85], v[38:41], v[26:29]
	v_mfma_f32_16x16x32_f16 v[14:17], v[86:89], v[38:41], v[14:17]
	ds_read_b128 v[38:41], v0 offset:32768
	ds_read_b128 v[50:53], v0 offset:34816
	ds_read_b128 v[54:57], v0 offset:36864
	ds_read_b128 v[58:61], v0 offset:38912
	ds_read_b128 v[62:65], v4 offset:49152
	ds_read_b128 v[70:73], v4 offset:51200
	v_mfma_f32_16x16x32_f16 v[66:69], v[82:85], v[46:49], v[66:69]
	v_mfma_f32_16x16x32_f16 v[22:25], v[86:89], v[46:49], v[22:25]
	v_mfma_f32_16x16x32_f16 v[42:45], v[82:85], v[74:77], v[42:45]
	v_mfma_f32_16x16x32_f16 v[34:37], v[86:89], v[74:77], v[34:37]
	v_mfma_f32_16x16x32_f16 v[10:13], v[82:85], v[78:81], v[10:13]
	v_mfma_f32_16x16x32_f16 v[18:21], v[86:89], v[78:81], v[18:21]
	s_add_u32 s20, s0, 0x380
	s_mov_b32 m0, s14
	s_waitcnt vmcnt(0) lgkmcnt(0)
	s_barrier
	s_addc_u32 s21, s1, 0
	s_add_u32 s22, s4, 0x380
	global_load_lds_dwordx4 v1, s[20:21]
	s_mov_b32 m0, s3
	s_addc_u32 s23, s5, 0
	global_load_lds_dwordx4 v2, s[20:21]
	s_mov_b32 m0, s6
	s_nop 0
	global_load_lds_dwordx4 v1, s[22:23]
	s_mov_b32 m0, s7
	s_nop 0
	global_load_lds_dwordx4 v2, s[22:23]
	s_waitcnt lgkmcnt(0)
	v_mfma_f32_16x16x32_f16 v[26:29], v[62:65], v[38:41], v[26:29]
	v_mfma_f32_16x16x32_f16 v[14:17], v[70:73], v[38:41], v[14:17]
	ds_read_b128 v[38:41], v5
	ds_read_b128 v[46:49], v5 offset:2048
	ds_read_b128 v[74:77], v5 offset:4096
	ds_read_b128 v[78:81], v5 offset:6144
	ds_read_b128 v[82:85], v3 offset:16384
	ds_read_b128 v[86:89], v3 offset:18432
	v_mfma_f32_16x16x32_f16 v[66:69], v[62:65], v[50:53], v[66:69]
	v_mfma_f32_16x16x32_f16 v[22:25], v[70:73], v[50:53], v[22:25]
	v_mfma_f32_16x16x32_f16 v[42:45], v[62:65], v[54:57], v[42:45]
	v_mfma_f32_16x16x32_f16 v[34:37], v[70:73], v[54:57], v[34:37]
	v_mfma_f32_16x16x32_f16 v[10:13], v[62:65], v[58:61], v[10:13]
	v_mfma_f32_16x16x32_f16 v[18:21], v[70:73], v[58:61], v[18:21]
	s_waitcnt lgkmcnt(0)
	v_mfma_f32_16x16x32_f16 v[26:29], v[82:85], v[38:41], v[26:29]
	v_mfma_f32_16x16x32_f16 v[14:17], v[86:89], v[38:41], v[14:17]
	ds_read_b128 v[38:41], v0
	ds_read_b128 v[50:53], v0 offset:2048
	ds_read_b128 v[54:57], v0 offset:4096
	ds_read_b128 v[58:61], v0 offset:6144
	ds_read_b128 v[62:65], v4 offset:16384
	ds_read_b128 v[70:73], v4 offset:18432
	v_mfma_f32_16x16x32_f16 v[66:69], v[82:85], v[46:49], v[66:69]
	v_mfma_f32_16x16x32_f16 v[22:25], v[86:89], v[46:49], v[22:25]
	v_mfma_f32_16x16x32_f16 v[42:45], v[82:85], v[74:77], v[42:45]
	v_mfma_f32_16x16x32_f16 v[34:37], v[86:89], v[74:77], v[34:37]
	v_mfma_f32_16x16x32_f16 v[10:13], v[82:85], v[78:81], v[10:13]
	v_mfma_f32_16x16x32_f16 v[18:21], v[86:89], v[78:81], v[18:21]
	s_add_u32 s20, s0, 0x400
	s_mov_b32 m0, s18
	s_waitcnt vmcnt(0) lgkmcnt(0)
	s_barrier
	s_addc_u32 s21, s1, 0
	s_add_u32 s22, s4, 0x400
	global_load_lds_dwordx4 v1, s[20:21]
	s_mov_b32 m0, s15
	s_addc_u32 s23, s5, 0
	global_load_lds_dwordx4 v2, s[20:21]
	s_mov_b32 m0, s16
	s_nop 0
	global_load_lds_dwordx4 v1, s[22:23]
	s_mov_b32 m0, s17
	s_nop 0
	global_load_lds_dwordx4 v2, s[22:23]
	s_waitcnt lgkmcnt(0)
	v_mfma_f32_16x16x32_f16 v[26:29], v[62:65], v[38:41], v[26:29]
	v_mfma_f32_16x16x32_f16 v[14:17], v[70:73], v[38:41], v[14:17]
	ds_read_b128 v[38:41], v5 offset:32768
	ds_read_b128 v[46:49], v5 offset:34816
	ds_read_b128 v[74:77], v5 offset:36864
	ds_read_b128 v[78:81], v5 offset:38912
	ds_read_b128 v[82:85], v3 offset:49152
	ds_read_b128 v[86:89], v3 offset:51200
	v_mfma_f32_16x16x32_f16 v[66:69], v[62:65], v[50:53], v[66:69]
	v_mfma_f32_16x16x32_f16 v[22:25], v[70:73], v[50:53], v[22:25]
	v_mfma_f32_16x16x32_f16 v[42:45], v[62:65], v[54:57], v[42:45]
	v_mfma_f32_16x16x32_f16 v[34:37], v[70:73], v[54:57], v[34:37]
	v_mfma_f32_16x16x32_f16 v[10:13], v[62:65], v[58:61], v[10:13]
	v_mfma_f32_16x16x32_f16 v[18:21], v[70:73], v[58:61], v[18:21]
	s_waitcnt lgkmcnt(0)
	v_mfma_f32_16x16x32_f16 v[26:29], v[82:85], v[38:41], v[26:29]
	v_mfma_f32_16x16x32_f16 v[14:17], v[86:89], v[38:41], v[14:17]
	ds_read_b128 v[38:41], v0 offset:32768
	ds_read_b128 v[50:53], v0 offset:34816
	ds_read_b128 v[54:57], v0 offset:36864
	ds_read_b128 v[58:61], v0 offset:38912
	ds_read_b128 v[62:65], v4 offset:49152
	ds_read_b128 v[70:73], v4 offset:51200
	v_mfma_f32_16x16x32_f16 v[66:69], v[82:85], v[46:49], v[66:69]
	v_mfma_f32_16x16x32_f16 v[22:25], v[86:89], v[46:49], v[22:25]
	v_mfma_f32_16x16x32_f16 v[42:45], v[82:85], v[74:77], v[42:45]
	v_mfma_f32_16x16x32_f16 v[34:37], v[86:89], v[74:77], v[34:37]
	v_mfma_f32_16x16x32_f16 v[10:13], v[82:85], v[78:81], v[10:13]
	v_mfma_f32_16x16x32_f16 v[18:21], v[86:89], v[78:81], v[18:21]
	s_add_u32 s20, s0, 0x480
	s_mov_b32 m0, s14
	s_waitcnt vmcnt(0) lgkmcnt(0)
	s_barrier
	s_addc_u32 s21, s1, 0
	s_add_u32 s22, s4, 0x480
	global_load_lds_dwordx4 v1, s[20:21]
	s_mov_b32 m0, s3
	s_addc_u32 s23, s5, 0
	global_load_lds_dwordx4 v2, s[20:21]
	s_mov_b32 m0, s6
	s_nop 0
	global_load_lds_dwordx4 v1, s[22:23]
	s_mov_b32 m0, s7
	s_nop 0
	global_load_lds_dwordx4 v2, s[22:23]
	s_waitcnt lgkmcnt(0)
	v_mfma_f32_16x16x32_f16 v[26:29], v[62:65], v[38:41], v[26:29]
	v_mfma_f32_16x16x32_f16 v[14:17], v[70:73], v[38:41], v[14:17]
	ds_read_b128 v[38:41], v5
	ds_read_b128 v[46:49], v5 offset:2048
	ds_read_b128 v[74:77], v5 offset:4096
	ds_read_b128 v[78:81], v5 offset:6144
	ds_read_b128 v[82:85], v3 offset:16384
	ds_read_b128 v[86:89], v3 offset:18432
	v_mfma_f32_16x16x32_f16 v[66:69], v[62:65], v[50:53], v[66:69]
	v_mfma_f32_16x16x32_f16 v[22:25], v[70:73], v[50:53], v[22:25]
	v_mfma_f32_16x16x32_f16 v[42:45], v[62:65], v[54:57], v[42:45]
	v_mfma_f32_16x16x32_f16 v[34:37], v[70:73], v[54:57], v[34:37]
	v_mfma_f32_16x16x32_f16 v[10:13], v[62:65], v[58:61], v[10:13]
	v_mfma_f32_16x16x32_f16 v[18:21], v[70:73], v[58:61], v[18:21]
	s_waitcnt lgkmcnt(0)
	v_mfma_f32_16x16x32_f16 v[26:29], v[82:85], v[38:41], v[26:29]
	v_mfma_f32_16x16x32_f16 v[14:17], v[86:89], v[38:41], v[14:17]
	ds_read_b128 v[38:41], v0
	ds_read_b128 v[50:53], v0 offset:2048
	ds_read_b128 v[54:57], v0 offset:4096
	ds_read_b128 v[58:61], v0 offset:6144
	ds_read_b128 v[62:65], v4 offset:16384
	ds_read_b128 v[70:73], v4 offset:18432
	v_mfma_f32_16x16x32_f16 v[66:69], v[82:85], v[46:49], v[66:69]
	v_mfma_f32_16x16x32_f16 v[22:25], v[86:89], v[46:49], v[22:25]
	v_mfma_f32_16x16x32_f16 v[42:45], v[82:85], v[74:77], v[42:45]
	v_mfma_f32_16x16x32_f16 v[34:37], v[86:89], v[74:77], v[34:37]
	v_mfma_f32_16x16x32_f16 v[10:13], v[82:85], v[78:81], v[10:13]
	v_mfma_f32_16x16x32_f16 v[18:21], v[86:89], v[78:81], v[18:21]
	s_add_u32 s20, s0, 0x500
	s_mov_b32 m0, s18
	s_waitcnt vmcnt(0) lgkmcnt(0)
	s_barrier
	s_addc_u32 s21, s1, 0
	s_add_u32 s22, s4, 0x500
	global_load_lds_dwordx4 v1, s[20:21]
	s_mov_b32 m0, s15
	s_addc_u32 s23, s5, 0
	global_load_lds_dwordx4 v2, s[20:21]
	s_mov_b32 m0, s16
	s_nop 0
	global_load_lds_dwordx4 v1, s[22:23]
	s_mov_b32 m0, s17
	s_nop 0
	global_load_lds_dwordx4 v2, s[22:23]
	s_waitcnt lgkmcnt(0)
	v_mfma_f32_16x16x32_f16 v[26:29], v[62:65], v[38:41], v[26:29]
	v_mfma_f32_16x16x32_f16 v[14:17], v[70:73], v[38:41], v[14:17]
	ds_read_b128 v[38:41], v5 offset:32768
	ds_read_b128 v[46:49], v5 offset:34816
	ds_read_b128 v[74:77], v5 offset:36864
	ds_read_b128 v[78:81], v5 offset:38912
	ds_read_b128 v[82:85], v3 offset:49152
	ds_read_b128 v[86:89], v3 offset:51200
	v_mfma_f32_16x16x32_f16 v[66:69], v[62:65], v[50:53], v[66:69]
	v_mfma_f32_16x16x32_f16 v[22:25], v[70:73], v[50:53], v[22:25]
	v_mfma_f32_16x16x32_f16 v[42:45], v[62:65], v[54:57], v[42:45]
	v_mfma_f32_16x16x32_f16 v[34:37], v[70:73], v[54:57], v[34:37]
	v_mfma_f32_16x16x32_f16 v[10:13], v[62:65], v[58:61], v[10:13]
	v_mfma_f32_16x16x32_f16 v[18:21], v[70:73], v[58:61], v[18:21]
	s_waitcnt lgkmcnt(0)
	v_mfma_f32_16x16x32_f16 v[26:29], v[82:85], v[38:41], v[26:29]
	v_mfma_f32_16x16x32_f16 v[14:17], v[86:89], v[38:41], v[14:17]
	ds_read_b128 v[38:41], v0 offset:32768
	ds_read_b128 v[50:53], v0 offset:34816
	ds_read_b128 v[54:57], v0 offset:36864
	ds_read_b128 v[58:61], v0 offset:38912
	ds_read_b128 v[62:65], v4 offset:49152
	ds_read_b128 v[70:73], v4 offset:51200
	v_mfma_f32_16x16x32_f16 v[66:69], v[82:85], v[46:49], v[66:69]
	v_mfma_f32_16x16x32_f16 v[22:25], v[86:89], v[46:49], v[22:25]
	v_mfma_f32_16x16x32_f16 v[42:45], v[82:85], v[74:77], v[42:45]
	v_mfma_f32_16x16x32_f16 v[34:37], v[86:89], v[74:77], v[34:37]
	v_mfma_f32_16x16x32_f16 v[10:13], v[82:85], v[78:81], v[10:13]
	v_mfma_f32_16x16x32_f16 v[18:21], v[86:89], v[78:81], v[18:21]
	s_add_u32 s20, s0, 0x580
	s_mov_b32 m0, s14
	s_waitcnt vmcnt(0) lgkmcnt(0)
	s_barrier
	s_addc_u32 s21, s1, 0
	s_add_u32 s22, s4, 0x580
	global_load_lds_dwordx4 v1, s[20:21]
	s_mov_b32 m0, s3
	s_addc_u32 s23, s5, 0
	global_load_lds_dwordx4 v2, s[20:21]
	s_mov_b32 m0, s6
	s_nop 0
	global_load_lds_dwordx4 v1, s[22:23]
	s_mov_b32 m0, s7
	s_nop 0
	global_load_lds_dwordx4 v2, s[22:23]
	s_waitcnt lgkmcnt(0)
	v_mfma_f32_16x16x32_f16 v[26:29], v[62:65], v[38:41], v[26:29]
	v_mfma_f32_16x16x32_f16 v[14:17], v[70:73], v[38:41], v[14:17]
	ds_read_b128 v[38:41], v5
	ds_read_b128 v[46:49], v5 offset:2048
	ds_read_b128 v[74:77], v5 offset:4096
	ds_read_b128 v[78:81], v5 offset:6144
	ds_read_b128 v[82:85], v3 offset:16384
	ds_read_b128 v[86:89], v3 offset:18432
	v_mfma_f32_16x16x32_f16 v[66:69], v[62:65], v[50:53], v[66:69]
	v_mfma_f32_16x16x32_f16 v[22:25], v[70:73], v[50:53], v[22:25]
	v_mfma_f32_16x16x32_f16 v[42:45], v[62:65], v[54:57], v[42:45]
	v_mfma_f32_16x16x32_f16 v[34:37], v[70:73], v[54:57], v[34:37]
	v_mfma_f32_16x16x32_f16 v[10:13], v[62:65], v[58:61], v[10:13]
	v_mfma_f32_16x16x32_f16 v[18:21], v[70:73], v[58:61], v[18:21]
	s_waitcnt lgkmcnt(0)
	v_mfma_f32_16x16x32_f16 v[26:29], v[82:85], v[38:41], v[26:29]
	v_mfma_f32_16x16x32_f16 v[14:17], v[86:89], v[38:41], v[14:17]
	ds_read_b128 v[38:41], v0
	ds_read_b128 v[50:53], v0 offset:2048
	ds_read_b128 v[54:57], v0 offset:4096
	ds_read_b128 v[58:61], v0 offset:6144
	ds_read_b128 v[62:65], v4 offset:16384
	ds_read_b128 v[70:73], v4 offset:18432
	v_mfma_f32_16x16x32_f16 v[66:69], v[82:85], v[46:49], v[66:69]
	v_mfma_f32_16x16x32_f16 v[22:25], v[86:89], v[46:49], v[22:25]
	v_mfma_f32_16x16x32_f16 v[42:45], v[82:85], v[74:77], v[42:45]
	v_mfma_f32_16x16x32_f16 v[34:37], v[86:89], v[74:77], v[34:37]
	v_mfma_f32_16x16x32_f16 v[10:13], v[82:85], v[78:81], v[10:13]
	v_mfma_f32_16x16x32_f16 v[18:21], v[86:89], v[78:81], v[18:21]
	s_add_u32 s20, s0, 0x600
	s_mov_b32 m0, s18
	s_waitcnt vmcnt(0) lgkmcnt(0)
	s_barrier
	s_addc_u32 s21, s1, 0
	s_add_u32 s22, s4, 0x600
	global_load_lds_dwordx4 v1, s[20:21]
	s_mov_b32 m0, s15
	s_addc_u32 s23, s5, 0
	global_load_lds_dwordx4 v2, s[20:21]
	s_mov_b32 m0, s16
	s_nop 0
	global_load_lds_dwordx4 v1, s[22:23]
	s_mov_b32 m0, s17
	s_nop 0
	global_load_lds_dwordx4 v2, s[22:23]
	s_waitcnt lgkmcnt(0)
	v_mfma_f32_16x16x32_f16 v[26:29], v[62:65], v[38:41], v[26:29]
	v_mfma_f32_16x16x32_f16 v[14:17], v[70:73], v[38:41], v[14:17]
	ds_read_b128 v[38:41], v5 offset:32768
	ds_read_b128 v[46:49], v5 offset:34816
	ds_read_b128 v[74:77], v5 offset:36864
	ds_read_b128 v[78:81], v5 offset:38912
	ds_read_b128 v[82:85], v3 offset:49152
	ds_read_b128 v[86:89], v3 offset:51200
	v_mfma_f32_16x16x32_f16 v[66:69], v[62:65], v[50:53], v[66:69]
	v_mfma_f32_16x16x32_f16 v[22:25], v[70:73], v[50:53], v[22:25]
	v_mfma_f32_16x16x32_f16 v[42:45], v[62:65], v[54:57], v[42:45]
	v_mfma_f32_16x16x32_f16 v[34:37], v[70:73], v[54:57], v[34:37]
	v_mfma_f32_16x16x32_f16 v[10:13], v[62:65], v[58:61], v[10:13]
	v_mfma_f32_16x16x32_f16 v[18:21], v[70:73], v[58:61], v[18:21]
	s_waitcnt lgkmcnt(0)
	v_mfma_f32_16x16x32_f16 v[26:29], v[82:85], v[38:41], v[26:29]
	v_mfma_f32_16x16x32_f16 v[14:17], v[86:89], v[38:41], v[14:17]
	ds_read_b128 v[38:41], v0 offset:32768
	ds_read_b128 v[50:53], v0 offset:34816
	ds_read_b128 v[54:57], v0 offset:36864
	ds_read_b128 v[58:61], v0 offset:38912
	ds_read_b128 v[62:65], v4 offset:49152
	ds_read_b128 v[70:73], v4 offset:51200
	v_mfma_f32_16x16x32_f16 v[66:69], v[82:85], v[46:49], v[66:69]
	v_mfma_f32_16x16x32_f16 v[22:25], v[86:89], v[46:49], v[22:25]
	v_mfma_f32_16x16x32_f16 v[42:45], v[82:85], v[74:77], v[42:45]
	v_mfma_f32_16x16x32_f16 v[34:37], v[86:89], v[74:77], v[34:37]
	v_mfma_f32_16x16x32_f16 v[10:13], v[82:85], v[78:81], v[10:13]
	v_mfma_f32_16x16x32_f16 v[18:21], v[86:89], v[78:81], v[18:21]
	s_add_u32 s20, s0, 0x680
	s_mov_b32 m0, s14
	s_waitcnt vmcnt(0) lgkmcnt(0)
	s_barrier
	s_addc_u32 s21, s1, 0
	s_add_u32 s22, s4, 0x680
	global_load_lds_dwordx4 v1, s[20:21]
	s_mov_b32 m0, s3
	s_addc_u32 s23, s5, 0
	global_load_lds_dwordx4 v2, s[20:21]
	s_mov_b32 m0, s6
	s_nop 0
	global_load_lds_dwordx4 v1, s[22:23]
	s_mov_b32 m0, s7
	s_nop 0
	global_load_lds_dwordx4 v2, s[22:23]
	s_waitcnt lgkmcnt(0)
	v_mfma_f32_16x16x32_f16 v[26:29], v[62:65], v[38:41], v[26:29]
	v_mfma_f32_16x16x32_f16 v[14:17], v[70:73], v[38:41], v[14:17]
	ds_read_b128 v[38:41], v5
	ds_read_b128 v[46:49], v5 offset:2048
	ds_read_b128 v[74:77], v5 offset:4096
	ds_read_b128 v[78:81], v5 offset:6144
	ds_read_b128 v[82:85], v3 offset:16384
	ds_read_b128 v[86:89], v3 offset:18432
	v_mfma_f32_16x16x32_f16 v[66:69], v[62:65], v[50:53], v[66:69]
	v_mfma_f32_16x16x32_f16 v[22:25], v[70:73], v[50:53], v[22:25]
	v_mfma_f32_16x16x32_f16 v[42:45], v[62:65], v[54:57], v[42:45]
	v_mfma_f32_16x16x32_f16 v[34:37], v[70:73], v[54:57], v[34:37]
	v_mfma_f32_16x16x32_f16 v[10:13], v[62:65], v[58:61], v[10:13]
	v_mfma_f32_16x16x32_f16 v[18:21], v[70:73], v[58:61], v[18:21]
	s_waitcnt lgkmcnt(0)
	v_mfma_f32_16x16x32_f16 v[26:29], v[82:85], v[38:41], v[26:29]
	v_mfma_f32_16x16x32_f16 v[14:17], v[86:89], v[38:41], v[14:17]
	ds_read_b128 v[38:41], v0
	ds_read_b128 v[50:53], v0 offset:2048
	ds_read_b128 v[54:57], v0 offset:4096
	ds_read_b128 v[58:61], v0 offset:6144
	ds_read_b128 v[62:65], v4 offset:16384
	ds_read_b128 v[70:73], v4 offset:18432
	v_mfma_f32_16x16x32_f16 v[66:69], v[82:85], v[46:49], v[66:69]
	v_mfma_f32_16x16x32_f16 v[22:25], v[86:89], v[46:49], v[22:25]
	v_mfma_f32_16x16x32_f16 v[42:45], v[82:85], v[74:77], v[42:45]
	v_mfma_f32_16x16x32_f16 v[34:37], v[86:89], v[74:77], v[34:37]
	v_mfma_f32_16x16x32_f16 v[10:13], v[82:85], v[78:81], v[10:13]
	v_mfma_f32_16x16x32_f16 v[18:21], v[86:89], v[78:81], v[18:21]
	s_mov_b32 m0, s18
	s_add_u32 s18, s0, 0x700
	s_waitcnt vmcnt(0) lgkmcnt(0)
	s_barrier
	s_addc_u32 s19, s1, 0
	s_add_u32 s20, s4, 0x700
	global_load_lds_dwordx4 v1, s[18:19]
	s_mov_b32 m0, s15
	s_addc_u32 s21, s5, 0
	global_load_lds_dwordx4 v2, s[18:19]
	s_mov_b32 m0, s16
	s_nop 0
	global_load_lds_dwordx4 v1, s[20:21]
	s_mov_b32 m0, s17
	s_nop 0
	global_load_lds_dwordx4 v2, s[20:21]
	s_waitcnt lgkmcnt(0)
	v_mfma_f32_16x16x32_f16 v[26:29], v[62:65], v[38:41], v[26:29]
	v_mfma_f32_16x16x32_f16 v[14:17], v[70:73], v[38:41], v[14:17]
	ds_read_b128 v[38:41], v5 offset:32768
	ds_read_b128 v[46:49], v5 offset:34816
	ds_read_b128 v[74:77], v5 offset:36864
	ds_read_b128 v[78:81], v5 offset:38912
	ds_read_b128 v[82:85], v3 offset:49152
	ds_read_b128 v[86:89], v3 offset:51200
	v_mfma_f32_16x16x32_f16 v[66:69], v[62:65], v[50:53], v[66:69]
	v_mfma_f32_16x16x32_f16 v[22:25], v[70:73], v[50:53], v[22:25]
	v_mfma_f32_16x16x32_f16 v[42:45], v[62:65], v[54:57], v[42:45]
	v_mfma_f32_16x16x32_f16 v[34:37], v[70:73], v[54:57], v[34:37]
	v_mfma_f32_16x16x32_f16 v[10:13], v[62:65], v[58:61], v[10:13]
	v_mfma_f32_16x16x32_f16 v[18:21], v[70:73], v[58:61], v[18:21]
	s_waitcnt lgkmcnt(0)
	v_mfma_f32_16x16x32_f16 v[26:29], v[82:85], v[38:41], v[26:29]
	v_mfma_f32_16x16x32_f16 v[14:17], v[86:89], v[38:41], v[14:17]
	ds_read_b128 v[38:41], v0 offset:32768
	ds_read_b128 v[50:53], v0 offset:34816
	ds_read_b128 v[54:57], v0 offset:36864
	ds_read_b128 v[58:61], v0 offset:38912
	ds_read_b128 v[62:65], v4 offset:49152
	ds_read_b128 v[70:73], v4 offset:51200
	v_mfma_f32_16x16x32_f16 v[66:69], v[82:85], v[46:49], v[66:69]
	v_mfma_f32_16x16x32_f16 v[22:25], v[86:89], v[46:49], v[22:25]
	v_mfma_f32_16x16x32_f16 v[42:45], v[82:85], v[74:77], v[42:45]
	v_mfma_f32_16x16x32_f16 v[34:37], v[86:89], v[74:77], v[34:37]
	v_mfma_f32_16x16x32_f16 v[10:13], v[82:85], v[78:81], v[10:13]
	v_mfma_f32_16x16x32_f16 v[18:21], v[86:89], v[78:81], v[18:21]
	s_add_u32 s0, s0, 0x780
	s_mov_b32 m0, s14
	s_waitcnt vmcnt(0) lgkmcnt(0)
	s_barrier
	s_addc_u32 s1, s1, 0
	s_add_u32 s4, s4, 0x780
	global_load_lds_dwordx4 v1, s[0:1]
	s_mov_b32 m0, s3
	s_addc_u32 s5, s5, 0
	global_load_lds_dwordx4 v2, s[0:1]
	s_mov_b32 m0, s6
	s_nop 0
	global_load_lds_dwordx4 v1, s[4:5]
	s_mov_b32 m0, s7
	s_nop 0
	global_load_lds_dwordx4 v2, s[4:5]
	s_waitcnt lgkmcnt(0)
	v_mfma_f32_16x16x32_f16 v[26:29], v[62:65], v[38:41], v[26:29]
	v_mfma_f32_16x16x32_f16 v[14:17], v[70:73], v[38:41], v[14:17]
	ds_read_b128 v[38:41], v5
	ds_read_b128 v[46:49], v5 offset:2048
	ds_read_b128 v[74:77], v5 offset:4096
	ds_read_b128 v[78:81], v5 offset:6144
	ds_read_b128 v[82:85], v3 offset:16384
	ds_read_b128 v[86:89], v3 offset:18432
	v_mfma_f32_16x16x32_f16 v[66:69], v[62:65], v[50:53], v[66:69]
	v_mfma_f32_16x16x32_f16 v[22:25], v[70:73], v[50:53], v[22:25]
	v_mfma_f32_16x16x32_f16 v[42:45], v[62:65], v[54:57], v[42:45]
	v_mfma_f32_16x16x32_f16 v[34:37], v[70:73], v[54:57], v[34:37]
	v_mfma_f32_16x16x32_f16 v[10:13], v[62:65], v[58:61], v[10:13]
	v_mfma_f32_16x16x32_f16 v[18:21], v[70:73], v[58:61], v[18:21]
	s_waitcnt lgkmcnt(0)
	v_mfma_f32_16x16x32_f16 v[26:29], v[82:85], v[38:41], v[26:29]
	v_mfma_f32_16x16x32_f16 v[14:17], v[86:89], v[38:41], v[14:17]
	ds_read_b128 v[38:41], v0
	ds_read_b128 v[50:53], v0 offset:2048
	ds_read_b128 v[54:57], v0 offset:4096
	ds_read_b128 v[58:61], v0 offset:6144
	ds_read_b128 v[62:65], v4 offset:16384
	ds_read_b128 v[70:73], v4 offset:18432
	v_mfma_f32_16x16x32_f16 v[66:69], v[82:85], v[46:49], v[66:69]
	v_mfma_f32_16x16x32_f16 v[22:25], v[86:89], v[46:49], v[22:25]
	v_mfma_f32_16x16x32_f16 v[42:45], v[82:85], v[74:77], v[42:45]
	v_mfma_f32_16x16x32_f16 v[34:37], v[86:89], v[74:77], v[34:37]
	v_mfma_f32_16x16x32_f16 v[10:13], v[82:85], v[78:81], v[10:13]
	v_mfma_f32_16x16x32_f16 v[18:21], v[86:89], v[78:81], v[18:21]
	s_waitcnt vmcnt(0) lgkmcnt(0)
	s_barrier
	s_waitcnt lgkmcnt(0)
	v_mfma_f32_16x16x32_f16 v[26:29], v[62:65], v[38:41], v[26:29]
	v_mfma_f32_16x16x32_f16 v[14:17], v[70:73], v[38:41], v[14:17]
	ds_read_b128 v[38:41], v5 offset:32768
	ds_read_b128 v[46:49], v5 offset:34816
	ds_read_b128 v[74:77], v5 offset:36864
	ds_read_b128 v[78:81], v5 offset:38912
	ds_read_b128 v[82:85], v3 offset:49152
	ds_read_b128 v[86:89], v3 offset:51200
	v_mfma_f32_16x16x32_f16 v[66:69], v[62:65], v[50:53], v[66:69]
	v_mfma_f32_16x16x32_f16 v[22:25], v[70:73], v[50:53], v[22:25]
	v_mfma_f32_16x16x32_f16 v[42:45], v[62:65], v[54:57], v[42:45]
	v_mfma_f32_16x16x32_f16 v[34:37], v[70:73], v[54:57], v[34:37]
	v_mfma_f32_16x16x32_f16 v[10:13], v[62:65], v[58:61], v[10:13]
	v_mfma_f32_16x16x32_f16 v[18:21], v[70:73], v[58:61], v[18:21]
	s_waitcnt lgkmcnt(0)
	v_mfma_f32_16x16x32_f16 v[26:29], v[82:85], v[38:41], v[26:29]
	v_mfma_f32_16x16x32_f16 v[14:17], v[86:89], v[38:41], v[14:17]
	ds_read_b128 v[38:41], v0 offset:32768
	ds_read_b128 v[50:53], v0 offset:34816
	ds_read_b128 v[54:57], v0 offset:36864
	ds_read_b128 v[0:3], v0 offset:38912
	ds_read_b128 v[58:61], v4 offset:49152
	ds_read_b128 v[62:65], v4 offset:51200
	v_mfma_f32_16x16x32_f16 v[4:7], v[82:85], v[46:49], v[66:69]
	v_mfma_f32_16x16x32_f16 v[22:25], v[86:89], v[46:49], v[22:25]
	v_mfma_f32_16x16x32_f16 v[42:45], v[82:85], v[74:77], v[42:45]
	v_mfma_f32_16x16x32_f16 v[34:37], v[86:89], v[74:77], v[34:37]
	v_mfma_f32_16x16x32_f16 v[10:13], v[82:85], v[78:81], v[10:13]
	v_mfma_f32_16x16x32_f16 v[46:49], v[86:89], v[78:81], v[18:21]
	s_waitcnt lgkmcnt(0)
	v_mfma_f32_16x16x32_f16 v[66:69], v[58:61], v[38:41], v[26:29]
	v_mfma_f32_16x16x32_f16 v[38:41], v[62:65], v[38:41], v[14:17]
	v_mfma_f32_16x16x32_f16 v[28:31], v[58:61], v[50:53], v[4:7]
	v_mfma_f32_16x16x32_f16 v[24:27], v[62:65], v[50:53], v[22:25]
	v_mfma_f32_16x16x32_f16 v[20:23], v[58:61], v[54:57], v[42:45]
	v_mfma_f32_16x16x32_f16 v[16:19], v[62:65], v[54:57], v[34:37]
	v_mfma_f32_16x16x32_f16 v[4:7], v[58:61], v[0:3], v[10:13]
	v_mfma_f32_16x16x32_f16 v[0:3], v[62:65], v[0:3], v[46:49]
	v_lshlrev_b32_e32 v9, 2, v9
	v_or3_b32 v34, v9, v8, s13
	v_mov_b32_e32 v35, 0
	v_lshl_add_u64 v[36:37], v[34:35], 2, s[10:11]
	global_load_dwordx4 v[8:11], v[36:37], off
	global_load_dwordx4 v[12:15], v[36:37], off offset:64
	v_or_b32_e32 v36, s12, v32
	v_mad_u64_u32 v[42:43], s[18:19], v36, s2, 0
	s_ashr_i32 s1, s2, 31
	s_mov_b32 s16, 0xbf3a00e3
	v_mov_b32_e32 v44, v43
	v_mov_b64_e32 v[32:33], s[16:17]
	v_mad_u64_u32 v[44:45], s[16:17], v36, s1, v[44:45]
	s_mov_b32 s14, 0x3e6d3388
	v_mov_b32_e32 v43, v44
	s_mov_b32 s10, 0x3f07dc22
	s_mov_b32 s6, 0xbf38aa3b
	s_mov_b32 s12, 0x3f35f0e3
	s_mov_b32 s0, 0xbe11a98e
	s_mov_b32 s4, 0x3e027906
	v_lshlrev_b64 v[34:35], 1, v[34:35]
	v_lshl_add_u64 v[42:43], v[42:43], 1, s[8:9]
	v_lshl_add_u64 v[42:43], v[42:43], 0, v[34:35]
	s_waitcnt vmcnt(0)
	v_pk_add_f32 v[46:47], v[66:67], v[8:9]
	v_pk_add_f32 v[44:45], v[68:69], v[10:11]
	v_and_b32_e32 v49, 0x7fffffff, v47
	v_and_b32_e32 v48, 0x7fffffff, v46
	v_and_b32_e32 v55, 0x7fffffff, v45
	v_and_b32_e32 v54, 0x7fffffff, v44
	v_pk_fma_f32 v[48:49], v[48:49], s[14:15], 1.0 op_sel_hi:[1,0,0]
	v_pk_add_f32 v[38:39], v[38:39], v[12:13]
	v_pk_fma_f32 v[54:55], v[54:55], s[14:15], 1.0 op_sel_hi:[1,0,0]
	v_rcp_f32_e32 v48, v48
	v_rcp_f32_e32 v49, v49
	v_and_b32_e32 v57, 0x7fffffff, v39
	v_and_b32_e32 v56, 0x7fffffff, v38
	v_rcp_f32_e32 v54, v54
	v_rcp_f32_e32 v55, v55
	v_pk_fma_f32 v[56:57], v[56:57], s[14:15], 1.0 op_sel_hi:[1,0,0]
	v_pk_mul_f32 v[52:53], v[46:47], v[46:47]
	v_rcp_f32_e32 v56, v56
	v_rcp_f32_e32 v57, v57
	v_pk_mul_f32 v[50:51], v[44:45], v[44:45]
	v_pk_mul_f32 v[52:53], v[52:53], s[6:7] op_sel_hi:[1,0]
	v_pk_fma_f32 v[64:65], v[48:49], s[10:11], v[32:33] op_sel_hi:[1,0,0]
	v_pk_mul_f32 v[50:51], v[50:51], s[6:7] op_sel_hi:[1,0]
	v_exp_f32_e32 v52, v52
	v_exp_f32_e32 v53, v53
	v_pk_fma_f32 v[66:67], v[54:55], s[10:11], v[32:33] op_sel_hi:[1,0,0]
	v_pk_fma_f32 v[64:65], v[48:49], v[64:65], s[12:13] op_sel_hi:[1,1,0]
	v_pk_mul_f32 v[60:61], v[38:39], v[38:39]
	v_exp_f32_e32 v50, v50
	v_exp_f32_e32 v51, v51
	v_pk_fma_f32 v[66:67], v[54:55], v[66:67], s[12:13] op_sel_hi:[1,1,0]
	v_pk_fma_f32 v[64:65], v[48:49], v[64:65], s[0:1] op_sel_hi:[1,1,0]
	v_pk_mul_f32 v[60:61], v[60:61], s[6:7] op_sel_hi:[1,0]
	v_pk_fma_f32 v[68:69], v[56:57], s[10:11], v[32:33] op_sel_hi:[1,0,0]
	v_pk_fma_f32 v[66:67], v[54:55], v[66:67], s[0:1] op_sel_hi:[1,1,0]
	v_pk_fma_f32 v[64:65], v[48:49], v[64:65], s[4:5] op_sel_hi:[1,1,0]
	v_exp_f32_e32 v60, v60
	v_exp_f32_e32 v61, v61
	v_pk_fma_f32 v[68:69], v[56:57], v[68:69], s[12:13] op_sel_hi:[1,1,0]
	v_pk_fma_f32 v[66:67], v[54:55], v[66:67], s[4:5] op_sel_hi:[1,1,0]
	v_pk_mul_f32 v[48:49], v[48:49], v[64:65]
	v_pk_add_f32 v[40:41], v[40:41], v[14:15]
	v_pk_fma_f32 v[68:69], v[56:57], v[68:69], s[0:1] op_sel_hi:[1,1,0]
	v_pk_mul_f32 v[54:55], v[54:55], v[66:67]
	v_pk_mul_f32 v[48:49], v[52:53], v[48:49]
	v_and_b32_e32 v63, 0x7fffffff, v41
	v_and_b32_e32 v62, 0x7fffffff, v40
	v_pk_fma_f32 v[68:69], v[56:57], v[68:69], s[4:5] op_sel_hi:[1,1,0]
	v_pk_mul_f32 v[50:51], v[50:51], v[54:55]
	v_pk_mul_f32 v[54:55], v[46:47], v[48:49]
	v_pk_fma_f32 v[48:49], v[46:47], v[48:49], v[46:47] neg_lo:[1,0,0] neg_hi:[1,0,0]
	v_cmp_gt_f32_e32 vcc, 0, v46
	v_pk_fma_f32 v[62:63], v[62:63], s[14:15], 1.0 op_sel_hi:[1,0,0]
	v_pk_mul_f32 v[56:57], v[56:57], v[68:69]
	v_cndmask_b32_e32 v37, v48, v54, vcc
	v_cmp_gt_f32_e32 vcc, 0, v47
	v_rcp_f32_e32 v62, v62
	v_rcp_f32_e32 v63, v63
	v_pk_mul_f32 v[52:53], v[60:61], v[56:57]
	v_pk_mul_f32 v[56:57], v[44:45], v[50:51]
	v_pk_fma_f32 v[50:51], v[44:45], v[50:51], v[44:45] neg_lo:[1,0,0] neg_hi:[1,0,0]
	v_cndmask_b32_e32 v46, v49, v55, vcc
	v_cmp_gt_f32_e32 vcc, 0, v44
	v_pk_mul_f32 v[58:59], v[40:41], v[40:41]
	v_pk_mul_f32 v[60:61], v[38:39], v[52:53]
	v_cndmask_b32_e32 v44, v50, v56, vcc
	v_cmp_gt_f32_e32 vcc, 0, v45
	v_pk_fma_f32 v[52:53], v[38:39], v[52:53], v[38:39] neg_lo:[1,0,0] neg_hi:[1,0,0]
	v_pk_add_f32 v[28:29], v[28:29], v[8:9]
	v_cndmask_b32_e32 v45, v51, v57, vcc
	v_cmp_gt_f32_e32 vcc, 0, v38
	v_cvt_pk_f16_f32 v45, v44, v45
	v_cvt_pk_f16_f32 v44, v37, v46
	v_cndmask_b32_e32 v47, v52, v60, vcc
	global_store_dwordx2 v[42:43], v[44:45], off
	v_cmp_gt_f32_e32 vcc, 0, v39
	v_pk_fma_f32 v[38:39], v[62:63], s[10:11], v[32:33] op_sel_hi:[1,0,0]
	v_pk_mul_f32 v[44:45], v[58:59], s[6:7] op_sel_hi:[1,0]
	v_pk_fma_f32 v[38:39], v[62:63], v[38:39], s[12:13] op_sel_hi:[1,1,0]
	v_exp_f32_e32 v44, v44
	v_exp_f32_e32 v45, v45
	v_pk_fma_f32 v[38:39], v[62:63], v[38:39], s[0:1] op_sel_hi:[1,1,0]
	v_cndmask_b32_e32 v37, v53, v61, vcc
	v_pk_fma_f32 v[38:39], v[62:63], v[38:39], s[4:5] op_sel_hi:[1,1,0]
	v_cmp_gt_f32_e32 vcc, 0, v40
	v_pk_mul_f32 v[38:39], v[62:63], v[38:39]
	v_pk_add_f32 v[30:31], v[30:31], v[10:11]
	v_pk_mul_f32 v[38:39], v[44:45], v[38:39]
	v_and_b32_e32 v46, 0x7fffffff, v30
	v_pk_mul_f32 v[44:45], v[40:41], v[38:39]
	v_pk_fma_f32 v[38:39], v[40:41], v[38:39], v[40:41] neg_lo:[1,0,0] neg_hi:[1,0,0]
	v_pk_add_f32 v[24:25], v[24:25], v[12:13]
	v_cndmask_b32_e32 v38, v38, v44, vcc
	v_cmp_gt_f32_e32 vcc, 0, v41
	v_pk_add_f32 v[26:27], v[26:27], v[14:15]
	v_pk_add_f32 v[20:21], v[20:21], v[8:9]
	v_cndmask_b32_e32 v39, v39, v45, vcc
	v_cvt_pk_f16_f32 v39, v38, v39
	v_cvt_pk_f16_f32 v38, v47, v37
	global_store_dwordx2 v[42:43], v[38:39], off offset:32
	v_and_b32_e32 v43, 0x7fffffff, v29
	v_and_b32_e32 v42, 0x7fffffff, v28
	v_pk_fma_f32 v[42:43], v[42:43], s[14:15], 1.0 op_sel_hi:[1,0,0]
	v_or_b32_e32 v37, 16, v36
	v_rcp_f32_e32 v42, v42
	v_rcp_f32_e32 v43, v43
	v_mad_u64_u32 v[38:39], s[16:17], v37, s2, 0
	v_mov_b32_e32 v40, v39
	v_mad_u64_u32 v[40:41], s[16:17], v37, s1, v[40:41]
	v_pk_mul_f32 v[44:45], v[28:29], v[28:29]
	v_mov_b32_e32 v39, v40
	v_pk_fma_f32 v[40:41], v[42:43], s[10:11], v[32:33] op_sel_hi:[1,0,0]
	v_pk_mul_f32 v[44:45], v[44:45], s[6:7] op_sel_hi:[1,0]
	v_pk_fma_f32 v[40:41], v[42:43], v[40:41], s[12:13] op_sel_hi:[1,1,0]
	v_exp_f32_e32 v44, v44
	v_exp_f32_e32 v45, v45
	v_pk_fma_f32 v[40:41], v[42:43], v[40:41], s[0:1] op_sel_hi:[1,1,0]
	v_and_b32_e32 v47, 0x7fffffff, v31
	v_pk_fma_f32 v[40:41], v[42:43], v[40:41], s[4:5] op_sel_hi:[1,1,0]
	v_pk_fma_f32 v[46:47], v[46:47], s[14:15], 1.0 op_sel_hi:[1,0,0]
	v_pk_mul_f32 v[40:41], v[42:43], v[40:41]
	v_rcp_f32_e32 v46, v46
	v_rcp_f32_e32 v47, v47
	v_pk_mul_f32 v[40:41], v[44:45], v[40:41]
	v_cmp_gt_f32_e32 vcc, 0, v28
	v_pk_mul_f32 v[44:45], v[28:29], v[40:41]
	v_pk_fma_f32 v[40:41], v[28:29], v[40:41], v[28:29] neg_lo:[1,0,0] neg_hi:[1,0,0]
	v_pk_mul_f32 v[42:43], v[30:31], v[30:31]
	v_cndmask_b32_e32 v37, v40, v44, vcc
	v_cmp_gt_f32_e32 vcc, 0, v29
	v_pk_fma_f32 v[28:29], v[46:47], s[10:11], v[32:33] op_sel_hi:[1,0,0]
	v_lshl_add_u64 v[38:39], v[38:39], 1, s[8:9]
	v_cndmask_b32_e32 v44, v41, v45, vcc
	v_pk_mul_f32 v[40:41], v[42:43], s[6:7] op_sel_hi:[1,0]
	v_pk_fma_f32 v[28:29], v[46:47], v[28:29], s[12:13] op_sel_hi:[1,1,0]
	v_exp_f32_e32 v40, v40
	v_exp_f32_e32 v41, v41
	v_pk_fma_f32 v[28:29], v[46:47], v[28:29], s[0:1] op_sel_hi:[1,1,0]
	v_cmp_gt_f32_e32 vcc, 0, v30
	v_pk_fma_f32 v[28:29], v[46:47], v[28:29], s[4:5] op_sel_hi:[1,1,0]
	v_lshl_add_u64 v[38:39], v[38:39], 0, v[34:35]
	v_pk_mul_f32 v[28:29], v[46:47], v[28:29]
	v_and_b32_e32 v43, 0x7fffffff, v27
	v_pk_mul_f32 v[28:29], v[40:41], v[28:29]
	v_and_b32_e32 v42, 0x7fffffff, v26
	v_pk_mul_f32 v[40:41], v[30:31], v[28:29]
	v_pk_fma_f32 v[28:29], v[30:31], v[28:29], v[30:31] neg_lo:[1,0,0] neg_hi:[1,0,0]
	v_and_b32_e32 v30, 0x7fffffff, v24
	v_cndmask_b32_e32 v28, v28, v40, vcc
	v_cmp_gt_f32_e32 vcc, 0, v31
	v_and_b32_e32 v31, 0x7fffffff, v25
	v_pk_fma_f32 v[30:31], v[30:31], s[14:15], 1.0 op_sel_hi:[1,0,0]
	v_cndmask_b32_e32 v29, v29, v41, vcc
	v_rcp_f32_e32 v30, v30
	v_rcp_f32_e32 v31, v31
	v_cvt_pk_f16_f32 v29, v28, v29
	v_cvt_pk_f16_f32 v28, v37, v44
	v_pk_mul_f32 v[40:41], v[24:25], v[24:25]
	global_store_dwordx2 v[38:39], v[28:29], off
	v_pk_fma_f32 v[28:29], v[30:31], s[10:11], v[32:33] op_sel_hi:[1,0,0]
	v_pk_mul_f32 v[40:41], v[40:41], s[6:7] op_sel_hi:[1,0]
	v_pk_fma_f32 v[28:29], v[30:31], v[28:29], s[12:13] op_sel_hi:[1,1,0]
	v_exp_f32_e32 v40, v40
	v_exp_f32_e32 v41, v41
	v_pk_fma_f32 v[28:29], v[30:31], v[28:29], s[0:1] op_sel_hi:[1,1,0]
	v_pk_fma_f32 v[42:43], v[42:43], s[14:15], 1.0 op_sel_hi:[1,0,0]
	v_pk_fma_f32 v[28:29], v[30:31], v[28:29], s[4:5] op_sel_hi:[1,1,0]
	v_rcp_f32_e32 v42, v42
	v_pk_mul_f32 v[28:29], v[30:31], v[28:29]
	v_rcp_f32_e32 v43, v43
	v_pk_mul_f32 v[28:29], v[40:41], v[28:29]
	v_cmp_gt_f32_e32 vcc, 0, v24
	v_pk_mul_f32 v[40:41], v[24:25], v[28:29]
	v_pk_fma_f32 v[28:29], v[24:25], v[28:29], v[24:25] neg_lo:[1,0,0] neg_hi:[1,0,0]
	v_pk_mul_f32 v[30:31], v[26:27], v[26:27]
	v_cndmask_b32_e32 v37, v28, v40, vcc
	v_cmp_gt_f32_e32 vcc, 0, v25
	v_pk_fma_f32 v[24:25], v[42:43], s[10:11], v[32:33] op_sel_hi:[1,0,0]
	v_pk_add_f32 v[22:23], v[22:23], v[10:11]
	v_cndmask_b32_e32 v40, v29, v41, vcc
	v_pk_mul_f32 v[28:29], v[30:31], s[6:7] op_sel_hi:[1,0]
	v_pk_fma_f32 v[24:25], v[42:43], v[24:25], s[12:13] op_sel_hi:[1,1,0]
	v_exp_f32_e32 v28, v28
	v_exp_f32_e32 v29, v29
	v_pk_fma_f32 v[24:25], v[42:43], v[24:25], s[0:1] op_sel_hi:[1,1,0]
	v_cmp_gt_f32_e32 vcc, 0, v26
	v_pk_fma_f32 v[24:25], v[42:43], v[24:25], s[4:5] op_sel_hi:[1,1,0]
	v_pk_mul_f32 v[30:31], v[20:21], v[20:21]
	v_pk_mul_f32 v[24:25], v[42:43], v[24:25]
	v_pk_mul_f32 v[30:31], v[30:31], s[6:7] op_sel_hi:[1,0]
	v_pk_mul_f32 v[24:25], v[28:29], v[24:25]
	v_exp_f32_e32 v30, v30
	v_pk_mul_f32 v[28:29], v[26:27], v[24:25]
	v_pk_fma_f32 v[24:25], v[26:27], v[24:25], v[26:27] neg_lo:[1,0,0] neg_hi:[1,0,0]
	v_exp_f32_e32 v31, v31
	v_cndmask_b32_e32 v24, v24, v28, vcc
	v_cmp_gt_f32_e32 vcc, 0, v27
	v_and_b32_e32 v28, 0x7fffffff, v20
	v_or_b32_e32 v27, 32, v36
	v_cndmask_b32_e32 v25, v25, v29, vcc
	v_and_b32_e32 v29, 0x7fffffff, v21
	v_pk_fma_f32 v[28:29], v[28:29], s[14:15], 1.0 op_sel_hi:[1,0,0]
	v_cvt_pk_f16_f32 v25, v24, v25
	v_cvt_pk_f16_f32 v24, v37, v40
	v_rcp_f32_e32 v28, v28
	v_rcp_f32_e32 v29, v29
	global_store_dwordx2 v[38:39], v[24:25], off offset:32
	v_mad_u64_u32 v[24:25], s[16:17], v27, s2, 0
	v_mov_b32_e32 v26, v25
	v_mad_u64_u32 v[26:27], s[16:17], v27, s1, v[26:27]
	v_mov_b32_e32 v25, v26
	v_pk_fma_f32 v[26:27], v[28:29], s[10:11], v[32:33] op_sel_hi:[1,0,0]
	v_and_b32_e32 v39, 0x7fffffff, v23
	v_pk_fma_f32 v[26:27], v[28:29], v[26:27], s[12:13] op_sel_hi:[1,1,0]
	v_and_b32_e32 v38, 0x7fffffff, v22
	v_pk_fma_f32 v[26:27], v[28:29], v[26:27], s[0:1] op_sel_hi:[1,1,0]
	v_pk_fma_f32 v[38:39], v[38:39], s[14:15], 1.0 op_sel_hi:[1,0,0]
	v_pk_fma_f32 v[26:27], v[28:29], v[26:27], s[4:5] op_sel_hi:[1,1,0]
	v_rcp_f32_e32 v38, v38
	v_pk_mul_f32 v[26:27], v[28:29], v[26:27]
	v_rcp_f32_e32 v39, v39
	v_pk_mul_f32 v[26:27], v[30:31], v[26:27]
	v_cmp_gt_f32_e32 vcc, 0, v20
	v_pk_mul_f32 v[30:31], v[20:21], v[26:27]
	v_pk_fma_f32 v[26:27], v[20:21], v[26:27], v[20:21] neg_lo:[1,0,0] neg_hi:[1,0,0]
	v_pk_mul_f32 v[28:29], v[22:23], v[22:23]
	v_cndmask_b32_e32 v30, v26, v30, vcc
	v_cmp_gt_f32_e32 vcc, 0, v21
	v_pk_fma_f32 v[20:21], v[38:39], s[10:11], v[32:33] op_sel_hi:[1,0,0]
	v_pk_add_f32 v[16:17], v[16:17], v[12:13]
	v_cndmask_b32_e32 v31, v27, v31, vcc
	v_pk_mul_f32 v[26:27], v[28:29], s[6:7] op_sel_hi:[1,0]
	v_pk_fma_f32 v[20:21], v[38:39], v[20:21], s[12:13] op_sel_hi:[1,1,0]
	v_exp_f32_e32 v26, v26
	v_exp_f32_e32 v27, v27
	v_pk_fma_f32 v[20:21], v[38:39], v[20:21], s[0:1] op_sel_hi:[1,1,0]
	v_cmp_gt_f32_e32 vcc, 0, v22
	v_pk_fma_f32 v[20:21], v[38:39], v[20:21], s[4:5] op_sel_hi:[1,1,0]
	v_lshl_add_u64 v[24:25], v[24:25], 1, s[8:9]
	v_pk_mul_f32 v[20:21], v[38:39], v[20:21]
	v_lshl_add_u64 v[24:25], v[24:25], 0, v[34:35]
	v_pk_mul_f32 v[20:21], v[26:27], v[20:21]
	v_pk_add_f32 v[18:19], v[18:19], v[14:15]
	v_pk_mul_f32 v[26:27], v[22:23], v[20:21]
	v_pk_fma_f32 v[20:21], v[22:23], v[20:21], v[22:23] neg_lo:[1,0,0] neg_hi:[1,0,0]
	v_and_b32_e32 v22, 0x7fffffff, v16
	v_cndmask_b32_e32 v20, v20, v26, vcc
	v_cmp_gt_f32_e32 vcc, 0, v23
	v_and_b32_e32 v23, 0x7fffffff, v17
	v_pk_fma_f32 v[22:23], v[22:23], s[14:15], 1.0 op_sel_hi:[1,0,0]
	v_cndmask_b32_e32 v21, v21, v27, vcc
	v_rcp_f32_e32 v22, v22
	v_rcp_f32_e32 v23, v23
	v_cvt_pk_f16_f32 v21, v20, v21
	v_cvt_pk_f16_f32 v20, v30, v31
	v_pk_mul_f32 v[26:27], v[16:17], v[16:17]
	global_store_dwordx2 v[24:25], v[20:21], off
	v_pk_fma_f32 v[20:21], v[22:23], s[10:11], v[32:33] op_sel_hi:[1,0,0]
	v_pk_mul_f32 v[26:27], v[26:27], s[6:7] op_sel_hi:[1,0]
	v_pk_fma_f32 v[20:21], v[22:23], v[20:21], s[12:13] op_sel_hi:[1,1,0]
	v_exp_f32_e32 v26, v26
	v_exp_f32_e32 v27, v27
	v_pk_fma_f32 v[20:21], v[22:23], v[20:21], s[0:1] op_sel_hi:[1,1,0]
	v_and_b32_e32 v29, 0x7fffffff, v19
	v_and_b32_e32 v28, 0x7fffffff, v18
	v_pk_fma_f32 v[20:21], v[22:23], v[20:21], s[4:5] op_sel_hi:[1,1,0]
	v_pk_fma_f32 v[28:29], v[28:29], s[14:15], 1.0 op_sel_hi:[1,0,0]
	v_pk_mul_f32 v[20:21], v[22:23], v[20:21]
	v_rcp_f32_e32 v28, v28
	v_rcp_f32_e32 v29, v29
	v_pk_mul_f32 v[20:21], v[26:27], v[20:21]
	v_cmp_gt_f32_e32 vcc, 0, v16
	v_pk_mul_f32 v[26:27], v[16:17], v[20:21]
	v_pk_fma_f32 v[20:21], v[16:17], v[20:21], v[16:17] neg_lo:[1,0,0] neg_hi:[1,0,0]
	v_pk_mul_f32 v[22:23], v[18:19], v[18:19]
	v_cndmask_b32_e32 v26, v20, v26, vcc
	v_cmp_gt_f32_e32 vcc, 0, v17
	v_pk_fma_f32 v[16:17], v[28:29], s[10:11], v[32:33] op_sel_hi:[1,0,0]
	v_pk_add_f32 v[4:5], v[4:5], v[8:9]
	v_cndmask_b32_e32 v27, v21, v27, vcc
	v_pk_mul_f32 v[20:21], v[22:23], s[6:7] op_sel_hi:[1,0]
	v_pk_fma_f32 v[16:17], v[28:29], v[16:17], s[12:13] op_sel_hi:[1,1,0]
	v_exp_f32_e32 v20, v20
	v_exp_f32_e32 v21, v21
	v_pk_fma_f32 v[16:17], v[28:29], v[16:17], s[0:1] op_sel_hi:[1,1,0]
	v_cmp_gt_f32_e32 vcc, 0, v18
	v_pk_fma_f32 v[16:17], v[28:29], v[16:17], s[4:5] op_sel_hi:[1,1,0]
	v_and_b32_e32 v9, 0x7fffffff, v5
	v_pk_mul_f32 v[16:17], v[28:29], v[16:17]
	v_and_b32_e32 v8, 0x7fffffff, v4
	v_pk_mul_f32 v[16:17], v[20:21], v[16:17]
	v_pk_fma_f32 v[8:9], v[8:9], s[14:15], 1.0 op_sel_hi:[1,0,0]
	v_pk_mul_f32 v[20:21], v[18:19], v[16:17]
	v_pk_fma_f32 v[16:17], v[18:19], v[16:17], v[18:19] neg_lo:[1,0,0] neg_hi:[1,0,0]
	v_rcp_f32_e32 v8, v8
	v_cndmask_b32_e32 v16, v16, v20, vcc
	v_cmp_gt_f32_e32 vcc, 0, v19
	v_or_b32_e32 v19, 48, v36
	v_rcp_f32_e32 v9, v9
	v_cndmask_b32_e32 v17, v17, v21, vcc
	v_cvt_pk_f16_f32 v17, v16, v17
	v_cvt_pk_f16_f32 v16, v26, v27
	global_store_dwordx2 v[24:25], v[16:17], off offset:32
	v_mad_u64_u32 v[16:17], s[2:3], v19, s2, 0
	v_mov_b32_e32 v18, v17
	v_mad_u64_u32 v[18:19], s[2:3], v19, s1, v[18:19]
	v_mov_b32_e32 v17, v18
	v_pk_mul_f32 v[18:19], v[4:5], v[4:5]
	v_pk_add_f32 v[6:7], v[6:7], v[10:11]
	v_pk_fma_f32 v[10:11], v[8:9], s[10:11], v[32:33] op_sel_hi:[1,0,0]
	v_pk_mul_f32 v[18:19], v[18:19], s[6:7] op_sel_hi:[1,0]
	v_pk_fma_f32 v[10:11], v[8:9], v[10:11], s[12:13] op_sel_hi:[1,1,0]
	v_exp_f32_e32 v18, v18
	v_exp_f32_e32 v19, v19
	v_pk_fma_f32 v[10:11], v[8:9], v[10:11], s[0:1] op_sel_hi:[1,1,0]
	v_and_b32_e32 v21, 0x7fffffff, v7
	v_and_b32_e32 v20, 0x7fffffff, v6
	v_pk_fma_f32 v[10:11], v[8:9], v[10:11], s[4:5] op_sel_hi:[1,1,0]
	v_pk_fma_f32 v[20:21], v[20:21], s[14:15], 1.0 op_sel_hi:[1,0,0]
	v_pk_mul_f32 v[8:9], v[8:9], v[10:11]
	v_rcp_f32_e32 v20, v20
	v_rcp_f32_e32 v21, v21
	v_pk_mul_f32 v[8:9], v[18:19], v[8:9]
	v_cmp_gt_f32_e32 vcc, 0, v4
	v_pk_mul_f32 v[18:19], v[4:5], v[8:9]
	v_pk_fma_f32 v[8:9], v[4:5], v[8:9], v[4:5] neg_lo:[1,0,0] neg_hi:[1,0,0]
	v_pk_mul_f32 v[10:11], v[6:7], v[6:7]
	v_cndmask_b32_e32 v18, v8, v18, vcc
	v_cmp_gt_f32_e32 vcc, 0, v5
	v_pk_fma_f32 v[4:5], v[20:21], s[10:11], v[32:33] op_sel_hi:[1,0,0]
	v_pk_add_f32 v[0:1], v[0:1], v[12:13]
	v_cndmask_b32_e32 v19, v9, v19, vcc
	v_pk_mul_f32 v[8:9], v[10:11], s[6:7] op_sel_hi:[1,0]
	v_pk_fma_f32 v[4:5], v[20:21], v[4:5], s[12:13] op_sel_hi:[1,1,0]
	v_exp_f32_e32 v8, v8
	v_exp_f32_e32 v9, v9
	v_pk_fma_f32 v[4:5], v[20:21], v[4:5], s[0:1] op_sel_hi:[1,1,0]
	v_cmp_gt_f32_e32 vcc, 0, v6
	v_pk_fma_f32 v[4:5], v[20:21], v[4:5], s[4:5] op_sel_hi:[1,1,0]
	v_lshl_add_u64 v[16:17], v[16:17], 1, s[8:9]
	v_pk_mul_f32 v[4:5], v[20:21], v[4:5]
	v_pk_mul_f32 v[10:11], v[0:1], v[0:1]
	v_pk_mul_f32 v[4:5], v[8:9], v[4:5]
	v_pk_mul_f32 v[10:11], v[10:11], s[6:7] op_sel_hi:[1,0]
	v_pk_mul_f32 v[8:9], v[6:7], v[4:5]
	v_pk_fma_f32 v[4:5], v[6:7], v[4:5], v[6:7] neg_lo:[1,0,0] neg_hi:[1,0,0]
	v_and_b32_e32 v6, 0x7fffffff, v0
	v_cndmask_b32_e32 v4, v4, v8, vcc
	v_cmp_gt_f32_e32 vcc, 0, v7
	v_and_b32_e32 v7, 0x7fffffff, v1
	v_pk_fma_f32 v[6:7], v[6:7], s[14:15], 1.0 op_sel_hi:[1,0,0]
	v_cndmask_b32_e32 v5, v5, v9, vcc
	v_rcp_f32_e32 v6, v6
	v_rcp_f32_e32 v7, v7
	v_cvt_pk_f16_f32 v5, v4, v5
	v_cvt_pk_f16_f32 v4, v18, v19
	v_lshl_add_u64 v[8:9], v[16:17], 0, v[34:35]
	global_store_dwordx2 v[8:9], v[4:5], off
	v_pk_fma_f32 v[4:5], v[6:7], s[10:11], v[32:33] op_sel_hi:[1,0,0]
	v_pk_add_f32 v[2:3], v[2:3], v[14:15]
	v_pk_fma_f32 v[4:5], v[6:7], v[4:5], s[12:13] op_sel_hi:[1,1,0]
	v_exp_f32_e32 v10, v10
	v_exp_f32_e32 v11, v11
	v_pk_fma_f32 v[4:5], v[6:7], v[4:5], s[0:1] op_sel_hi:[1,1,0]
	v_and_b32_e32 v13, 0x7fffffff, v3
	v_and_b32_e32 v12, 0x7fffffff, v2
	v_pk_fma_f32 v[4:5], v[6:7], v[4:5], s[4:5] op_sel_hi:[1,1,0]
	v_pk_fma_f32 v[12:13], v[12:13], s[14:15], 1.0 op_sel_hi:[1,0,0]
	v_pk_mul_f32 v[4:5], v[6:7], v[4:5]
	v_rcp_f32_e32 v12, v12
	v_rcp_f32_e32 v13, v13
	v_pk_mul_f32 v[4:5], v[10:11], v[4:5]
	v_cmp_gt_f32_e32 vcc, 0, v0
	v_pk_mul_f32 v[10:11], v[0:1], v[4:5]
	v_pk_fma_f32 v[4:5], v[0:1], v[4:5], v[0:1] neg_lo:[1,0,0] neg_hi:[1,0,0]
	v_pk_mul_f32 v[6:7], v[2:3], v[2:3]
	v_cndmask_b32_e32 v10, v4, v10, vcc
	v_cmp_gt_f32_e32 vcc, 0, v1
	v_pk_fma_f32 v[0:1], v[12:13], s[10:11], v[32:33] op_sel_hi:[1,0,0]
	s_nop 0
	v_cndmask_b32_e32 v11, v5, v11, vcc
	v_pk_mul_f32 v[4:5], v[6:7], s[6:7] op_sel_hi:[1,0]
	v_pk_fma_f32 v[0:1], v[12:13], v[0:1], s[12:13] op_sel_hi:[1,1,0]
	v_exp_f32_e32 v4, v4
	v_exp_f32_e32 v5, v5
	v_pk_fma_f32 v[0:1], v[12:13], v[0:1], s[0:1] op_sel_hi:[1,1,0]
	v_cmp_gt_f32_e32 vcc, 0, v2
	v_pk_fma_f32 v[0:1], v[12:13], v[0:1], s[4:5] op_sel_hi:[1,1,0]
	s_nop 0
	v_pk_mul_f32 v[0:1], v[12:13], v[0:1]
	s_nop 0
	v_pk_mul_f32 v[0:1], v[4:5], v[0:1]
	s_nop 0
	v_pk_mul_f32 v[4:5], v[2:3], v[0:1]
	v_pk_fma_f32 v[0:1], v[2:3], v[0:1], v[2:3] neg_lo:[1,0,0] neg_hi:[1,0,0]
	s_nop 0
	v_cndmask_b32_e32 v0, v0, v4, vcc
	v_cmp_gt_f32_e32 vcc, 0, v3
	s_nop 1
	v_cndmask_b32_e32 v1, v1, v5, vcc
	v_cvt_pk_f16_f32 v1, v0, v1
	v_cvt_pk_f16_f32 v0, v10, v11
	global_store_dwordx2 v[8:9], v[0:1], off offset:32
	s_endpgm
	s_endpgm
	s_endpgm
	s_endpgm
	s_endpgm
	s_endpgm
	s_endpgm
	s_endpgm
	s_endpgm
	s_endpgm
	s_endpgm
	s_endpgm
	s_endpgm
	s_endpgm
	s_endpgm
	s_endpgm
	.section	.rodata,"a",@progbits
	.p2align	6, 0x0
	.amdhsa_kernel _Z5gemm8ILi128ELi2ELi2ELi2ELi1ELi16EEvPKDF16_S1_iiiPDF16_PfPKf
		.amdhsa_group_segment_fixed_size 0
		.amdhsa_private_segment_fixed_size 0
		.amdhsa_kernarg_size 312
		.amdhsa_user_sgpr_count 2
		.amdhsa_user_sgpr_dispatch_ptr 0
		.amdhsa_user_sgpr_queue_ptr 0
		.amdhsa_user_sgpr_kernarg_segment_ptr 1
		.amdhsa_user_sgpr_dispatch_id 0
		.amdhsa_user_sgpr_kernarg_preload_length 0
		.amdhsa_user_sgpr_kernarg_preload_offset 0
		.amdhsa_user_sgpr_private_segment_size 0
		.amdhsa_uses_dynamic_stack 0
		.amdhsa_enable_private_segment 0
		.amdhsa_system_sgpr_workgroup_id_x 1
		.amdhsa_system_sgpr_workgroup_id_y 0
		.amdhsa_system_sgpr_workgroup_id_z 0
		.amdhsa_system_sgpr_workgroup_info 0
		.amdhsa_system_vgpr_workitem_id 0
		.amdhsa_next_free_vgpr 90
		.amdhsa_next_free_sgpr 28
		.amdhsa_accum_offset 92
		.amdhsa_reserve_vcc 1
		.amdhsa_float_round_mode_32 0
		.amdhsa_float_round_mode_16_64 0
		.amdhsa_float_denorm_mode_32 3
		.amdhsa_float_denorm_mode_16_64 3
		.amdhsa_dx10_clamp 1
		.amdhsa_ieee_mode 1
		.amdhsa_fp16_overflow 0
		.amdhsa_tg_split 0
		.amdhsa_exception_fp_ieee_invalid_op 0
		.amdhsa_exception_fp_denorm_src 0
		.amdhsa_exception_fp_ieee_div_zero 0
		.amdhsa_exception_fp_ieee_overflow 0
		.amdhsa_exception_fp_ieee_underflow 0
		.amdhsa_exception_fp_ieee_inexact 0
		.amdhsa_exception_int_div_zero 0
	.end_amdhsa_kernel

_Z5gemm8ILi64ELi4ELi6ELi1ELi1ELi16EEvPKDF16_S1_iiiPDF16_PfPKf:
	v_readfirstlane_b32 s28, v0
	s_nop 3
	s_bitcmp1_b32 s28, 8
	s_cbranch_scc0 .Lprio_skip2
	s_setprio 1
.Lprio_skip2:
	s_load_dword s10, s[0:1], 0x38
	s_load_dwordx4 s[4:7], s[0:1], 0x0
	s_load_dwordx2 s[8:9], s[0:1], 0x28
	s_and_b32 s3, s2, 7
	s_waitcnt lgkmcnt(0)
	s_cmpk_lg_i32 s10, 0x200
	s_cbranch_scc0 .LBB6_2
	s_lshl_b32 s10, s3, 1
	s_and_b32 s10, s10, 12
	s_bfe_u32 s11, s2, 0x20003
	s_or_b32 s14, s10, s11
	s_lshl_b32 s10, s2, 3
	s_and_b32 s10, s10, 8
	s_lshr_b32 s11, s2, 5
	s_add_i32 s15, s10, s11
	s_load_dwordx2 s[10:11], s[0:1], 0x30
	s_cbranch_execz .LBB6_3
	s_branch .LBB6_4

.LBB6_4:
	s_load_dwordx2 s[2:3], s[0:1], 0x14
	s_lshl_b32 s12, s15, 7
	s_lshl_b32 s13, s14, 6
	v_lshrrev_b32_e32 v2, 4, v0
	v_xor_b32_e32 v1, v2, v0
	s_waitcnt lgkmcnt(0)
	v_and_b32_e32 v76, 15, v0
	v_lshrrev_b32_e32 v77, 7, v0
	v_lshl_or_b32 v76, v77, 5, v76
	v_or_b32_e32 v76, s12, v76
	v_bfe_u32 v77, v0, 4, 2
	v_bfe_u32 v78, v0, 6, 1
	v_lshlrev_b32_e32 v77, 2, v77
	v_lshl_or_b32 v77, v78, 5, v77
	v_or_b32_e32 v77, s13, v77
	v_mul_lo_u32 v78, v76, s2
	s_lshl_b32 s22, s2, 6
	v_add_lshl_u32 v78, v78, v77, 2
	v_lshlrev_b32_e32 v77, 2, v77
	v_add_u32_e32 v79, s22, v78
	global_load_dwordx4 v[80:83], v78, s[8:9]
	global_load_dwordx4 v[84:87], v78, s[8:9] offset:64
	global_load_dwordx4 v[88:91], v77, s[10:11]
	global_load_dwordx4 v[92:95], v77, s[10:11] offset:64
	global_load_dwordx4 v[96:99], v79, s[8:9]
	global_load_dwordx4 v[100:103], v79, s[8:9] offset:64
	s_ashr_i32 s14, s3, 31
	s_mul_i32 s0, s12, s14
	s_mul_hi_u32 s1, s12, s3
	s_add_i32 s1, s1, s0
	s_mul_i32 s0, s12, s3
	v_or_b32_e32 v4, 0x200, v0
	s_lshl_b64 s[0:1], s[0:1], 1
	v_lshlrev_b32_e32 v1, 3, v1
	v_lshrrev_b32_e32 v3, 3, v0
	v_lshrrev_b32_e32 v4, 3, v4
	s_add_u32 s0, s4, s0
	v_and_b32_e32 v1, 56, v1
	v_mul_lo_u32 v3, v3, s3
	v_mul_lo_u32 v4, v4, s3
	s_addc_u32 s1, s5, s1
	s_mul_i32 s4, s13, s14
	s_mul_hi_u32 s5, s13, s3
	v_lshlrev_b32_e32 v54, 4, v0
	v_add_lshl_u32 v3, v3, v1, 1
	v_add_lshl_u32 v4, v4, v1, 1
	s_add_i32 s5, s5, s4
	s_mul_i32 s4, s13, s3
	v_add_u32_e32 v1, 0, v54
	s_lshl_b64 s[4:5], s[4:5], 1
	v_readfirstlane_b32 s19, v1
	v_add_u32_e32 v5, 0x2000, v1
	s_add_u32 s4, s6, s4
	s_mov_b32 m0, s19
	v_readfirstlane_b32 s17, v5
	v_add_u32_e32 v5, 0x4000, v1
	s_addc_u32 s5, s7, s5
	global_load_lds_dwordx4 v3, s[0:1]
	s_mov_b32 m0, s17
	v_readfirstlane_b32 s18, v5
	v_add_u32_e32 v5, 0x6000, v1
	global_load_lds_dwordx4 v4, s[0:1]
	s_mov_b32 m0, s18
	s_add_u32 s6, s0, 0x80
	v_readfirstlane_b32 s16, v5
	v_add_u32_e32 v5, 0x8000, v1
	global_load_lds_dwordx4 v3, s[4:5]
	s_addc_u32 s7, s1, 0
	s_mov_b32 m0, s16
	v_readfirstlane_b32 s14, v5
	v_add_u32_e32 v5, 0xa000, v1
	s_add_u32 s20, s4, 0x80
	global_load_lds_dwordx4 v3, s[6:7]
	s_mov_b32 m0, s14
	v_readfirstlane_b32 s15, v5
	s_addc_u32 s21, s5, 0
	global_load_lds_dwordx4 v4, s[6:7]
	s_mov_b32 m0, s15
	v_add_u32_e32 v5, 0xc000, v1
	global_load_lds_dwordx4 v3, s[20:21]
	s_add_u32 s20, s0, 0x100
	s_addc_u32 s21, s1, 0
	v_readfirstlane_b32 s7, v5
	v_add_u32_e32 v5, 0xe000, v1
	s_add_u32 s22, s4, 0x100
	s_mov_b32 m0, s7
	v_readfirstlane_b32 s3, v5
	v_add_u32_e32 v5, 0x10000, v1
	s_addc_u32 s23, s5, 0
	global_load_lds_dwordx4 v3, s[20:21]
	s_mov_b32 m0, s3
	v_readfirstlane_b32 s6, v5
	v_add_u32_e32 v5, 0x12000, v1
	global_load_lds_dwordx4 v4, s[20:21]
	s_mov_b32 m0, s6
	s_add_u32 s20, s0, 0x180
	v_readfirstlane_b32 s24, v5
	v_add_u32_e32 v5, 0x14000, v1
	global_load_lds_dwordx4 v3, s[22:23]
	s_addc_u32 s21, s1, 0
	s_mov_b32 m0, s24
	v_readfirstlane_b32 s24, v5
	s_add_u32 s22, s4, 0x180
	global_load_lds_dwordx4 v3, s[20:21]
	s_mov_b32 m0, s24
	v_add_u32_e32 v5, 0x16000, v1
	s_addc_u32 s23, s5, 0
	global_load_lds_dwordx4 v4, s[20:21]
	v_readfirstlane_b32 s20, v5
	v_add_u32_e32 v5, 0x18000, v1
	s_mov_b32 m0, s20
	s_add_u32 s20, s0, 0x200
	v_readfirstlane_b32 s24, v5
	v_add_u32_e32 v5, 0x1a000, v1
	global_load_lds_dwordx4 v3, s[22:23]
	s_addc_u32 s21, s1, 0
	s_mov_b32 m0, s24
	v_readfirstlane_b32 s24, v5
	s_add_u32 s22, s4, 0x200
	global_load_lds_dwordx4 v3, s[20:21]
	s_mov_b32 m0, s24
	v_add_u32_e32 v5, 0x1c000, v1
	s_addc_u32 s23, s5, 0
	global_load_lds_dwordx4 v4, s[20:21]
	v_readfirstlane_b32 s20, v5
	v_add_u32_e32 v5, 0x1e000, v1
	s_mov_b32 m0, s20
	s_add_u32 s20, s0, 0x280
	v_readfirstlane_b32 s24, v5
	v_add_u32_e32 v5, 0x20000, v1
	global_load_lds_dwordx4 v3, s[22:23]
	s_addc_u32 s21, s1, 0
	s_mov_b32 m0, s24
	v_readfirstlane_b32 s24, v5
	global_load_lds_dwordx4 v3, s[20:21]
	s_mov_b32 m0, s24
	v_add_u32_e32 v1, 0x22000, v1
	s_add_u32 s22, s4, 0x280
	global_load_lds_dwordx4 v4, s[20:21]
	v_readfirstlane_b32 s20, v1
	s_addc_u32 s23, s5, 0
	s_mov_b32 m0, s20
	v_bfe_u32 v7, v0, 1, 3
	global_load_lds_dwordx4 v3, s[22:23]
	v_lshrrev_b32_e32 v6, 1, v0
	v_bitop3_b32 v2, v2, v7, 3 bitop3:0x6c
	v_and_b32_e32 v5, 15, v0
	v_lshrrev_b32_e32 v1, 2, v0
	s_movk_i32 s20, 0x60
	v_lshlrev_b32_e32 v9, 4, v2
	v_and_b32_e32 v2, 32, v6
	v_and_or_b32 v1, v1, s20, v5
	v_or_b32_e32 v5, v2, v5
	v_lshlrev_b32_e32 v6, 7, v5
	v_add_u32_e32 v38, 0, v6
	s_waitcnt vmcnt(15)
	s_barrier
	v_add_u32_e32 v8, v38, v9
	ds_read_b128 v[10:13], v8 offset:16384
	v_lshlrev_b32_e32 v55, 7, v1
	v_add_u32_e32 v30, 0, v55
	v_add_u32_e32 v5, v30, v9
	ds_read_b128 v[14:17], v5
	ds_read_b128 v[18:21], v8 offset:18432
	ds_read_b128 v[22:25], v5 offset:2048
	v_bfe_u32 v0, v0, 4, 2
	v_bitop3_b32 v9, v0, v7, 4 bitop3:0x36
	s_waitcnt lgkmcnt(0)
	v_mfma_f32_16x16x32_f16 v[26:29], v[10:13], v[14:17], 0
	v_or_b32_e32 v56, 0x4000, v6
	v_add_u32_e32 v7, 0x4000, v8
	v_lshlrev_b32_e32 v57, 4, v9
	v_mfma_f32_16x16x32_f16 v[14:17], v[18:21], v[14:17], 0
	v_add_u32_e32 v6, v30, v57
	v_add_u32_e32 v9, v38, v57
	ds_read_b128 v[30:33], v6
	ds_read_b128 v[34:37], v6 offset:2048
	ds_read_b128 v[38:41], v9 offset:16384
	ds_read_b128 v[42:45], v9 offset:18432
	v_mfma_f32_16x16x32_f16 v[10:13], v[10:13], v[22:25], 0
	v_mfma_f32_16x16x32_f16 v[18:21], v[18:21], v[22:25], 0
	s_add_u32 s20, s0, 0x300
	s_mov_b32 m0, s19
	s_waitcnt vmcnt(12) lgkmcnt(0)
	s_barrier
	s_addc_u32 s21, s1, 0
	s_add_u32 s22, s4, 0x300
	global_load_lds_dwordx4 v3, s[20:21]
	s_mov_b32 m0, s17
	s_addc_u32 s23, s5, 0
	global_load_lds_dwordx4 v4, s[20:21]
	s_mov_b32 m0, s18
	s_nop 0
	global_load_lds_dwordx4 v3, s[22:23]
	s_waitcnt lgkmcnt(0)
	v_mfma_f32_16x16x32_f16 v[22:25], v[38:41], v[30:33], v[26:29]
	v_mfma_f32_16x16x32_f16 v[14:17], v[42:45], v[30:33], v[14:17]
	s_nop 1
	ds_read_b128 v[26:29], v5 offset:24576
	ds_read_b128 v[30:33], v5 offset:26624
	ds_read_b128 v[46:49], v8 offset:40960
	ds_read_b128 v[50:53], v8 offset:43008
	v_mfma_f32_16x16x32_f16 v[10:13], v[38:41], v[34:37], v[10:13]
	v_mfma_f32_16x16x32_f16 v[18:21], v[42:45], v[34:37], v[18:21]
	s_waitcnt lgkmcnt(0)
	v_mfma_f32_16x16x32_f16 v[22:25], v[46:49], v[26:29], v[22:25]
	v_mfma_f32_16x16x32_f16 v[14:17], v[50:53], v[26:29], v[14:17]
	ds_read_b128 v[26:29], v6 offset:24576
	ds_read_b128 v[34:37], v6 offset:26624
	ds_read_b128 v[38:41], v9 offset:40960
	ds_read_b128 v[42:45], v9 offset:43008
	v_mfma_f32_16x16x32_f16 v[10:13], v[46:49], v[30:33], v[10:13]
	v_mfma_f32_16x16x32_f16 v[18:21], v[50:53], v[30:33], v[18:21]
	s_add_u32 s20, s0, 0x380
	s_mov_b32 m0, s16
	s_waitcnt vmcnt(12) lgkmcnt(0)
	s_barrier
	s_addc_u32 s21, s1, 0
	s_add_u32 s22, s4, 0x380
	global_load_lds_dwordx4 v3, s[20:21]
	s_mov_b32 m0, s14
	s_addc_u32 s23, s5, 0
	global_load_lds_dwordx4 v4, s[20:21]
	s_mov_b32 m0, s15
	s_nop 0
	global_load_lds_dwordx4 v3, s[22:23]
	s_waitcnt lgkmcnt(0)
	v_mfma_f32_16x16x32_f16 v[22:25], v[38:41], v[26:29], v[22:25]
	v_mfma_f32_16x16x32_f16 v[14:17], v[42:45], v[26:29], v[14:17]
	ds_read_b128 v[26:29], v5 offset:49152
	ds_read_b128 v[30:33], v5 offset:51200
	ds_read_b128 v[46:49], v7 offset:49152
	ds_read_b128 v[50:53], v7 offset:51200
	v_mfma_f32_16x16x32_f16 v[10:13], v[38:41], v[34:37], v[10:13]
	v_mfma_f32_16x16x32_f16 v[18:21], v[42:45], v[34:37], v[18:21]
	s_waitcnt lgkmcnt(0)
	v_mfma_f32_16x16x32_f16 v[22:25], v[46:49], v[26:29], v[22:25]
	v_mfma_f32_16x16x32_f16 v[14:17], v[50:53], v[26:29], v[14:17]
	s_add_i32 s20, 0, 0xc000
	v_add3_u32 v58, s20, v57, v56
	ds_read_b128 v[26:29], v6 offset:49152
	ds_read_b128 v[34:37], v6 offset:51200
	ds_read_b128 v[38:41], v58
	ds_read_b128 v[42:45], v58 offset:2048
	v_mfma_f32_16x16x32_f16 v[10:13], v[46:49], v[30:33], v[10:13]
	v_mfma_f32_16x16x32_f16 v[18:21], v[50:53], v[30:33], v[18:21]
	s_add_u32 s20, s0, 0x400
	s_mov_b32 m0, s7
	s_waitcnt vmcnt(12) lgkmcnt(0)
	s_barrier
	s_addc_u32 s21, s1, 0
	s_add_u32 s22, s4, 0x400
	global_load_lds_dwordx4 v3, s[20:21]
	s_mov_b32 m0, s3
	s_addc_u32 s23, s5, 0
	global_load_lds_dwordx4 v4, s[20:21]
	s_mov_b32 m0, s6
	s_nop 0
	global_load_lds_dwordx4 v3, s[22:23]
	s_waitcnt lgkmcnt(0)
	v_mfma_f32_16x16x32_f16 v[22:25], v[38:41], v[26:29], v[22:25]
	v_mfma_f32_16x16x32_f16 v[14:17], v[42:45], v[26:29], v[14:17]
	v_add_u32_e32 v59, 0x12000, v5
	v_add_u32_e32 v61, 0x16000, v8
	v_add_u32_e32 v60, 0x12800, v5
	ds_read_b128 v[26:29], v59
	ds_read_b128 v[30:33], v60
	v_add_u32_e32 v62, 0x16800, v8
	ds_read_b128 v[46:49], v61
	ds_read_b128 v[50:53], v62
	v_mfma_f32_16x16x32_f16 v[10:13], v[38:41], v[34:37], v[10:13]
	v_mfma_f32_16x16x32_f16 v[18:21], v[42:45], v[34:37], v[18:21]
	s_waitcnt lgkmcnt(0)
	v_mfma_f32_16x16x32_f16 v[22:25], v[46:49], v[26:29], v[22:25]
	v_mfma_f32_16x16x32_f16 v[14:17], v[50:53], v[26:29], v[14:17]
	s_add_i32 s20, 0, 0x12000
	v_add_u32_e32 v38, s20, v57
	v_add_u32_e32 v63, v38, v55
	v_add_u32_e32 v64, v38, v56
	ds_read_b128 v[26:29], v63
	ds_read_b128 v[34:37], v63 offset:2048
	ds_read_b128 v[38:41], v64
	ds_read_b128 v[42:45], v64 offset:2048
	v_mfma_f32_16x16x32_f16 v[10:13], v[46:49], v[30:33], v[10:13]
	v_mfma_f32_16x16x32_f16 v[18:21], v[50:53], v[30:33], v[18:21]
	v_add_u32_e32 v30, s20, v54
	s_add_u32 s24, s0, 0x480
	v_readfirstlane_b32 s22, v30
	v_add_u32_e32 v31, 0x2000, v30
	s_waitcnt vmcnt(12) lgkmcnt(0)
	s_barrier
	s_addc_u32 s25, s1, 0
	s_mov_b32 m0, s22
	v_readfirstlane_b32 s20, v31
	v_add_u32_e32 v30, 0x4000, v30
	s_add_u32 s26, s4, 0x480
	global_load_lds_dwordx4 v3, s[24:25]
	s_mov_b32 m0, s20
	v_readfirstlane_b32 s21, v30
	s_addc_u32 s27, s5, 0
	global_load_lds_dwordx4 v4, s[24:25]
	s_mov_b32 m0, s21
	s_nop 0
	global_load_lds_dwordx4 v3, s[26:27]
	s_waitcnt lgkmcnt(0)
	v_mfma_f32_16x16x32_f16 v[22:25], v[38:41], v[26:29], v[22:25]
	v_mfma_f32_16x16x32_f16 v[14:17], v[42:45], v[26:29], v[14:17]
	v_add_u32_e32 v65, 0x18000, v5
	v_add_u32_e32 v67, 0x1c000, v8
	v_add_u32_e32 v66, 0x18800, v5
	ds_read_b128 v[26:29], v65
	ds_read_b128 v[30:33], v66
	v_add_u32_e32 v68, 0x1c800, v8
	ds_read_b128 v[46:49], v67
	ds_read_b128 v[50:53], v68
	v_mfma_f32_16x16x32_f16 v[10:13], v[38:41], v[34:37], v[10:13]
	v_mfma_f32_16x16x32_f16 v[18:21], v[42:45], v[34:37], v[18:21]
	s_waitcnt lgkmcnt(0)
	v_mfma_f32_16x16x32_f16 v[22:25], v[46:49], v[26:29], v[22:25]
	v_mfma_f32_16x16x32_f16 v[14:17], v[50:53], v[26:29], v[14:17]
	s_add_i32 s23, 0, 0x18000
	v_add_u32_e32 v38, s23, v57
	v_add_u32_e32 v69, v38, v55
	v_add_u32_e32 v70, v38, v56
	ds_read_b128 v[26:29], v69
	ds_read_b128 v[34:37], v69 offset:2048
	ds_read_b128 v[38:41], v70
	ds_read_b128 v[42:45], v70 offset:2048
	v_mfma_f32_16x16x32_f16 v[10:13], v[46:49], v[30:33], v[10:13]
	v_mfma_f32_16x16x32_f16 v[18:21], v[50:53], v[30:33], v[18:21]
	v_add_u32_e32 v30, s23, v54
	s_add_u32 s24, s0, 0x500
	v_readfirstlane_b32 s23, v30
	v_add_u32_e32 v31, 0x2000, v30
	s_waitcnt vmcnt(12) lgkmcnt(0)
	s_barrier
	s_addc_u32 s25, s1, 0
	s_mov_b32 m0, s23
	v_readfirstlane_b32 s23, v31
	v_add_u32_e32 v30, 0x4000, v30
	s_add_u32 s26, s4, 0x500
	global_load_lds_dwordx4 v3, s[24:25]
	s_mov_b32 m0, s23
	v_readfirstlane_b32 s23, v30
	s_addc_u32 s27, s5, 0
	global_load_lds_dwordx4 v4, s[24:25]
	s_mov_b32 m0, s23
	s_nop 0
	global_load_lds_dwordx4 v3, s[26:27]
	s_waitcnt lgkmcnt(0)
	v_mfma_f32_16x16x32_f16 v[22:25], v[38:41], v[26:29], v[22:25]
	v_mfma_f32_16x16x32_f16 v[14:17], v[42:45], v[26:29], v[14:17]
	v_add_u32_e32 v71, 0x1e000, v5
	v_add_u32_e32 v73, 0x22000, v8
	v_add_u32_e32 v72, 0x1e800, v5
	ds_read_b128 v[26:29], v71
	ds_read_b128 v[30:33], v72
	v_add_u32_e32 v74, 0x22800, v8
	ds_read_b128 v[46:49], v73
	ds_read_b128 v[50:53], v74
	v_mfma_f32_16x16x32_f16 v[10:13], v[38:41], v[34:37], v[10:13]
	v_mfma_f32_16x16x32_f16 v[18:21], v[42:45], v[34:37], v[18:21]
	s_waitcnt lgkmcnt(0)
	v_mfma_f32_16x16x32_f16 v[22:25], v[46:49], v[26:29], v[22:25]
	v_mfma_f32_16x16x32_f16 v[14:17], v[50:53], v[26:29], v[14:17]
	s_add_i32 s23, 0, 0x1e000
	v_add_u32_e32 v38, s23, v57
	v_add_u32_e32 v55, v38, v55
	v_add_u32_e32 v56, v38, v56
	ds_read_b128 v[26:29], v55
	ds_read_b128 v[34:37], v55 offset:2048
	ds_read_b128 v[38:41], v56
	ds_read_b128 v[42:45], v56 offset:2048
	v_mfma_f32_16x16x32_f16 v[10:13], v[46:49], v[30:33], v[10:13]
	v_mfma_f32_16x16x32_f16 v[18:21], v[50:53], v[30:33], v[18:21]
	v_add_u32_e32 v30, s23, v54
	s_add_u32 s24, s0, 0x580
	v_readfirstlane_b32 s23, v30
	v_add_u32_e32 v31, 0x2000, v30
	s_waitcnt vmcnt(12) lgkmcnt(0)
	s_barrier
	s_addc_u32 s25, s1, 0
	s_mov_b32 m0, s23
	v_readfirstlane_b32 s23, v31
	v_add_u32_e32 v30, 0x4000, v30
	s_add_u32 s26, s4, 0x580
	global_load_lds_dwordx4 v3, s[24:25]
	s_mov_b32 m0, s23
	v_readfirstlane_b32 s23, v30
	s_addc_u32 s27, s5, 0
	global_load_lds_dwordx4 v4, s[24:25]
	s_mov_b32 m0, s23
	s_nop 0
	global_load_lds_dwordx4 v3, s[26:27]
	s_waitcnt lgkmcnt(0)
	v_mfma_f32_16x16x32_f16 v[22:25], v[38:41], v[26:29], v[22:25]
	v_mfma_f32_16x16x32_f16 v[14:17], v[42:45], v[26:29], v[14:17]
	ds_read_b128 v[26:29], v5
	ds_read_b128 v[30:33], v5 offset:2048
	ds_read_b128 v[46:49], v8 offset:16384
	ds_read_b128 v[50:53], v8 offset:18432
	v_mfma_f32_16x16x32_f16 v[10:13], v[38:41], v[34:37], v[10:13]
	v_mfma_f32_16x16x32_f16 v[18:21], v[42:45], v[34:37], v[18:21]
	s_waitcnt lgkmcnt(0)
	v_mfma_f32_16x16x32_f16 v[22:25], v[46:49], v[26:29], v[22:25]
	v_mfma_f32_16x16x32_f16 v[14:17], v[50:53], v[26:29], v[14:17]
	ds_read_b128 v[26:29], v6
	ds_read_b128 v[34:37], v6 offset:2048
	ds_read_b128 v[38:41], v9 offset:16384
	ds_read_b128 v[42:45], v9 offset:18432
	v_mfma_f32_16x16x32_f16 v[10:13], v[46:49], v[30:33], v[10:13]
	v_mfma_f32_16x16x32_f16 v[18:21], v[50:53], v[30:33], v[18:21]
	s_add_u32 s24, s0, 0x600
	s_mov_b32 m0, s19
	s_waitcnt vmcnt(12) lgkmcnt(0)
	s_barrier
	s_addc_u32 s25, s1, 0
	s_add_u32 s26, s4, 0x600
	global_load_lds_dwordx4 v3, s[24:25]
	s_mov_b32 m0, s17
	s_addc_u32 s27, s5, 0
	global_load_lds_dwordx4 v4, s[24:25]
	s_mov_b32 m0, s18
	s_nop 0
	global_load_lds_dwordx4 v3, s[26:27]
	s_waitcnt lgkmcnt(0)
	v_mfma_f32_16x16x32_f16 v[22:25], v[38:41], v[26:29], v[22:25]
	v_mfma_f32_16x16x32_f16 v[14:17], v[42:45], v[26:29], v[14:17]
	ds_read_b128 v[26:29], v5 offset:24576
	ds_read_b128 v[30:33], v5 offset:26624
	ds_read_b128 v[46:49], v8 offset:40960
	ds_read_b128 v[50:53], v8 offset:43008
	v_mfma_f32_16x16x32_f16 v[10:13], v[38:41], v[34:37], v[10:13]
	v_mfma_f32_16x16x32_f16 v[18:21], v[42:45], v[34:37], v[18:21]
	s_waitcnt lgkmcnt(0)
	v_mfma_f32_16x16x32_f16 v[22:25], v[46:49], v[26:29], v[22:25]
	v_mfma_f32_16x16x32_f16 v[14:17], v[50:53], v[26:29], v[14:17]
	ds_read_b128 v[26:29], v6 offset:24576
	ds_read_b128 v[34:37], v6 offset:26624
	ds_read_b128 v[38:41], v9 offset:40960
	ds_read_b128 v[42:45], v9 offset:43008
	v_mfma_f32_16x16x32_f16 v[10:13], v[46:49], v[30:33], v[10:13]
	v_mfma_f32_16x16x32_f16 v[18:21], v[50:53], v[30:33], v[18:21]
	s_mov_b32 m0, s16
	s_add_u32 s16, s0, 0x680
	s_waitcnt vmcnt(12) lgkmcnt(0)
	s_barrier
	s_addc_u32 s17, s1, 0
	s_add_u32 s18, s4, 0x680
	global_load_lds_dwordx4 v3, s[16:17]
	s_mov_b32 m0, s14
	s_addc_u32 s19, s5, 0
	global_load_lds_dwordx4 v4, s[16:17]
	s_mov_b32 m0, s15
	s_nop 0
	global_load_lds_dwordx4 v3, s[18:19]
	s_waitcnt lgkmcnt(0)
	v_mfma_f32_16x16x32_f16 v[22:25], v[38:41], v[26:29], v[22:25]
	v_mfma_f32_16x16x32_f16 v[14:17], v[42:45], v[26:29], v[14:17]
	ds_read_b128 v[26:29], v5 offset:49152
	ds_read_b128 v[30:33], v5 offset:51200
	ds_read_b128 v[46:49], v7 offset:49152
	ds_read_b128 v[50:53], v7 offset:51200
	v_mfma_f32_16x16x32_f16 v[10:13], v[38:41], v[34:37], v[10:13]
	v_mfma_f32_16x16x32_f16 v[18:21], v[42:45], v[34:37], v[18:21]
	s_waitcnt lgkmcnt(0)
	v_mfma_f32_16x16x32_f16 v[22:25], v[46:49], v[26:29], v[22:25]
	v_mfma_f32_16x16x32_f16 v[14:17], v[50:53], v[26:29], v[14:17]
	ds_read_b128 v[26:29], v6 offset:49152
	ds_read_b128 v[34:37], v6 offset:51200
	ds_read_b128 v[38:41], v58
	ds_read_b128 v[42:45], v58 offset:2048
	v_mfma_f32_16x16x32_f16 v[10:13], v[46:49], v[30:33], v[10:13]
	v_mfma_f32_16x16x32_f16 v[18:21], v[50:53], v[30:33], v[18:21]
	s_add_u32 s14, s0, 0x700
	s_mov_b32 m0, s7
	s_waitcnt vmcnt(12) lgkmcnt(0)
	s_barrier
	s_addc_u32 s15, s1, 0
	s_add_u32 s16, s4, 0x700
	global_load_lds_dwordx4 v3, s[14:15]
	s_mov_b32 m0, s3
	s_addc_u32 s17, s5, 0
	global_load_lds_dwordx4 v4, s[14:15]
	s_mov_b32 m0, s6
	s_nop 0
	global_load_lds_dwordx4 v3, s[16:17]
	s_waitcnt lgkmcnt(0)
	v_mfma_f32_16x16x32_f16 v[22:25], v[38:41], v[26:29], v[22:25]
	v_mfma_f32_16x16x32_f16 v[14:17], v[42:45], v[26:29], v[14:17]
	ds_read_b128 v[26:29], v59
	ds_read_b128 v[30:33], v60
	ds_read_b128 v[46:49], v61
	ds_read_b128 v[50:53], v62
	v_mfma_f32_16x16x32_f16 v[10:13], v[38:41], v[34:37], v[10:13]
	v_mfma_f32_16x16x32_f16 v[18:21], v[42:45], v[34:37], v[18:21]
	s_waitcnt lgkmcnt(0)
	v_mfma_f32_16x16x32_f16 v[22:25], v[46:49], v[26:29], v[22:25]
	v_mfma_f32_16x16x32_f16 v[14:17], v[50:53], v[26:29], v[14:17]
	ds_read_b128 v[26:29], v63
	ds_read_b128 v[34:37], v63 offset:2048
	ds_read_b128 v[38:41], v64
	ds_read_b128 v[42:45], v64 offset:2048
	v_mfma_f32_16x16x32_f16 v[10:13], v[46:49], v[30:33], v[10:13]
	v_mfma_f32_16x16x32_f16 v[18:21], v[50:53], v[30:33], v[18:21]
	s_add_u32 s0, s0, 0x780
	s_mov_b32 m0, s22
	s_waitcnt vmcnt(12) lgkmcnt(0)
	s_barrier
	s_addc_u32 s1, s1, 0
	s_add_u32 s4, s4, 0x780
	global_load_lds_dwordx4 v3, s[0:1]
	s_mov_b32 m0, s20
	s_addc_u32 s5, s5, 0
	global_load_lds_dwordx4 v4, s[0:1]
	s_mov_b32 m0, s21
	s_nop 0
	global_load_lds_dwordx4 v3, s[4:5]
	s_waitcnt lgkmcnt(0)
	v_mfma_f32_16x16x32_f16 v[22:25], v[38:41], v[26:29], v[22:25]
	v_mfma_f32_16x16x32_f16 v[14:17], v[42:45], v[26:29], v[14:17]
	ds_read_b128 v[26:29], v65
	ds_read_b128 v[30:33], v66
	ds_read_b128 v[46:49], v67
	ds_read_b128 v[50:53], v68
	v_mfma_f32_16x16x32_f16 v[10:13], v[38:41], v[34:37], v[10:13]
	v_mfma_f32_16x16x32_f16 v[18:21], v[42:45], v[34:37], v[18:21]
	s_waitcnt lgkmcnt(0)
	v_mfma_f32_16x16x32_f16 v[22:25], v[46:49], v[26:29], v[22:25]
	v_mfma_f32_16x16x32_f16 v[14:17], v[50:53], v[26:29], v[14:17]
	ds_read_b128 v[26:29], v69
	ds_read_b128 v[34:37], v69 offset:2048
	ds_read_b128 v[38:41], v70
	ds_read_b128 v[42:45], v70 offset:2048
	v_mfma_f32_16x16x32_f16 v[10:13], v[46:49], v[30:33], v[10:13]
	v_mfma_f32_16x16x32_f16 v[18:21], v[50:53], v[30:33], v[18:21]
	s_waitcnt vmcnt(12) lgkmcnt(0)
	s_barrier
	s_waitcnt lgkmcnt(0)
	v_mfma_f32_16x16x32_f16 v[22:25], v[38:41], v[26:29], v[22:25]
	v_mfma_f32_16x16x32_f16 v[14:17], v[42:45], v[26:29], v[14:17]
	ds_read_b128 v[26:29], v71
	ds_read_b128 v[30:33], v72
	ds_read_b128 v[46:49], v73
	ds_read_b128 v[50:53], v74
	v_mfma_f32_16x16x32_f16 v[10:13], v[38:41], v[34:37], v[10:13]
	v_mfma_f32_16x16x32_f16 v[18:21], v[42:45], v[34:37], v[18:21]
	s_waitcnt lgkmcnt(0)
	v_mfma_f32_16x16x32_f16 v[22:25], v[46:49], v[26:29], v[22:25]
	v_mfma_f32_16x16x32_f16 v[14:17], v[50:53], v[26:29], v[14:17]
	ds_read_b128 v[26:29], v55
	ds_read_b128 v[34:37], v55 offset:2048
	ds_read_b128 v[38:41], v56
	ds_read_b128 v[42:45], v56 offset:2048
	v_mfma_f32_16x16x32_f16 v[10:13], v[46:49], v[30:33], v[10:13]
	v_mfma_f32_16x16x32_f16 v[18:21], v[50:53], v[30:33], v[18:21]
	s_waitcnt vmcnt(0) lgkmcnt(0)
	s_barrier
	s_waitcnt lgkmcnt(0)
	v_mfma_f32_16x16x32_f16 v[22:25], v[38:41], v[26:29], v[22:25]
	v_mfma_f32_16x16x32_f16 v[14:17], v[42:45], v[26:29], v[14:17]
	ds_read_b128 v[26:29], v5
	ds_read_b128 v[30:33], v5 offset:2048
	ds_read_b128 v[46:49], v8 offset:16384
	ds_read_b128 v[50:53], v8 offset:18432
	v_mfma_f32_16x16x32_f16 v[10:13], v[38:41], v[34:37], v[10:13]
	v_mfma_f32_16x16x32_f16 v[18:21], v[42:45], v[34:37], v[18:21]
	s_waitcnt lgkmcnt(0)
	v_mfma_f32_16x16x32_f16 v[22:25], v[46:49], v[26:29], v[22:25]
	v_mfma_f32_16x16x32_f16 v[14:17], v[50:53], v[26:29], v[14:17]
	ds_read_b128 v[26:29], v6
	ds_read_b128 v[34:37], v6 offset:2048
	ds_read_b128 v[38:41], v9 offset:16384
	ds_read_b128 v[42:45], v9 offset:18432
	v_mfma_f32_16x16x32_f16 v[10:13], v[46:49], v[30:33], v[10:13]
	v_mfma_f32_16x16x32_f16 v[18:21], v[50:53], v[30:33], v[18:21]
	s_waitcnt vmcnt(0) lgkmcnt(0)
	s_barrier
	s_waitcnt lgkmcnt(0)
	v_mfma_f32_16x16x32_f16 v[22:25], v[38:41], v[26:29], v[22:25]
	v_mfma_f32_16x16x32_f16 v[14:17], v[42:45], v[26:29], v[14:17]
	ds_read_b128 v[26:29], v5 offset:24576
	ds_read_b128 v[30:33], v5 offset:26624
	ds_read_b128 v[46:49], v8 offset:40960
	ds_read_b128 v[50:53], v8 offset:43008
	v_mfma_f32_16x16x32_f16 v[10:13], v[38:41], v[34:37], v[10:13]
	v_mfma_f32_16x16x32_f16 v[18:21], v[42:45], v[34:37], v[18:21]
	s_waitcnt lgkmcnt(0)
	v_mfma_f32_16x16x32_f16 v[22:25], v[46:49], v[26:29], v[22:25]
	v_mfma_f32_16x16x32_f16 v[14:17], v[50:53], v[26:29], v[14:17]
	ds_read_b128 v[26:29], v6 offset:24576
	ds_read_b128 v[34:37], v6 offset:26624
	ds_read_b128 v[38:41], v9 offset:40960
	ds_read_b128 v[42:45], v9 offset:43008
	v_mfma_f32_16x16x32_f16 v[8:11], v[46:49], v[30:33], v[10:13]
	v_mfma_f32_16x16x32_f16 v[18:21], v[50:53], v[30:33], v[18:21]
	s_waitcnt vmcnt(0) lgkmcnt(0)
	s_barrier
	s_waitcnt lgkmcnt(0)
	v_mfma_f32_16x16x32_f16 v[22:25], v[38:41], v[26:29], v[22:25]
	v_mfma_f32_16x16x32_f16 v[12:15], v[42:45], v[26:29], v[14:17]
	ds_read_b128 v[26:29], v5 offset:49152
	ds_read_b128 v[30:33], v5 offset:51200
	ds_read_b128 v[46:49], v7 offset:49152
	ds_read_b128 v[50:53], v7 offset:51200
	v_mfma_f32_16x16x32_f16 v[8:11], v[38:41], v[34:37], v[8:11]
	v_mfma_f32_16x16x32_f16 v[16:19], v[42:45], v[34:37], v[18:21]
	s_waitcnt lgkmcnt(0)
	v_mfma_f32_16x16x32_f16 v[20:23], v[46:49], v[26:29], v[22:25]
	v_mfma_f32_16x16x32_f16 v[12:15], v[50:53], v[26:29], v[12:15]
	s_nop 1
	ds_read_b128 v[24:27], v6 offset:49152
	ds_read_b128 v[4:7], v6 offset:51200
	ds_read_b128 v[34:37], v58
	ds_read_b128 v[38:41], v58 offset:2048
	v_mfma_f32_16x16x32_f16 v[8:11], v[46:49], v[30:33], v[8:11]
	v_mfma_f32_16x16x32_f16 v[16:19], v[50:53], v[30:33], v[16:19]
	s_waitcnt vmcnt(0) lgkmcnt(0)
	s_barrier
	s_waitcnt lgkmcnt(0)
	v_mfma_f32_16x16x32_f16 v[20:23], v[34:37], v[24:27], v[20:23]
	v_mfma_f32_16x16x32_f16 v[12:15], v[38:41], v[24:27], v[12:15]
	ds_read_b128 v[24:27], v59
	ds_read_b128 v[28:31], v60
	ds_read_b128 v[42:45], v61
	ds_read_b128 v[46:49], v62
	v_mfma_f32_16x16x32_f16 v[8:11], v[34:37], v[4:7], v[8:11]
	v_mfma_f32_16x16x32_f16 v[4:7], v[38:41], v[4:7], v[16:19]
	s_waitcnt lgkmcnt(0)
	v_mfma_f32_16x16x32_f16 v[16:19], v[42:45], v[24:27], v[20:23]
	v_mfma_f32_16x16x32_f16 v[12:15], v[46:49], v[24:27], v[12:15]
	s_nop 1
	ds_read_b128 v[20:23], v63
	ds_read_b128 v[24:27], v63 offset:2048
	ds_read_b128 v[32:35], v64
	ds_read_b128 v[36:39], v64 offset:2048
	v_mfma_f32_16x16x32_f16 v[8:11], v[42:45], v[28:31], v[8:11]
	v_mfma_f32_16x16x32_f16 v[4:7], v[46:49], v[28:31], v[4:7]
	s_waitcnt lgkmcnt(0)
	v_mfma_f32_16x16x32_f16 v[16:19], v[32:35], v[20:23], v[16:19]
	v_mfma_f32_16x16x32_f16 v[12:15], v[36:39], v[20:23], v[12:15]
	v_mfma_f32_16x16x32_f16 v[8:11], v[32:35], v[24:27], v[8:11]
	v_mfma_f32_16x16x32_f16 v[4:7], v[36:39], v[24:27], v[4:7]
	v_or_b32_e32 v38, s12, v1
	v_lshlrev_b32_e32 v0, 2, v0
	v_or3_b32 v0, v0, v2, s13
	v_mad_u64_u32 v[2:3], s[0:1], v38, s2, 0
	s_ashr_i32 s3, s2, 31
	v_mov_b32_e32 v20, v3
	v_mad_u64_u32 v[20:21], s[0:1], v38, s3, v[20:21]
	v_mov_b32_e32 v3, v20
	v_mov_b32_e32 v1, 0
	v_lshl_add_u64 v[2:3], v[2:3], 2, s[8:9]
	v_lshlrev_b64 v[32:33], 2, v[0:1]
	v_lshl_add_u64 v[34:35], v[2:3], 0, v[32:33]
	v_lshl_add_u64 v[36:37], s[10:11], 0, v[32:33]
	v_or_b32_e32 v39, 16, v38
	v_mad_u64_u32 v[36:37], s[0:1], v39, s2, 0
	v_mov_b32_e32 v38, v37
	v_mad_u64_u32 v[38:39], s[0:1], v39, s3, v[38:39]
	v_mov_b32_e32 v37, v38
	v_lshl_add_u64 v[36:37], v[36:37], 2, s[8:9]
	v_lshl_add_u64 v[32:33], v[36:37], 0, v[32:33]
	s_waitcnt vmcnt(0)
	v_pk_add_f32 v[2:3], v[18:19], v[82:83]
	v_pk_add_f32 v[0:1], v[16:17], v[80:81]
	v_pk_add_f32 v[14:15], v[14:15], v[86:87]
	v_pk_add_f32 v[12:13], v[12:13], v[84:85]
	v_pk_add_f32 v[2:3], v[90:91], v[2:3]
	v_pk_add_f32 v[0:1], v[88:89], v[0:1]
	v_pk_add_f32 v[14:15], v[94:95], v[14:15]
	v_pk_add_f32 v[12:13], v[92:93], v[12:13]
	global_store_dwordx4 v[34:35], v[0:3], off
	global_store_dwordx4 v[34:35], v[12:15], off offset:64
	v_pk_add_f32 v[42:43], v[10:11], v[98:99]
	v_pk_add_f32 v[40:41], v[8:9], v[96:97]
	v_pk_add_f32 v[6:7], v[6:7], v[102:103]
	v_pk_add_f32 v[4:5], v[4:5], v[100:101]
	v_pk_add_f32 v[42:43], v[90:91], v[42:43]
	v_pk_add_f32 v[40:41], v[88:89], v[40:41]
	v_pk_add_f32 v[6:7], v[94:95], v[6:7]
	v_pk_add_f32 v[4:5], v[92:93], v[4:5]
	global_store_dwordx4 v[32:33], v[40:43], off
	global_store_dwordx4 v[32:33], v[4:7], off offset:64
	s_endpgm
	s_endpgm
	s_endpgm
	s_endpgm
	s_endpgm
	s_endpgm
	s_endpgm
	s_endpgm
	s_endpgm
	s_endpgm
	s_endpgm
	s_endpgm
	s_endpgm
	s_endpgm
	s_endpgm
	s_endpgm
	s_endpgm
	s_endpgm
	s_endpgm
	s_endpgm
	s_endpgm
	s_endpgm
	s_endpgm
	s_endpgm
	s_endpgm
	s_endpgm
	s_endpgm
	s_endpgm
	s_endpgm
	s_endpgm
	s_endpgm
	s_endpgm
	s_endpgm
	s_endpgm
	s_endpgm
	s_endpgm
	s_endpgm
	s_endpgm
	s_endpgm
	s_endpgm
	s_endpgm
	s_endpgm
	s_endpgm
	s_endpgm
	s_endpgm
	s_endpgm
	s_endpgm
	s_endpgm
	s_endpgm
	s_endpgm
	s_endpgm
	s_endpgm
	s_endpgm
	s_endpgm
	s_endpgm
	s_endpgm
	s_endpgm
	s_endpgm
	s_endpgm
	s_endpgm
	s_endpgm
	s_endpgm
	s_endpgm

	.amdhsa_kernel _Z5gemm8ILi64ELi4ELi6ELi1ELi1ELi16EEvPKDF16_S1_iiiPDF16_PfPKf
		.amdhsa_group_segment_fixed_size 0
		.amdhsa_private_segment_fixed_size 0
		.amdhsa_kernarg_size 312
		.amdhsa_user_sgpr_count 2
		.amdhsa_user_sgpr_dispatch_ptr 0
		.amdhsa_user_sgpr_queue_ptr 0
		.amdhsa_user_sgpr_kernarg_segment_ptr 1
		.amdhsa_user_sgpr_dispatch_id 0
		.amdhsa_user_sgpr_kernarg_preload_length 0
		.amdhsa_user_sgpr_kernarg_preload_offset 0
		.amdhsa_user_sgpr_private_segment_size 0
		.amdhsa_uses_dynamic_stack 0
		.amdhsa_enable_private_segment 0
		.amdhsa_system_sgpr_workgroup_id_x 1
		.amdhsa_system_sgpr_workgroup_id_y 0
		.amdhsa_system_sgpr_workgroup_id_z 0
		.amdhsa_system_sgpr_workgroup_info 0
		.amdhsa_system_vgpr_workitem_id 0
		.amdhsa_next_free_vgpr 104
		.amdhsa_next_free_sgpr 32
		.amdhsa_accum_offset 104
		.amdhsa_reserve_vcc 0
		.amdhsa_float_round_mode_32 0
		.amdhsa_float_round_mode_16_64 0
		.amdhsa_float_denorm_mode_32 3
		.amdhsa_float_denorm_mode_16_64 3
		.amdhsa_dx10_clamp 1
		.amdhsa_ieee_mode 1
		.amdhsa_fp16_overflow 0
		.amdhsa_tg_split 0
		.amdhsa_exception_fp_ieee_invalid_op 0
		.amdhsa_exception_fp_denorm_src 0
		.amdhsa_exception_fp_ieee_div_zero 0
		.amdhsa_exception_fp_ieee_overflow 0
		.amdhsa_exception_fp_ieee_underflow 0
		.amdhsa_exception_fp_ieee_inexact 0
		.amdhsa_exception_int_div_zero 0
	.end_amdhsa_kernel

_Z5gemm8ILi128ELi2ELi4ELi4ELi2ELi32EEvPKDF16_S1_iiiPDF16_PfPKf:
	v_readfirstlane_b32 s32, v0
	s_nop 3
	s_bitcmp1_b32 s32, 8
	s_cbranch_scc0 .Lprio_skip3
	s_setprio 1
.Lprio_skip3:
	s_load_dwordx8 s[4:11], s[0:1], 0x0
	s_lshl_b32 s3, s2, 2
	s_waitcnt lgkmcnt(0)
	s_and_b32 s11, s2, 4
	s_lshr_b32 s12, s2, 6
	s_bfe_u32 s13, s2, 0x30003
	s_add_i32 s11, s11, s12
	s_and_b32 s12, s2, 1
	s_and_b32 s2, s3, 8
	s_or_b32 s2, s2, s13
	s_lshl_b32 s13, s2, 7
	s_lshr_b32 s2, s10, 31
	s_add_i32 s2, s10, s2
	s_ashr_i32 s14, s2, 1
	s_mul_hi_i32 s3, s10, s13
	s_mul_i32 s2, s10, s13
	s_lshl_b32 s11, s11, 7
	s_lshl_b64 s[2:3], s[2:3], 1
	v_lshrrev_b32_e32 v2, 4, v0
	s_add_u32 s15, s4, s2
	s_mul_i32 s2, s14, s12
	v_xor_b32_e32 v1, v2, v0
	v_or_b32_e32 v4, 0x200, v0
	s_addc_u32 s16, s5, s3
	s_ashr_i32 s3, s2, 31
	v_lshlrev_b32_e32 v1, 3, v1
	v_lshrrev_b32_e32 v3, 3, v0
	v_lshrrev_b32_e32 v4, 3, v4
	s_lshl_b64 s[4:5], s[2:3], 1
	v_and_b32_e32 v1, 56, v1
	v_mul_lo_u32 v3, v3, s10
	v_mul_lo_u32 v4, v4, s10
	s_add_u32 s2, s15, s4
	s_mul_hi_i32 s15, s10, s11
	s_mul_i32 s14, s10, s11
	v_lshlrev_b32_e32 v106, 4, v0
	v_add_lshl_u32 v3, v3, v1, 1
	v_add_lshl_u32 v4, v4, v1, 1
	s_addc_u32 s3, s16, s5
	s_lshl_b64 s[14:15], s[14:15], 1
	v_add_u32_e32 v1, 0, v106
	s_add_u32 s6, s6, s14
	v_readfirstlane_b32 s18, v1
	v_add_u32_e32 v5, 0x2000, v1
	s_addc_u32 s7, s7, s15
	s_mov_b32 m0, s18
	v_readfirstlane_b32 s15, v5
	v_add_u32_e32 v5, 0x4000, v1
	s_add_u32 s4, s6, s4
	global_load_lds_dwordx4 v3, s[2:3]
	s_mov_b32 m0, s15
	v_readfirstlane_b32 s16, v5
	v_add_u32_e32 v5, 0x6000, v1
	s_addc_u32 s5, s7, s5
	global_load_lds_dwordx4 v4, s[2:3]
	s_mov_b32 m0, s16
	v_readfirstlane_b32 s17, v5
	v_add_u32_e32 v5, 0x8000, v1
	global_load_lds_dwordx4 v3, s[4:5]
	s_mov_b32 m0, s17
	s_add_u32 s20, s2, 0x80
	v_readfirstlane_b32 s14, v5
	v_add_u32_e32 v5, 0xa000, v1
	global_load_lds_dwordx4 v4, s[4:5]
	s_addc_u32 s21, s3, 0
	s_mov_b32 m0, s14
	v_readfirstlane_b32 s6, v5
	v_add_u32_e32 v5, 0xc000, v1
	s_add_u32 s22, s4, 0x80
	global_load_lds_dwordx4 v3, s[20:21]
	s_mov_b32 m0, s6
	v_readfirstlane_b32 s7, v5
	v_add_u32_e32 v5, 0xe000, v1
	s_addc_u32 s23, s5, 0
	global_load_lds_dwordx4 v4, s[20:21]
	s_mov_b32 m0, s7
	v_readfirstlane_b32 s10, v5
	v_add_u32_e32 v5, 0x10000, v1
	global_load_lds_dwordx4 v3, s[22:23]
	s_mov_b32 m0, s10
	s_add_u32 s20, s2, 0x100
	v_readfirstlane_b32 s19, v5
	v_add_u32_e32 v5, 0x12000, v1
	global_load_lds_dwordx4 v4, s[22:23]
	s_addc_u32 s21, s3, 0
	s_mov_b32 m0, s19
	v_readfirstlane_b32 s19, v5
	v_add_u32_e32 v5, 0x14000, v1
	s_add_u32 s22, s4, 0x100
	global_load_lds_dwordx4 v3, s[20:21]
	s_mov_b32 m0, s19
	v_readfirstlane_b32 s19, v5
	v_add_u32_e32 v5, 0x16000, v1
	s_addc_u32 s23, s5, 0
	global_load_lds_dwordx4 v4, s[20:21]
	s_mov_b32 m0, s19
	v_readfirstlane_b32 s19, v5
	v_add_u32_e32 v5, 0x18000, v1
	global_load_lds_dwordx4 v3, s[22:23]
	s_mov_b32 m0, s19
	s_add_u32 s20, s2, 0x180
	v_readfirstlane_b32 s19, v5
	v_add_u32_e32 v5, 0x1a000, v1
	global_load_lds_dwordx4 v4, s[22:23]
	s_addc_u32 s21, s3, 0
	s_mov_b32 m0, s19
	v_readfirstlane_b32 s19, v5
	v_add_u32_e32 v5, 0x1c000, v1
	s_add_u32 s22, s4, 0x180
	global_load_lds_dwordx4 v3, s[20:21]
	s_mov_b32 m0, s19
	v_readfirstlane_b32 s19, v5
	v_add_u32_e32 v1, 0x1e000, v1
	s_addc_u32 s23, s5, 0
	global_load_lds_dwordx4 v4, s[20:21]
	s_mov_b32 m0, s19
	v_readfirstlane_b32 s19, v1
	global_load_lds_dwordx4 v3, s[22:23]
	s_mov_b32 m0, s19
	v_bfe_u32 v8, v0, 1, 3
	global_load_lds_dwordx4 v4, s[22:23]
	v_lshrrev_b32_e32 v6, 1, v0
	v_bitop3_b32 v2, v2, v8, 3 bitop3:0x6c
	v_and_b32_e32 v5, 15, v0
	v_lshrrev_b32_e32 v1, 2, v0
	v_lshlrev_b32_e32 v7, 4, v2
	v_and_b32_e32 v2, 0x60, v6
	v_and_or_b32 v1, v1, 64, v5
	v_or_b32_e32 v5, v2, v5
	v_lshlrev_b32_e32 v6, 7, v5
	v_lshlrev_b32_e32 v102, 7, v1
	v_add_u32_e32 v9, 0, v6
	v_add_u32_e32 v38, 0, v102
	s_waitcnt vmcnt(12)
	s_barrier
	v_add_u32_e32 v5, v9, v7
	v_add_u32_e32 v7, v38, v7
	ds_read_b128 v[10:13], v5 offset:18432
	ds_read_b128 v[14:17], v5 offset:16384
	ds_read_b128 v[18:21], v7
	ds_read_b128 v[22:25], v7 offset:2048
	ds_read_b128 v[30:33], v7 offset:4096
	ds_read_b128 v[34:37], v7 offset:6144
	s_load_dwordx2 s[0:1], s[0:1], 0x20
	v_bfe_u32 v0, v0, 4, 2
	v_bitop3_b32 v8, v0, v8, 4 bitop3:0x36
	v_or_b32_e32 v103, 0x4000, v6
	s_waitcnt lgkmcnt(0)
	v_mfma_f32_16x16x32_f16 v[26:29], v[14:17], v[18:21], 0
	v_lshlrev_b32_e32 v104, 4, v8
	v_mfma_f32_16x16x32_f16 v[18:21], v[10:13], v[18:21], 0
	v_add_u32_e32 v6, v38, v104
	ds_read_b128 v[38:41], v6
	ds_read_b128 v[42:45], v6 offset:2048
	ds_read_b128 v[46:49], v6 offset:4096
	ds_read_b128 v[50:53], v6 offset:6144
	v_add_u32_e32 v8, v9, v104
	ds_read_b128 v[54:57], v8 offset:16384
	ds_read_b128 v[58:61], v8 offset:18432
	v_mfma_f32_16x16x32_f16 v[62:65], v[14:17], v[22:25], 0
	v_mfma_f32_16x16x32_f16 v[22:25], v[10:13], v[22:25], 0
	v_mfma_f32_16x16x32_f16 v[66:69], v[14:17], v[30:33], 0
	v_mfma_f32_16x16x32_f16 v[30:33], v[10:13], v[30:33], 0
	v_mfma_f32_16x16x32_f16 v[14:17], v[14:17], v[34:37], 0
	v_mfma_f32_16x16x32_f16 v[10:13], v[10:13], v[34:37], 0
	s_add_u32 s20, s2, 0x200
	s_mov_b32 m0, s18
	s_waitcnt vmcnt(8) lgkmcnt(0)
	s_barrier
	s_addc_u32 s21, s3, 0
	s_add_u32 s22, s4, 0x200
	global_load_lds_dwordx4 v3, s[20:21]
	s_mov_b32 m0, s15
	s_addc_u32 s23, s5, 0
	global_load_lds_dwordx4 v4, s[20:21]
	s_mov_b32 m0, s16
	s_nop 0
	global_load_lds_dwordx4 v3, s[22:23]
	s_mov_b32 m0, s17
	s_nop 0
	global_load_lds_dwordx4 v4, s[22:23]
	s_waitcnt lgkmcnt(0)
	v_mfma_f32_16x16x32_f16 v[26:29], v[54:57], v[38:41], v[26:29]
	v_mfma_f32_16x16x32_f16 v[18:21], v[58:61], v[38:41], v[18:21]
	ds_read_b128 v[34:37], v7 offset:32768
	ds_read_b128 v[38:41], v7 offset:34816
	ds_read_b128 v[70:73], v7 offset:36864
	ds_read_b128 v[74:77], v7 offset:38912
	ds_read_b128 v[78:81], v5 offset:49152
	ds_read_b128 v[82:85], v5 offset:51200
	v_mfma_f32_16x16x32_f16 v[62:65], v[54:57], v[42:45], v[62:65]
	v_mfma_f32_16x16x32_f16 v[22:25], v[58:61], v[42:45], v[22:25]
	v_mfma_f32_16x16x32_f16 v[42:45], v[54:57], v[46:49], v[66:69]
	v_mfma_f32_16x16x32_f16 v[30:33], v[58:61], v[46:49], v[30:33]
	v_mfma_f32_16x16x32_f16 v[14:17], v[54:57], v[50:53], v[14:17]
	v_mfma_f32_16x16x32_f16 v[10:13], v[58:61], v[50:53], v[10:13]
	s_waitcnt lgkmcnt(0)
	v_mfma_f32_16x16x32_f16 v[26:29], v[78:81], v[34:37], v[26:29]
	v_mfma_f32_16x16x32_f16 v[18:21], v[82:85], v[34:37], v[18:21]
	ds_read_b128 v[34:37], v6 offset:32768
	ds_read_b128 v[46:49], v6 offset:34816
	ds_read_b128 v[50:53], v6 offset:36864
	ds_read_b128 v[54:57], v6 offset:38912
	ds_read_b128 v[58:61], v8 offset:49152
	ds_read_b128 v[66:69], v8 offset:51200
	v_mfma_f32_16x16x32_f16 v[62:65], v[78:81], v[38:41], v[62:65]
	v_mfma_f32_16x16x32_f16 v[22:25], v[82:85], v[38:41], v[22:25]
	v_mfma_f32_16x16x32_f16 v[38:41], v[78:81], v[70:73], v[42:45]
	v_mfma_f32_16x16x32_f16 v[30:33], v[82:85], v[70:73], v[30:33]
	v_mfma_f32_16x16x32_f16 v[42:45], v[78:81], v[74:77], v[14:17]
	v_mfma_f32_16x16x32_f16 v[70:73], v[82:85], v[74:77], v[10:13]
	s_add_u32 s20, s2, 0x280
	s_mov_b32 m0, s14
	s_waitcnt vmcnt(8) lgkmcnt(0)
	s_barrier
	s_addc_u32 s21, s3, 0
	s_add_u32 s22, s4, 0x280
	global_load_lds_dwordx4 v3, s[20:21]
	s_mov_b32 m0, s6
	s_addc_u32 s23, s5, 0
	global_load_lds_dwordx4 v4, s[20:21]
	s_mov_b32 m0, s7
	s_nop 0
	global_load_lds_dwordx4 v3, s[22:23]
	s_mov_b32 m0, s10
	s_nop 0
	global_load_lds_dwordx4 v4, s[22:23]
	s_waitcnt lgkmcnt(0)
	v_mfma_f32_16x16x32_f16 v[26:29], v[58:61], v[34:37], v[26:29]
	v_mfma_f32_16x16x32_f16 v[16:19], v[66:69], v[34:37], v[18:21]
	v_add_u32_e32 v9, 0x10000, v7
	v_add_u32_e32 v11, 0x11000, v7
	v_add_u32_e32 v13, 0x14000, v5
	v_add_u32_e32 v10, 0x10800, v7
	ds_read_b128 v[34:37], v9
	ds_read_b128 v[74:77], v10
	v_add_u32_e32 v12, 0x11800, v7
	ds_read_b128 v[78:81], v11
	ds_read_b128 v[82:85], v12
	v_add_u32_e32 v14, 0x14800, v5
	ds_read_b128 v[86:89], v13
	ds_read_b128 v[90:93], v14
	v_mfma_f32_16x16x32_f16 v[62:65], v[58:61], v[46:49], v[62:65]
	v_mfma_f32_16x16x32_f16 v[20:23], v[66:69], v[46:49], v[22:25]
	v_mfma_f32_16x16x32_f16 v[38:41], v[58:61], v[50:53], v[38:41]
	v_mfma_f32_16x16x32_f16 v[30:33], v[66:69], v[50:53], v[30:33]
	v_mfma_f32_16x16x32_f16 v[42:45], v[58:61], v[54:57], v[42:45]
	v_mfma_f32_16x16x32_f16 v[46:49], v[66:69], v[54:57], v[70:73]
	s_waitcnt lgkmcnt(0)
	v_mfma_f32_16x16x32_f16 v[24:27], v[86:89], v[34:37], v[26:29]
	v_mfma_f32_16x16x32_f16 v[34:37], v[90:93], v[34:37], v[16:19]
	s_add_i32 s19, 0, 0x10000
	s_nop 1
	v_add_u32_e32 v16, s19, v104
	v_add_u32_e32 v15, v16, v102
	ds_read_b128 v[50:53], v15
	ds_read_b128 v[54:57], v15 offset:2048
	ds_read_b128 v[58:61], v15 offset:4096
	ds_read_b128 v[66:69], v15 offset:6144
	v_add_u32_e32 v16, v16, v103
	ds_read_b128 v[70:73], v16
	ds_read_b128 v[94:97], v16 offset:2048
	v_mfma_f32_16x16x32_f16 v[62:65], v[86:89], v[74:77], v[62:65]
	v_mfma_f32_16x16x32_f16 v[74:77], v[90:93], v[74:77], v[20:23]
	v_mfma_f32_16x16x32_f16 v[38:41], v[86:89], v[78:81], v[38:41]
	v_mfma_f32_16x16x32_f16 v[28:31], v[90:93], v[78:81], v[30:33]
	v_mfma_f32_16x16x32_f16 v[42:45], v[86:89], v[82:85], v[42:45]
	v_mfma_f32_16x16x32_f16 v[46:49], v[90:93], v[82:85], v[46:49]
	v_add_u32_e32 v17, s19, v106
	s_add_u32 s20, s2, 0x300
	v_readfirstlane_b32 s22, v17
	v_add_u32_e32 v18, 0x2000, v17
	s_waitcnt vmcnt(8) lgkmcnt(0)
	s_barrier
	s_addc_u32 s21, s3, 0
	s_mov_b32 m0, s22
	v_readfirstlane_b32 s19, v18
	global_load_lds_dwordx4 v3, s[20:21]
	s_mov_b32 m0, s19
	v_add_u32_e32 v18, 0x4000, v17
	s_add_u32 s24, s4, 0x300
	global_load_lds_dwordx4 v4, s[20:21]
	v_readfirstlane_b32 s20, v18
	v_add_u32_e32 v17, 0x6000, v17
	s_addc_u32 s25, s5, 0
	s_mov_b32 m0, s20
	v_readfirstlane_b32 s21, v17
	global_load_lds_dwordx4 v3, s[24:25]
	s_mov_b32 m0, s21
	s_nop 0
	global_load_lds_dwordx4 v4, s[24:25]
	s_waitcnt lgkmcnt(0)
	v_mfma_f32_16x16x32_f16 v[24:27], v[70:73], v[50:53], v[24:27]
	v_mfma_f32_16x16x32_f16 v[32:35], v[94:97], v[50:53], v[34:37]
	v_add_u32_e32 v17, 0x18000, v7
	v_add_u32_e32 v19, 0x19000, v7
	v_add_u32_e32 v21, 0x1c000, v5
	v_add_u32_e32 v18, 0x18800, v7
	ds_read_b128 v[50:53], v17
	ds_read_b128 v[78:81], v18
	v_add_u32_e32 v20, 0x19800, v7
	ds_read_b128 v[82:85], v19
	ds_read_b128 v[86:89], v20
	v_add_u32_e32 v22, 0x1c800, v5
	ds_read_b128 v[90:93], v21
	ds_read_b128 v[98:101], v22
	v_mfma_f32_16x16x32_f16 v[62:65], v[70:73], v[54:57], v[62:65]
	v_mfma_f32_16x16x32_f16 v[54:57], v[94:97], v[54:57], v[74:77]
	v_mfma_f32_16x16x32_f16 v[36:39], v[70:73], v[58:61], v[38:41]
	v_mfma_f32_16x16x32_f16 v[28:31], v[94:97], v[58:61], v[28:31]
	v_mfma_f32_16x16x32_f16 v[40:43], v[70:73], v[66:69], v[42:45]
	v_mfma_f32_16x16x32_f16 v[44:47], v[94:97], v[66:69], v[46:49]
	s_waitcnt lgkmcnt(0)
	v_mfma_f32_16x16x32_f16 v[58:61], v[90:93], v[50:53], v[24:27]
	v_mfma_f32_16x16x32_f16 v[32:35], v[98:101], v[50:53], v[32:35]
	s_add_i32 s23, 0, 0x18000
	s_nop 0
	v_add_u32_e32 v24, s23, v104
	v_add_u32_e32 v23, v24, v102
	ds_read_b128 v[48:51], v23
	ds_read_b128 v[66:69], v23 offset:2048
	ds_read_b128 v[70:73], v23 offset:4096
	ds_read_b128 v[74:77], v23 offset:6144
	v_add_u32_e32 v24, v24, v103
	ds_read_b128 v[94:97], v24
	ds_read_b128 v[102:105], v24 offset:2048
	v_mfma_f32_16x16x32_f16 v[62:65], v[90:93], v[78:81], v[62:65]
	v_mfma_f32_16x16x32_f16 v[52:55], v[98:101], v[78:81], v[54:57]
	v_mfma_f32_16x16x32_f16 v[36:39], v[90:93], v[82:85], v[36:39]
	v_mfma_f32_16x16x32_f16 v[26:29], v[98:101], v[82:85], v[28:31]
	v_mfma_f32_16x16x32_f16 v[40:43], v[90:93], v[86:89], v[40:43]
	v_mfma_f32_16x16x32_f16 v[44:47], v[98:101], v[86:89], v[44:47]
	v_add_u32_e32 v25, s23, v106
	s_add_u32 s24, s2, 0x380
	v_readfirstlane_b32 s26, v25
	v_add_u32_e32 v30, 0x2000, v25
	s_waitcnt vmcnt(8) lgkmcnt(0)
	s_barrier
	s_addc_u32 s25, s3, 0
	s_mov_b32 m0, s26
	v_readfirstlane_b32 s23, v30
	global_load_lds_dwordx4 v3, s[24:25]
	s_mov_b32 m0, s23
	v_add_u32_e32 v30, 0x4000, v25
	s_add_u32 s28, s4, 0x380
	global_load_lds_dwordx4 v4, s[24:25]
	v_readfirstlane_b32 s24, v30
	v_add_u32_e32 v25, 0x6000, v25
	s_addc_u32 s29, s5, 0
	s_mov_b32 m0, s24
	v_readfirstlane_b32 s25, v25
	global_load_lds_dwordx4 v3, s[28:29]
	s_mov_b32 m0, s25
	s_nop 0
	global_load_lds_dwordx4 v4, s[28:29]
	s_waitcnt lgkmcnt(0)
	v_mfma_f32_16x16x32_f16 v[56:59], v[94:97], v[48:51], v[58:61]
	v_mfma_f32_16x16x32_f16 v[30:33], v[102:105], v[48:51], v[32:35]
	ds_read_b128 v[48:51], v7
	ds_read_b128 v[78:81], v7 offset:2048
	ds_read_b128 v[82:85], v7 offset:4096
	ds_read_b128 v[86:89], v7 offset:6144
	ds_read_b128 v[90:93], v5 offset:16384
	ds_read_b128 v[98:101], v5 offset:18432
	v_mfma_f32_16x16x32_f16 v[60:63], v[94:97], v[66:69], v[62:65]
	v_mfma_f32_16x16x32_f16 v[52:55], v[102:105], v[66:69], v[52:55]
	v_mfma_f32_16x16x32_f16 v[34:37], v[94:97], v[70:73], v[36:39]
	v_mfma_f32_16x16x32_f16 v[26:29], v[102:105], v[70:73], v[26:29]
	v_mfma_f32_16x16x32_f16 v[38:41], v[94:97], v[74:77], v[40:43]
	v_mfma_f32_16x16x32_f16 v[42:45], v[102:105], v[74:77], v[44:47]
	s_waitcnt lgkmcnt(0)
	v_mfma_f32_16x16x32_f16 v[56:59], v[90:93], v[48:51], v[56:59]
	v_mfma_f32_16x16x32_f16 v[30:33], v[98:101], v[48:51], v[30:33]
	ds_read_b128 v[46:49], v6
	ds_read_b128 v[64:67], v6 offset:2048
	ds_read_b128 v[68:71], v6 offset:4096
	ds_read_b128 v[72:75], v6 offset:6144
	ds_read_b128 v[94:97], v8 offset:16384
	ds_read_b128 v[102:105], v8 offset:18432
	v_mfma_f32_16x16x32_f16 v[60:63], v[90:93], v[78:81], v[60:63]
	v_mfma_f32_16x16x32_f16 v[50:53], v[98:101], v[78:81], v[52:55]
	v_mfma_f32_16x16x32_f16 v[34:37], v[90:93], v[82:85], v[34:37]
	v_mfma_f32_16x16x32_f16 v[26:29], v[98:101], v[82:85], v[26:29]
	v_mfma_f32_16x16x32_f16 v[38:41], v[90:93], v[86:89], v[38:41]
	v_mfma_f32_16x16x32_f16 v[42:45], v[98:101], v[86:89], v[42:45]
	s_add_u32 s28, s2, 0x400
	s_mov_b32 m0, s18
	s_waitcnt vmcnt(8) lgkmcnt(0)
	s_barrier
	s_addc_u32 s29, s3, 0
	s_add_u32 s30, s4, 0x400
	global_load_lds_dwordx4 v3, s[28:29]
	s_mov_b32 m0, s15
	s_addc_u32 s31, s5, 0
	global_load_lds_dwordx4 v4, s[28:29]
	s_mov_b32 m0, s16
	s_nop 0
	global_load_lds_dwordx4 v3, s[30:31]
	s_mov_b32 m0, s17
	s_nop 0
	global_load_lds_dwordx4 v4, s[30:31]
	s_waitcnt lgkmcnt(0)
	v_mfma_f32_16x16x32_f16 v[54:57], v[94:97], v[46:49], v[56:59]
	v_mfma_f32_16x16x32_f16 v[30:33], v[102:105], v[46:49], v[30:33]
	ds_read_b128 v[46:49], v7 offset:32768
	ds_read_b128 v[76:79], v7 offset:34816
	ds_read_b128 v[80:83], v7 offset:36864
	ds_read_b128 v[84:87], v7 offset:38912
	ds_read_b128 v[88:91], v5 offset:49152
	ds_read_b128 v[98:101], v5 offset:51200
	v_mfma_f32_16x16x32_f16 v[58:61], v[94:97], v[64:67], v[60:63]
	v_mfma_f32_16x16x32_f16 v[50:53], v[102:105], v[64:67], v[50:53]
	v_mfma_f32_16x16x32_f16 v[34:37], v[94:97], v[68:71], v[34:37]
	v_mfma_f32_16x16x32_f16 v[26:29], v[102:105], v[68:71], v[26:29]
	v_mfma_f32_16x16x32_f16 v[38:41], v[94:97], v[72:75], v[38:41]
	v_mfma_f32_16x16x32_f16 v[42:45], v[102:105], v[72:75], v[42:45]
	s_waitcnt lgkmcnt(0)
	v_mfma_f32_16x16x32_f16 v[54:57], v[88:91], v[46:49], v[54:57]
	v_mfma_f32_16x16x32_f16 v[30:33], v[98:101], v[46:49], v[30:33]
	ds_read_b128 v[46:49], v6 offset:32768
	ds_read_b128 v[62:65], v6 offset:34816
	ds_read_b128 v[66:69], v6 offset:36864
	ds_read_b128 v[70:73], v6 offset:38912
	ds_read_b128 v[92:95], v8 offset:49152
	ds_read_b128 v[102:105], v8 offset:51200
	v_mfma_f32_16x16x32_f16 v[58:61], v[88:91], v[76:79], v[58:61]
	v_mfma_f32_16x16x32_f16 v[50:53], v[98:101], v[76:79], v[50:53]
	v_mfma_f32_16x16x32_f16 v[34:37], v[88:91], v[80:83], v[34:37]
	v_mfma_f32_16x16x32_f16 v[26:29], v[98:101], v[80:83], v[26:29]
	v_mfma_f32_16x16x32_f16 v[38:41], v[88:91], v[84:87], v[38:41]
	v_mfma_f32_16x16x32_f16 v[42:45], v[98:101], v[84:87], v[42:45]
	s_add_u32 s28, s2, 0x480
	s_mov_b32 m0, s14
	s_waitcnt vmcnt(8) lgkmcnt(0)
	s_barrier
	s_addc_u32 s29, s3, 0
	s_add_u32 s30, s4, 0x480
	global_load_lds_dwordx4 v3, s[28:29]
	s_mov_b32 m0, s6
	s_addc_u32 s31, s5, 0
	global_load_lds_dwordx4 v4, s[28:29]
	s_mov_b32 m0, s7
	s_nop 0
	global_load_lds_dwordx4 v3, s[30:31]
	s_mov_b32 m0, s10
	s_nop 0
	global_load_lds_dwordx4 v4, s[30:31]
	s_waitcnt lgkmcnt(0)
	v_mfma_f32_16x16x32_f16 v[54:57], v[92:95], v[46:49], v[54:57]
	v_mfma_f32_16x16x32_f16 v[30:33], v[102:105], v[46:49], v[30:33]
	ds_read_b128 v[46:49], v9
	ds_read_b128 v[74:77], v10
	ds_read_b128 v[78:81], v11
	ds_read_b128 v[82:85], v12
	ds_read_b128 v[86:89], v13
	ds_read_b128 v[96:99], v14
	v_mfma_f32_16x16x32_f16 v[58:61], v[92:95], v[62:65], v[58:61]
	v_mfma_f32_16x16x32_f16 v[50:53], v[102:105], v[62:65], v[50:53]
	v_mfma_f32_16x16x32_f16 v[34:37], v[92:95], v[66:69], v[34:37]
	v_mfma_f32_16x16x32_f16 v[26:29], v[102:105], v[66:69], v[26:29]
	v_mfma_f32_16x16x32_f16 v[38:41], v[92:95], v[70:73], v[38:41]
	v_mfma_f32_16x16x32_f16 v[42:45], v[102:105], v[70:73], v[42:45]
	s_waitcnt lgkmcnt(0)
	v_mfma_f32_16x16x32_f16 v[54:57], v[86:89], v[46:49], v[54:57]
	v_mfma_f32_16x16x32_f16 v[30:33], v[96:99], v[46:49], v[30:33]
	ds_read_b128 v[46:49], v15
	ds_read_b128 v[62:65], v15 offset:2048
	ds_read_b128 v[66:69], v15 offset:4096
	ds_read_b128 v[70:73], v15 offset:6144
	ds_read_b128 v[90:93], v16
	ds_read_b128 v[100:103], v16 offset:2048
	v_mfma_f32_16x16x32_f16 v[58:61], v[86:89], v[74:77], v[58:61]
	v_mfma_f32_16x16x32_f16 v[50:53], v[96:99], v[74:77], v[50:53]
	v_mfma_f32_16x16x32_f16 v[34:37], v[86:89], v[78:81], v[34:37]
	v_mfma_f32_16x16x32_f16 v[26:29], v[96:99], v[78:81], v[26:29]
	v_mfma_f32_16x16x32_f16 v[38:41], v[86:89], v[82:85], v[38:41]
	v_mfma_f32_16x16x32_f16 v[42:45], v[96:99], v[82:85], v[42:45]
	s_add_u32 s28, s2, 0x500
	s_mov_b32 m0, s22
	s_waitcnt vmcnt(8) lgkmcnt(0)
	s_barrier
	s_addc_u32 s29, s3, 0
	s_add_u32 s30, s4, 0x500
	global_load_lds_dwordx4 v3, s[28:29]
	s_mov_b32 m0, s19
	s_addc_u32 s31, s5, 0
	global_load_lds_dwordx4 v4, s[28:29]
	s_mov_b32 m0, s20
	s_nop 0
	global_load_lds_dwordx4 v3, s[30:31]
	s_mov_b32 m0, s21
	s_nop 0
	global_load_lds_dwordx4 v4, s[30:31]
	s_waitcnt lgkmcnt(0)
	v_mfma_f32_16x16x32_f16 v[54:57], v[90:93], v[46:49], v[54:57]
	v_mfma_f32_16x16x32_f16 v[30:33], v[100:103], v[46:49], v[30:33]
	ds_read_b128 v[46:49], v17
	ds_read_b128 v[74:77], v18
	ds_read_b128 v[78:81], v19
	ds_read_b128 v[82:85], v20
	ds_read_b128 v[86:89], v21
	ds_read_b128 v[94:97], v22
	v_mfma_f32_16x16x32_f16 v[58:61], v[90:93], v[62:65], v[58:61]
	v_mfma_f32_16x16x32_f16 v[50:53], v[100:103], v[62:65], v[50:53]
	v_mfma_f32_16x16x32_f16 v[34:37], v[90:93], v[66:69], v[34:37]
	v_mfma_f32_16x16x32_f16 v[26:29], v[100:103], v[66:69], v[26:29]
	v_mfma_f32_16x16x32_f16 v[38:41], v[90:93], v[70:73], v[38:41]
	v_mfma_f32_16x16x32_f16 v[42:45], v[100:103], v[70:73], v[42:45]
	s_waitcnt lgkmcnt(0)
	v_mfma_f32_16x16x32_f16 v[54:57], v[86:89], v[46:49], v[54:57]
	v_mfma_f32_16x16x32_f16 v[30:33], v[94:97], v[46:49], v[30:33]
	ds_read_b128 v[46:49], v23
	ds_read_b128 v[62:65], v23 offset:2048
	ds_read_b128 v[66:69], v23 offset:4096
	ds_read_b128 v[70:73], v23 offset:6144
	ds_read_b128 v[90:93], v24
	ds_read_b128 v[98:101], v24 offset:2048
	v_mfma_f32_16x16x32_f16 v[58:61], v[86:89], v[74:77], v[58:61]
	v_mfma_f32_16x16x32_f16 v[50:53], v[94:97], v[74:77], v[50:53]
	v_mfma_f32_16x16x32_f16 v[34:37], v[86:89], v[78:81], v[34:37]
	v_mfma_f32_16x16x32_f16 v[26:29], v[94:97], v[78:81], v[26:29]
	v_mfma_f32_16x16x32_f16 v[38:41], v[86:89], v[82:85], v[38:41]
	v_mfma_f32_16x16x32_f16 v[42:45], v[94:97], v[82:85], v[42:45]
	s_add_u32 s28, s2, 0x580
	s_mov_b32 m0, s26
	s_waitcnt vmcnt(8) lgkmcnt(0)
	s_barrier
	s_addc_u32 s29, s3, 0
	s_add_u32 s30, s4, 0x580
	global_load_lds_dwordx4 v3, s[28:29]
	s_mov_b32 m0, s23
	s_addc_u32 s31, s5, 0
	global_load_lds_dwordx4 v4, s[28:29]
	s_mov_b32 m0, s24
	s_nop 0
	global_load_lds_dwordx4 v3, s[30:31]
	s_mov_b32 m0, s25
	s_nop 0
	global_load_lds_dwordx4 v4, s[30:31]
	s_waitcnt lgkmcnt(0)
	v_mfma_f32_16x16x32_f16 v[54:57], v[90:93], v[46:49], v[54:57]
	v_mfma_f32_16x16x32_f16 v[30:33], v[98:101], v[46:49], v[30:33]
	ds_read_b128 v[46:49], v7
	ds_read_b128 v[74:77], v7 offset:2048
	ds_read_b128 v[78:81], v7 offset:4096
	ds_read_b128 v[82:85], v7 offset:6144
	ds_read_b128 v[86:89], v5 offset:16384
	ds_read_b128 v[94:97], v5 offset:18432
	v_mfma_f32_16x16x32_f16 v[58:61], v[90:93], v[62:65], v[58:61]
	v_mfma_f32_16x16x32_f16 v[50:53], v[98:101], v[62:65], v[50:53]
	v_mfma_f32_16x16x32_f16 v[34:37], v[90:93], v[66:69], v[34:37]
	v_mfma_f32_16x16x32_f16 v[26:29], v[98:101], v[66:69], v[26:29]
	v_mfma_f32_16x16x32_f16 v[38:41], v[90:93], v[70:73], v[38:41]
	v_mfma_f32_16x16x32_f16 v[42:45], v[98:101], v[70:73], v[42:45]
	s_waitcnt lgkmcnt(0)
	v_mfma_f32_16x16x32_f16 v[54:57], v[86:89], v[46:49], v[54:57]
	v_mfma_f32_16x16x32_f16 v[30:33], v[94:97], v[46:49], v[30:33]
	ds_read_b128 v[46:49], v6
	ds_read_b128 v[62:65], v6 offset:2048
	ds_read_b128 v[66:69], v6 offset:4096
	ds_read_b128 v[70:73], v6 offset:6144
	ds_read_b128 v[90:93], v8 offset:16384
	ds_read_b128 v[98:101], v8 offset:18432
	v_mfma_f32_16x16x32_f16 v[58:61], v[86:89], v[74:77], v[58:61]
	v_mfma_f32_16x16x32_f16 v[50:53], v[94:97], v[74:77], v[50:53]
	v_mfma_f32_16x16x32_f16 v[34:37], v[86:89], v[78:81], v[34:37]
	v_mfma_f32_16x16x32_f16 v[26:29], v[94:97], v[78:81], v[26:29]
	v_mfma_f32_16x16x32_f16 v[38:41], v[86:89], v[82:85], v[38:41]
	v_mfma_f32_16x16x32_f16 v[42:45], v[94:97], v[82:85], v[42:45]
	s_add_u32 s28, s2, 0x600
	s_mov_b32 m0, s18
	s_waitcnt vmcnt(8) lgkmcnt(0)
	s_barrier
	s_addc_u32 s29, s3, 0
	s_add_u32 s30, s4, 0x600
	global_load_lds_dwordx4 v3, s[28:29]
	s_mov_b32 m0, s15
	s_addc_u32 s31, s5, 0
	global_load_lds_dwordx4 v4, s[28:29]
	s_mov_b32 m0, s16
	s_nop 0
	global_load_lds_dwordx4 v3, s[30:31]
	s_mov_b32 m0, s17
	s_nop 0
	global_load_lds_dwordx4 v4, s[30:31]
	s_waitcnt lgkmcnt(0)
	v_mfma_f32_16x16x32_f16 v[54:57], v[90:93], v[46:49], v[54:57]
	v_mfma_f32_16x16x32_f16 v[30:33], v[98:101], v[46:49], v[30:33]
	ds_read_b128 v[46:49], v7 offset:32768
	ds_read_b128 v[74:77], v7 offset:34816
	ds_read_b128 v[78:81], v7 offset:36864
	ds_read_b128 v[82:85], v7 offset:38912
	ds_read_b128 v[86:89], v5 offset:49152
	ds_read_b128 v[94:97], v5 offset:51200
	v_mfma_f32_16x16x32_f16 v[58:61], v[90:93], v[62:65], v[58:61]
	v_mfma_f32_16x16x32_f16 v[50:53], v[98:101], v[62:65], v[50:53]
	v_mfma_f32_16x16x32_f16 v[34:37], v[90:93], v[66:69], v[34:37]
	v_mfma_f32_16x16x32_f16 v[26:29], v[98:101], v[66:69], v[26:29]
	v_mfma_f32_16x16x32_f16 v[38:41], v[90:93], v[70:73], v[38:41]
	v_mfma_f32_16x16x32_f16 v[42:45], v[98:101], v[70:73], v[42:45]
	s_waitcnt lgkmcnt(0)
	v_mfma_f32_16x16x32_f16 v[54:57], v[86:89], v[46:49], v[54:57]
	v_mfma_f32_16x16x32_f16 v[30:33], v[94:97], v[46:49], v[30:33]
	ds_read_b128 v[46:49], v6 offset:32768
	ds_read_b128 v[62:65], v6 offset:34816
	ds_read_b128 v[66:69], v6 offset:36864
	ds_read_b128 v[70:73], v6 offset:38912
	ds_read_b128 v[90:93], v8 offset:49152
	ds_read_b128 v[98:101], v8 offset:51200
	v_mfma_f32_16x16x32_f16 v[58:61], v[86:89], v[74:77], v[58:61]
	v_mfma_f32_16x16x32_f16 v[50:53], v[94:97], v[74:77], v[50:53]
	v_mfma_f32_16x16x32_f16 v[34:37], v[86:89], v[78:81], v[34:37]
	v_mfma_f32_16x16x32_f16 v[26:29], v[94:97], v[78:81], v[26:29]
	v_mfma_f32_16x16x32_f16 v[38:41], v[86:89], v[82:85], v[38:41]
	v_mfma_f32_16x16x32_f16 v[42:45], v[94:97], v[82:85], v[42:45]
	s_add_u32 s28, s2, 0x680
	s_mov_b32 m0, s14
	s_waitcnt vmcnt(8) lgkmcnt(0)
	s_barrier
	s_addc_u32 s29, s3, 0
	s_add_u32 s30, s4, 0x680
	global_load_lds_dwordx4 v3, s[28:29]
	s_mov_b32 m0, s6
	s_addc_u32 s31, s5, 0
	global_load_lds_dwordx4 v4, s[28:29]
	s_mov_b32 m0, s7
	s_nop 0
	global_load_lds_dwordx4 v3, s[30:31]
	s_mov_b32 m0, s10
	s_nop 0
	global_load_lds_dwordx4 v4, s[30:31]
	s_waitcnt lgkmcnt(0)
	v_mfma_f32_16x16x32_f16 v[54:57], v[90:93], v[46:49], v[54:57]
	v_mfma_f32_16x16x32_f16 v[30:33], v[98:101], v[46:49], v[30:33]
	ds_read_b128 v[46:49], v9
	ds_read_b128 v[74:77], v10
	ds_read_b128 v[78:81], v11
	ds_read_b128 v[82:85], v12
	ds_read_b128 v[86:89], v13
	ds_read_b128 v[94:97], v14
	v_mfma_f32_16x16x32_f16 v[58:61], v[90:93], v[62:65], v[58:61]
	v_mfma_f32_16x16x32_f16 v[50:53], v[98:101], v[62:65], v[50:53]
	v_mfma_f32_16x16x32_f16 v[34:37], v[90:93], v[66:69], v[34:37]
	v_mfma_f32_16x16x32_f16 v[26:29], v[98:101], v[66:69], v[26:29]
	v_mfma_f32_16x16x32_f16 v[38:41], v[90:93], v[70:73], v[38:41]
	v_mfma_f32_16x16x32_f16 v[42:45], v[98:101], v[70:73], v[42:45]
	s_waitcnt lgkmcnt(0)
	v_mfma_f32_16x16x32_f16 v[54:57], v[86:89], v[46:49], v[54:57]
	v_mfma_f32_16x16x32_f16 v[30:33], v[94:97], v[46:49], v[30:33]
	ds_read_b128 v[46:49], v15
	ds_read_b128 v[62:65], v15 offset:2048
	ds_read_b128 v[66:69], v15 offset:4096
	ds_read_b128 v[70:73], v15 offset:6144
	ds_read_b128 v[90:93], v16
	ds_read_b128 v[98:101], v16 offset:2048
	v_mfma_f32_16x16x32_f16 v[58:61], v[86:89], v[74:77], v[58:61]
	v_mfma_f32_16x16x32_f16 v[50:53], v[94:97], v[74:77], v[50:53]
	v_mfma_f32_16x16x32_f16 v[34:37], v[86:89], v[78:81], v[34:37]
	v_mfma_f32_16x16x32_f16 v[26:29], v[94:97], v[78:81], v[26:29]
	v_mfma_f32_16x16x32_f16 v[38:41], v[86:89], v[82:85], v[38:41]
	v_mfma_f32_16x16x32_f16 v[42:45], v[94:97], v[82:85], v[42:45]
	s_add_u32 s28, s2, 0x700
	s_mov_b32 m0, s22
	s_waitcnt vmcnt(8) lgkmcnt(0)
	s_barrier
	s_addc_u32 s29, s3, 0
	s_add_u32 s30, s4, 0x700
	global_load_lds_dwordx4 v3, s[28:29]
	s_mov_b32 m0, s19
	s_addc_u32 s31, s5, 0
	global_load_lds_dwordx4 v4, s[28:29]
	s_mov_b32 m0, s20
	s_nop 0
	global_load_lds_dwordx4 v3, s[30:31]
	s_mov_b32 m0, s21
	s_nop 0
	global_load_lds_dwordx4 v4, s[30:31]
	s_waitcnt lgkmcnt(0)
	v_mfma_f32_16x16x32_f16 v[54:57], v[90:93], v[46:49], v[54:57]
	v_mfma_f32_16x16x32_f16 v[30:33], v[98:101], v[46:49], v[30:33]
	ds_read_b128 v[46:49], v17
	ds_read_b128 v[74:77], v18
	ds_read_b128 v[78:81], v19
	ds_read_b128 v[82:85], v20
	ds_read_b128 v[86:89], v21
	ds_read_b128 v[94:97], v22
	v_mfma_f32_16x16x32_f16 v[58:61], v[90:93], v[62:65], v[58:61]
	v_mfma_f32_16x16x32_f16 v[50:53], v[98:101], v[62:65], v[50:53]
	v_mfma_f32_16x16x32_f16 v[34:37], v[90:93], v[66:69], v[34:37]
	v_mfma_f32_16x16x32_f16 v[26:29], v[98:101], v[66:69], v[26:29]
	v_mfma_f32_16x16x32_f16 v[38:41], v[90:93], v[70:73], v[38:41]
	v_mfma_f32_16x16x32_f16 v[42:45], v[98:101], v[70:73], v[42:45]
	s_waitcnt lgkmcnt(0)
	v_mfma_f32_16x16x32_f16 v[54:57], v[86:89], v[46:49], v[54:57]
	v_mfma_f32_16x16x32_f16 v[30:33], v[94:97], v[46:49], v[30:33]
	ds_read_b128 v[46:49], v23
	ds_read_b128 v[62:65], v23 offset:2048
	ds_read_b128 v[66:69], v23 offset:4096
	ds_read_b128 v[70:73], v23 offset:6144
	ds_read_b128 v[90:93], v24
	ds_read_b128 v[98:101], v24 offset:2048
	v_mfma_f32_16x16x32_f16 v[58:61], v[86:89], v[74:77], v[58:61]
	v_mfma_f32_16x16x32_f16 v[50:53], v[94:97], v[74:77], v[50:53]
	v_mfma_f32_16x16x32_f16 v[34:37], v[86:89], v[78:81], v[34:37]
	v_mfma_f32_16x16x32_f16 v[26:29], v[94:97], v[78:81], v[26:29]
	v_mfma_f32_16x16x32_f16 v[38:41], v[86:89], v[82:85], v[38:41]
	v_mfma_f32_16x16x32_f16 v[42:45], v[94:97], v[82:85], v[42:45]
	s_add_u32 s28, s2, 0x780
	s_mov_b32 m0, s26
	s_waitcnt vmcnt(8) lgkmcnt(0)
	s_barrier
	s_addc_u32 s29, s3, 0
	s_add_u32 s30, s4, 0x780
	global_load_lds_dwordx4 v3, s[28:29]
	s_mov_b32 m0, s23
	s_addc_u32 s31, s5, 0
	global_load_lds_dwordx4 v4, s[28:29]
	s_mov_b32 m0, s24
	s_nop 0
	global_load_lds_dwordx4 v3, s[30:31]
	s_mov_b32 m0, s25
	s_nop 0
	global_load_lds_dwordx4 v4, s[30:31]
	s_waitcnt lgkmcnt(0)
	v_mfma_f32_16x16x32_f16 v[54:57], v[90:93], v[46:49], v[54:57]
	v_mfma_f32_16x16x32_f16 v[30:33], v[98:101], v[46:49], v[30:33]
	ds_read_b128 v[46:49], v7
	ds_read_b128 v[74:77], v7 offset:2048
	ds_read_b128 v[78:81], v7 offset:4096
	ds_read_b128 v[82:85], v7 offset:6144
	ds_read_b128 v[86:89], v5 offset:16384
	ds_read_b128 v[94:97], v5 offset:18432
	v_mfma_f32_16x16x32_f16 v[58:61], v[90:93], v[62:65], v[58:61]
	v_mfma_f32_16x16x32_f16 v[50:53], v[98:101], v[62:65], v[50:53]
	v_mfma_f32_16x16x32_f16 v[34:37], v[90:93], v[66:69], v[34:37]
	v_mfma_f32_16x16x32_f16 v[26:29], v[98:101], v[66:69], v[26:29]
	v_mfma_f32_16x16x32_f16 v[38:41], v[90:93], v[70:73], v[38:41]
	v_mfma_f32_16x16x32_f16 v[42:45], v[98:101], v[70:73], v[42:45]
	s_waitcnt lgkmcnt(0)
	v_mfma_f32_16x16x32_f16 v[54:57], v[86:89], v[46:49], v[54:57]
	v_mfma_f32_16x16x32_f16 v[30:33], v[94:97], v[46:49], v[30:33]
	ds_read_b128 v[46:49], v6
	ds_read_b128 v[62:65], v6 offset:2048
	ds_read_b128 v[66:69], v6 offset:4096
	ds_read_b128 v[70:73], v6 offset:6144
	ds_read_b128 v[90:93], v8 offset:16384
	ds_read_b128 v[98:101], v8 offset:18432
	v_mfma_f32_16x16x32_f16 v[58:61], v[86:89], v[74:77], v[58:61]
	v_mfma_f32_16x16x32_f16 v[50:53], v[94:97], v[74:77], v[50:53]
	v_mfma_f32_16x16x32_f16 v[34:37], v[86:89], v[78:81], v[34:37]
	v_mfma_f32_16x16x32_f16 v[26:29], v[94:97], v[78:81], v[26:29]
	v_mfma_f32_16x16x32_f16 v[38:41], v[86:89], v[82:85], v[38:41]
	v_mfma_f32_16x16x32_f16 v[42:45], v[94:97], v[82:85], v[42:45]
	s_add_u32 s28, s2, 0x800
	s_mov_b32 m0, s18
	s_waitcnt vmcnt(8) lgkmcnt(0)
	s_barrier
	s_addc_u32 s29, s3, 0
	s_add_u32 s30, s4, 0x800
	global_load_lds_dwordx4 v3, s[28:29]
	s_mov_b32 m0, s15
	s_addc_u32 s31, s5, 0
	global_load_lds_dwordx4 v4, s[28:29]
	s_mov_b32 m0, s16
	s_nop 0
	global_load_lds_dwordx4 v3, s[30:31]
	s_mov_b32 m0, s17
	s_nop 0
	global_load_lds_dwordx4 v4, s[30:31]
	s_waitcnt lgkmcnt(0)
	v_mfma_f32_16x16x32_f16 v[54:57], v[90:93], v[46:49], v[54:57]
	v_mfma_f32_16x16x32_f16 v[30:33], v[98:101], v[46:49], v[30:33]
	ds_read_b128 v[46:49], v7 offset:32768
	ds_read_b128 v[74:77], v7 offset:34816
	ds_read_b128 v[78:81], v7 offset:36864
	ds_read_b128 v[82:85], v7 offset:38912
	ds_read_b128 v[86:89], v5 offset:49152
	ds_read_b128 v[94:97], v5 offset:51200
	v_mfma_f32_16x16x32_f16 v[58:61], v[90:93], v[62:65], v[58:61]
	v_mfma_f32_16x16x32_f16 v[50:53], v[98:101], v[62:65], v[50:53]
	v_mfma_f32_16x16x32_f16 v[34:37], v[90:93], v[66:69], v[34:37]
	v_mfma_f32_16x16x32_f16 v[26:29], v[98:101], v[66:69], v[26:29]
	v_mfma_f32_16x16x32_f16 v[38:41], v[90:93], v[70:73], v[38:41]
	v_mfma_f32_16x16x32_f16 v[42:45], v[98:101], v[70:73], v[42:45]
	s_waitcnt lgkmcnt(0)
	v_mfma_f32_16x16x32_f16 v[54:57], v[86:89], v[46:49], v[54:57]
	v_mfma_f32_16x16x32_f16 v[30:33], v[94:97], v[46:49], v[30:33]
	ds_read_b128 v[46:49], v6 offset:32768
	ds_read_b128 v[62:65], v6 offset:34816
	ds_read_b128 v[66:69], v6 offset:36864
	ds_read_b128 v[70:73], v6 offset:38912
	ds_read_b128 v[90:93], v8 offset:49152
	ds_read_b128 v[98:101], v8 offset:51200
	v_mfma_f32_16x16x32_f16 v[58:61], v[86:89], v[74:77], v[58:61]
	v_mfma_f32_16x16x32_f16 v[50:53], v[94:97], v[74:77], v[50:53]
	v_mfma_f32_16x16x32_f16 v[34:37], v[86:89], v[78:81], v[34:37]
	v_mfma_f32_16x16x32_f16 v[26:29], v[94:97], v[78:81], v[26:29]
	v_mfma_f32_16x16x32_f16 v[38:41], v[86:89], v[82:85], v[38:41]
	v_mfma_f32_16x16x32_f16 v[42:45], v[94:97], v[82:85], v[42:45]
	s_add_u32 s28, s2, 0x880
	s_mov_b32 m0, s14
	s_waitcnt vmcnt(8) lgkmcnt(0)
	s_barrier
	s_addc_u32 s29, s3, 0
	s_add_u32 s30, s4, 0x880
	global_load_lds_dwordx4 v3, s[28:29]
	s_mov_b32 m0, s6
	s_addc_u32 s31, s5, 0
	global_load_lds_dwordx4 v4, s[28:29]
	s_mov_b32 m0, s7
	s_nop 0
	global_load_lds_dwordx4 v3, s[30:31]
	s_mov_b32 m0, s10
	s_nop 0
	global_load_lds_dwordx4 v4, s[30:31]
	s_waitcnt lgkmcnt(0)
	v_mfma_f32_16x16x32_f16 v[54:57], v[90:93], v[46:49], v[54:57]
	v_mfma_f32_16x16x32_f16 v[30:33], v[98:101], v[46:49], v[30:33]
	ds_read_b128 v[46:49], v9
	ds_read_b128 v[74:77], v10
	ds_read_b128 v[78:81], v11
	ds_read_b128 v[82:85], v12
	ds_read_b128 v[86:89], v13
	ds_read_b128 v[94:97], v14
	v_mfma_f32_16x16x32_f16 v[58:61], v[90:93], v[62:65], v[58:61]
	v_mfma_f32_16x16x32_f16 v[50:53], v[98:101], v[62:65], v[50:53]
	v_mfma_f32_16x16x32_f16 v[34:37], v[90:93], v[66:69], v[34:37]
	v_mfma_f32_16x16x32_f16 v[26:29], v[98:101], v[66:69], v[26:29]
	v_mfma_f32_16x16x32_f16 v[38:41], v[90:93], v[70:73], v[38:41]
	v_mfma_f32_16x16x32_f16 v[42:45], v[98:101], v[70:73], v[42:45]
	s_waitcnt lgkmcnt(0)
	v_mfma_f32_16x16x32_f16 v[54:57], v[86:89], v[46:49], v[54:57]
	v_mfma_f32_16x16x32_f16 v[30:33], v[94:97], v[46:49], v[30:33]
	ds_read_b128 v[46:49], v15
	ds_read_b128 v[62:65], v15 offset:2048
	ds_read_b128 v[66:69], v15 offset:4096
	ds_read_b128 v[70:73], v15 offset:6144
	ds_read_b128 v[90:93], v16
	ds_read_b128 v[98:101], v16 offset:2048
	v_mfma_f32_16x16x32_f16 v[58:61], v[86:89], v[74:77], v[58:61]
	v_mfma_f32_16x16x32_f16 v[50:53], v[94:97], v[74:77], v[50:53]
	v_mfma_f32_16x16x32_f16 v[34:37], v[86:89], v[78:81], v[34:37]
	v_mfma_f32_16x16x32_f16 v[26:29], v[94:97], v[78:81], v[26:29]
	v_mfma_f32_16x16x32_f16 v[38:41], v[86:89], v[82:85], v[38:41]
	v_mfma_f32_16x16x32_f16 v[42:45], v[94:97], v[82:85], v[42:45]
	s_add_u32 s28, s2, 0x900
	s_mov_b32 m0, s22
	s_waitcnt vmcnt(8) lgkmcnt(0)
	s_barrier
	s_addc_u32 s29, s3, 0
	s_add_u32 s30, s4, 0x900
	global_load_lds_dwordx4 v3, s[28:29]
	s_mov_b32 m0, s19
	s_addc_u32 s31, s5, 0
	global_load_lds_dwordx4 v4, s[28:29]
	s_mov_b32 m0, s20
	s_nop 0
	global_load_lds_dwordx4 v3, s[30:31]
	s_mov_b32 m0, s21
	s_nop 0
	global_load_lds_dwordx4 v4, s[30:31]
	s_waitcnt lgkmcnt(0)
	v_mfma_f32_16x16x32_f16 v[54:57], v[90:93], v[46:49], v[54:57]
	v_mfma_f32_16x16x32_f16 v[30:33], v[98:101], v[46:49], v[30:33]
	ds_read_b128 v[46:49], v17
	ds_read_b128 v[74:77], v18
	ds_read_b128 v[78:81], v19
	ds_read_b128 v[82:85], v20
	ds_read_b128 v[86:89], v21
	ds_read_b128 v[94:97], v22
	v_mfma_f32_16x16x32_f16 v[58:61], v[90:93], v[62:65], v[58:61]
	v_mfma_f32_16x16x32_f16 v[50:53], v[98:101], v[62:65], v[50:53]
	v_mfma_f32_16x16x32_f16 v[34:37], v[90:93], v[66:69], v[34:37]
	v_mfma_f32_16x16x32_f16 v[26:29], v[98:101], v[66:69], v[26:29]
	v_mfma_f32_16x16x32_f16 v[38:41], v[90:93], v[70:73], v[38:41]
	v_mfma_f32_16x16x32_f16 v[42:45], v[98:101], v[70:73], v[42:45]
	s_waitcnt lgkmcnt(0)
	v_mfma_f32_16x16x32_f16 v[54:57], v[86:89], v[46:49], v[54:57]
	v_mfma_f32_16x16x32_f16 v[30:33], v[94:97], v[46:49], v[30:33]
	ds_read_b128 v[46:49], v23
	ds_read_b128 v[62:65], v23 offset:2048
	ds_read_b128 v[66:69], v23 offset:4096
	ds_read_b128 v[70:73], v23 offset:6144
	ds_read_b128 v[90:93], v24
	ds_read_b128 v[98:101], v24 offset:2048
	v_mfma_f32_16x16x32_f16 v[58:61], v[86:89], v[74:77], v[58:61]
	v_mfma_f32_16x16x32_f16 v[50:53], v[94:97], v[74:77], v[50:53]
	v_mfma_f32_16x16x32_f16 v[34:37], v[86:89], v[78:81], v[34:37]
	v_mfma_f32_16x16x32_f16 v[26:29], v[94:97], v[78:81], v[26:29]
	v_mfma_f32_16x16x32_f16 v[38:41], v[86:89], v[82:85], v[38:41]
	v_mfma_f32_16x16x32_f16 v[42:45], v[94:97], v[82:85], v[42:45]
	s_add_u32 s28, s2, 0x980
	s_mov_b32 m0, s26
	s_waitcnt vmcnt(8) lgkmcnt(0)
	s_barrier
	s_addc_u32 s29, s3, 0
	s_add_u32 s30, s4, 0x980
	global_load_lds_dwordx4 v3, s[28:29]
	s_mov_b32 m0, s23
	s_addc_u32 s31, s5, 0
	global_load_lds_dwordx4 v4, s[28:29]
	s_mov_b32 m0, s24
	s_nop 0
	global_load_lds_dwordx4 v3, s[30:31]
	s_mov_b32 m0, s25
	s_nop 0
	global_load_lds_dwordx4 v4, s[30:31]
	s_waitcnt lgkmcnt(0)
	v_mfma_f32_16x16x32_f16 v[54:57], v[90:93], v[46:49], v[54:57]
	v_mfma_f32_16x16x32_f16 v[30:33], v[98:101], v[46:49], v[30:33]
	ds_read_b128 v[46:49], v7
	ds_read_b128 v[74:77], v7 offset:2048
	ds_read_b128 v[78:81], v7 offset:4096
	ds_read_b128 v[82:85], v7 offset:6144
	ds_read_b128 v[86:89], v5 offset:16384
	ds_read_b128 v[94:97], v5 offset:18432
	v_mfma_f32_16x16x32_f16 v[58:61], v[90:93], v[62:65], v[58:61]
	v_mfma_f32_16x16x32_f16 v[50:53], v[98:101], v[62:65], v[50:53]
	v_mfma_f32_16x16x32_f16 v[34:37], v[90:93], v[66:69], v[34:37]
	v_mfma_f32_16x16x32_f16 v[26:29], v[98:101], v[66:69], v[26:29]
	v_mfma_f32_16x16x32_f16 v[38:41], v[90:93], v[70:73], v[38:41]
	v_mfma_f32_16x16x32_f16 v[42:45], v[98:101], v[70:73], v[42:45]
	s_waitcnt lgkmcnt(0)
	v_mfma_f32_16x16x32_f16 v[54:57], v[86:89], v[46:49], v[54:57]
	v_mfma_f32_16x16x32_f16 v[30:33], v[94:97], v[46:49], v[30:33]
	ds_read_b128 v[46:49], v6
	ds_read_b128 v[62:65], v6 offset:2048
	ds_read_b128 v[66:69], v6 offset:4096
	ds_read_b128 v[70:73], v6 offset:6144
	ds_read_b128 v[90:93], v8 offset:16384
	ds_read_b128 v[98:101], v8 offset:18432
	v_mfma_f32_16x16x32_f16 v[58:61], v[86:89], v[74:77], v[58:61]
	v_mfma_f32_16x16x32_f16 v[50:53], v[94:97], v[74:77], v[50:53]
	v_mfma_f32_16x16x32_f16 v[34:37], v[86:89], v[78:81], v[34:37]
	v_mfma_f32_16x16x32_f16 v[26:29], v[94:97], v[78:81], v[26:29]
	v_mfma_f32_16x16x32_f16 v[38:41], v[86:89], v[82:85], v[38:41]
	v_mfma_f32_16x16x32_f16 v[42:45], v[94:97], v[82:85], v[42:45]
	s_add_u32 s28, s2, 0xa00
	s_mov_b32 m0, s18
	s_waitcnt vmcnt(8) lgkmcnt(0)
	s_barrier
	s_addc_u32 s29, s3, 0
	s_add_u32 s30, s4, 0xa00
	global_load_lds_dwordx4 v3, s[28:29]
	s_mov_b32 m0, s15
	s_addc_u32 s31, s5, 0
	global_load_lds_dwordx4 v4, s[28:29]
	s_mov_b32 m0, s16
	s_nop 0
	global_load_lds_dwordx4 v3, s[30:31]
	s_mov_b32 m0, s17
	s_nop 0
	global_load_lds_dwordx4 v4, s[30:31]
	s_waitcnt lgkmcnt(0)
	v_mfma_f32_16x16x32_f16 v[54:57], v[90:93], v[46:49], v[54:57]
	v_mfma_f32_16x16x32_f16 v[30:33], v[98:101], v[46:49], v[30:33]
	ds_read_b128 v[46:49], v7 offset:32768
	ds_read_b128 v[74:77], v7 offset:34816
	ds_read_b128 v[78:81], v7 offset:36864
	ds_read_b128 v[82:85], v7 offset:38912
	ds_read_b128 v[86:89], v5 offset:49152
	ds_read_b128 v[94:97], v5 offset:51200
	v_mfma_f32_16x16x32_f16 v[58:61], v[90:93], v[62:65], v[58:61]
	v_mfma_f32_16x16x32_f16 v[50:53], v[98:101], v[62:65], v[50:53]
	v_mfma_f32_16x16x32_f16 v[34:37], v[90:93], v[66:69], v[34:37]
	v_mfma_f32_16x16x32_f16 v[26:29], v[98:101], v[66:69], v[26:29]
	v_mfma_f32_16x16x32_f16 v[38:41], v[90:93], v[70:73], v[38:41]
	v_mfma_f32_16x16x32_f16 v[42:45], v[98:101], v[70:73], v[42:45]
	s_waitcnt lgkmcnt(0)
	v_mfma_f32_16x16x32_f16 v[54:57], v[86:89], v[46:49], v[54:57]
	v_mfma_f32_16x16x32_f16 v[30:33], v[94:97], v[46:49], v[30:33]
	ds_read_b128 v[46:49], v6 offset:32768
	ds_read_b128 v[62:65], v6 offset:34816
	ds_read_b128 v[66:69], v6 offset:36864
	ds_read_b128 v[70:73], v6 offset:38912
	ds_read_b128 v[90:93], v8 offset:49152
	ds_read_b128 v[98:101], v8 offset:51200
	v_mfma_f32_16x16x32_f16 v[58:61], v[86:89], v[74:77], v[58:61]
	v_mfma_f32_16x16x32_f16 v[50:53], v[94:97], v[74:77], v[50:53]
	v_mfma_f32_16x16x32_f16 v[34:37], v[86:89], v[78:81], v[34:37]
	v_mfma_f32_16x16x32_f16 v[26:29], v[94:97], v[78:81], v[26:29]
	v_mfma_f32_16x16x32_f16 v[38:41], v[86:89], v[82:85], v[38:41]
	v_mfma_f32_16x16x32_f16 v[42:45], v[94:97], v[82:85], v[42:45]
	s_add_u32 s28, s2, 0xa80
	s_mov_b32 m0, s14
	s_waitcnt vmcnt(8) lgkmcnt(0)
	s_barrier
	s_addc_u32 s29, s3, 0
	s_add_u32 s30, s4, 0xa80
	global_load_lds_dwordx4 v3, s[28:29]
	s_mov_b32 m0, s6
	s_addc_u32 s31, s5, 0
	global_load_lds_dwordx4 v4, s[28:29]
	s_mov_b32 m0, s7
	s_nop 0
	global_load_lds_dwordx4 v3, s[30:31]
	s_mov_b32 m0, s10
	s_nop 0
	global_load_lds_dwordx4 v4, s[30:31]
	s_waitcnt lgkmcnt(0)
	v_mfma_f32_16x16x32_f16 v[54:57], v[90:93], v[46:49], v[54:57]
	v_mfma_f32_16x16x32_f16 v[30:33], v[98:101], v[46:49], v[30:33]
	ds_read_b128 v[46:49], v9
	ds_read_b128 v[74:77], v10
	ds_read_b128 v[78:81], v11
	ds_read_b128 v[82:85], v12
	ds_read_b128 v[86:89], v13
	ds_read_b128 v[94:97], v14
	v_mfma_f32_16x16x32_f16 v[58:61], v[90:93], v[62:65], v[58:61]
	v_mfma_f32_16x16x32_f16 v[50:53], v[98:101], v[62:65], v[50:53]
	v_mfma_f32_16x16x32_f16 v[34:37], v[90:93], v[66:69], v[34:37]
	v_mfma_f32_16x16x32_f16 v[26:29], v[98:101], v[66:69], v[26:29]
	v_mfma_f32_16x16x32_f16 v[38:41], v[90:93], v[70:73], v[38:41]
	v_mfma_f32_16x16x32_f16 v[42:45], v[98:101], v[70:73], v[42:45]
	s_waitcnt lgkmcnt(0)
	v_mfma_f32_16x16x32_f16 v[54:57], v[86:89], v[46:49], v[54:57]
	v_mfma_f32_16x16x32_f16 v[30:33], v[94:97], v[46:49], v[30:33]
	ds_read_b128 v[46:49], v15
	ds_read_b128 v[62:65], v15 offset:2048
	ds_read_b128 v[66:69], v15 offset:4096
	ds_read_b128 v[70:73], v15 offset:6144
	ds_read_b128 v[90:93], v16
	ds_read_b128 v[98:101], v16 offset:2048
	v_mfma_f32_16x16x32_f16 v[58:61], v[86:89], v[74:77], v[58:61]
	v_mfma_f32_16x16x32_f16 v[50:53], v[94:97], v[74:77], v[50:53]
	v_mfma_f32_16x16x32_f16 v[34:37], v[86:89], v[78:81], v[34:37]
	v_mfma_f32_16x16x32_f16 v[26:29], v[94:97], v[78:81], v[26:29]
	v_mfma_f32_16x16x32_f16 v[38:41], v[86:89], v[82:85], v[38:41]
	v_mfma_f32_16x16x32_f16 v[42:45], v[94:97], v[82:85], v[42:45]
	s_add_u32 s28, s2, 0xb00
	s_mov_b32 m0, s22
	s_waitcnt vmcnt(8) lgkmcnt(0)
	s_barrier
	s_addc_u32 s29, s3, 0
	s_add_u32 s30, s4, 0xb00
	global_load_lds_dwordx4 v3, s[28:29]
	s_mov_b32 m0, s19
	s_addc_u32 s31, s5, 0
	global_load_lds_dwordx4 v4, s[28:29]
	s_mov_b32 m0, s20
	s_nop 0
	global_load_lds_dwordx4 v3, s[30:31]
	s_mov_b32 m0, s21
	s_nop 0
	global_load_lds_dwordx4 v4, s[30:31]
	s_waitcnt lgkmcnt(0)
	v_mfma_f32_16x16x32_f16 v[54:57], v[90:93], v[46:49], v[54:57]
	v_mfma_f32_16x16x32_f16 v[30:33], v[98:101], v[46:49], v[30:33]
	ds_read_b128 v[46:49], v17
	ds_read_b128 v[74:77], v18
	ds_read_b128 v[78:81], v19
	ds_read_b128 v[82:85], v20
	ds_read_b128 v[86:89], v21
	ds_read_b128 v[94:97], v22
	v_mfma_f32_16x16x32_f16 v[58:61], v[90:93], v[62:65], v[58:61]
	v_mfma_f32_16x16x32_f16 v[50:53], v[98:101], v[62:65], v[50:53]
	v_mfma_f32_16x16x32_f16 v[34:37], v[90:93], v[66:69], v[34:37]
	v_mfma_f32_16x16x32_f16 v[26:29], v[98:101], v[66:69], v[26:29]
	v_mfma_f32_16x16x32_f16 v[38:41], v[90:93], v[70:73], v[38:41]
	v_mfma_f32_16x16x32_f16 v[42:45], v[98:101], v[70:73], v[42:45]
	s_waitcnt lgkmcnt(0)
	v_mfma_f32_16x16x32_f16 v[54:57], v[86:89], v[46:49], v[54:57]
	v_mfma_f32_16x16x32_f16 v[30:33], v[94:97], v[46:49], v[30:33]
	ds_read_b128 v[46:49], v23
	ds_read_b128 v[62:65], v23 offset:2048
	ds_read_b128 v[66:69], v23 offset:4096
	ds_read_b128 v[70:73], v23 offset:6144
	ds_read_b128 v[90:93], v24
	ds_read_b128 v[98:101], v24 offset:2048
	v_mfma_f32_16x16x32_f16 v[58:61], v[86:89], v[74:77], v[58:61]
	v_mfma_f32_16x16x32_f16 v[50:53], v[94:97], v[74:77], v[50:53]
	v_mfma_f32_16x16x32_f16 v[34:37], v[86:89], v[78:81], v[34:37]
	v_mfma_f32_16x16x32_f16 v[26:29], v[94:97], v[78:81], v[26:29]
	v_mfma_f32_16x16x32_f16 v[38:41], v[86:89], v[82:85], v[38:41]
	v_mfma_f32_16x16x32_f16 v[42:45], v[94:97], v[82:85], v[42:45]
	s_add_u32 s28, s2, 0xb80
	s_mov_b32 m0, s26
	s_waitcnt vmcnt(8) lgkmcnt(0)
	s_barrier
	s_addc_u32 s29, s3, 0
	s_add_u32 s30, s4, 0xb80
	global_load_lds_dwordx4 v3, s[28:29]
	s_mov_b32 m0, s23
	s_addc_u32 s31, s5, 0
	global_load_lds_dwordx4 v4, s[28:29]
	s_mov_b32 m0, s24
	s_nop 0
	global_load_lds_dwordx4 v3, s[30:31]
	s_mov_b32 m0, s25
	s_nop 0
	global_load_lds_dwordx4 v4, s[30:31]
	s_waitcnt lgkmcnt(0)
	v_mfma_f32_16x16x32_f16 v[54:57], v[90:93], v[46:49], v[54:57]
	v_mfma_f32_16x16x32_f16 v[30:33], v[98:101], v[46:49], v[30:33]
	ds_read_b128 v[46:49], v7
	ds_read_b128 v[74:77], v7 offset:2048
	ds_read_b128 v[78:81], v7 offset:4096
	ds_read_b128 v[82:85], v7 offset:6144
	ds_read_b128 v[86:89], v5 offset:16384
	ds_read_b128 v[94:97], v5 offset:18432
	v_mfma_f32_16x16x32_f16 v[58:61], v[90:93], v[62:65], v[58:61]
	v_mfma_f32_16x16x32_f16 v[50:53], v[98:101], v[62:65], v[50:53]
	v_mfma_f32_16x16x32_f16 v[34:37], v[90:93], v[66:69], v[34:37]
	v_mfma_f32_16x16x32_f16 v[26:29], v[98:101], v[66:69], v[26:29]
	v_mfma_f32_16x16x32_f16 v[38:41], v[90:93], v[70:73], v[38:41]
	v_mfma_f32_16x16x32_f16 v[42:45], v[98:101], v[70:73], v[42:45]
	s_waitcnt lgkmcnt(0)
	v_mfma_f32_16x16x32_f16 v[54:57], v[86:89], v[46:49], v[54:57]
	v_mfma_f32_16x16x32_f16 v[30:33], v[94:97], v[46:49], v[30:33]
	ds_read_b128 v[46:49], v6
	ds_read_b128 v[62:65], v6 offset:2048
	ds_read_b128 v[66:69], v6 offset:4096
	ds_read_b128 v[70:73], v6 offset:6144
	ds_read_b128 v[90:93], v8 offset:16384
	ds_read_b128 v[98:101], v8 offset:18432
	v_mfma_f32_16x16x32_f16 v[58:61], v[86:89], v[74:77], v[58:61]
	v_mfma_f32_16x16x32_f16 v[50:53], v[94:97], v[74:77], v[50:53]
	v_mfma_f32_16x16x32_f16 v[34:37], v[86:89], v[78:81], v[34:37]
	v_mfma_f32_16x16x32_f16 v[26:29], v[94:97], v[78:81], v[26:29]
	v_mfma_f32_16x16x32_f16 v[38:41], v[86:89], v[82:85], v[38:41]
	v_mfma_f32_16x16x32_f16 v[42:45], v[94:97], v[82:85], v[42:45]
	s_add_u32 s28, s2, 0xc00
	s_mov_b32 m0, s18
	s_waitcnt vmcnt(8) lgkmcnt(0)
	s_barrier
	s_addc_u32 s29, s3, 0
	s_add_u32 s30, s4, 0xc00
	global_load_lds_dwordx4 v3, s[28:29]
	s_mov_b32 m0, s15
	s_addc_u32 s31, s5, 0
	global_load_lds_dwordx4 v4, s[28:29]
	s_mov_b32 m0, s16
	s_nop 0
	global_load_lds_dwordx4 v3, s[30:31]
	s_mov_b32 m0, s17
	s_nop 0
	global_load_lds_dwordx4 v4, s[30:31]
	s_waitcnt lgkmcnt(0)
	v_mfma_f32_16x16x32_f16 v[54:57], v[90:93], v[46:49], v[54:57]
	v_mfma_f32_16x16x32_f16 v[30:33], v[98:101], v[46:49], v[30:33]
	ds_read_b128 v[46:49], v7 offset:32768
	ds_read_b128 v[74:77], v7 offset:34816
	ds_read_b128 v[78:81], v7 offset:36864
	ds_read_b128 v[82:85], v7 offset:38912
	ds_read_b128 v[86:89], v5 offset:49152
	ds_read_b128 v[94:97], v5 offset:51200
	v_mfma_f32_16x16x32_f16 v[58:61], v[90:93], v[62:65], v[58:61]
	v_mfma_f32_16x16x32_f16 v[50:53], v[98:101], v[62:65], v[50:53]
	v_mfma_f32_16x16x32_f16 v[34:37], v[90:93], v[66:69], v[34:37]
	v_mfma_f32_16x16x32_f16 v[26:29], v[98:101], v[66:69], v[26:29]
	v_mfma_f32_16x16x32_f16 v[38:41], v[90:93], v[70:73], v[38:41]
	v_mfma_f32_16x16x32_f16 v[42:45], v[98:101], v[70:73], v[42:45]
	s_waitcnt lgkmcnt(0)
	v_mfma_f32_16x16x32_f16 v[54:57], v[86:89], v[46:49], v[54:57]
	v_mfma_f32_16x16x32_f16 v[30:33], v[94:97], v[46:49], v[30:33]
	ds_read_b128 v[46:49], v6 offset:32768
	ds_read_b128 v[62:65], v6 offset:34816
	ds_read_b128 v[66:69], v6 offset:36864
	ds_read_b128 v[70:73], v6 offset:38912
	ds_read_b128 v[90:93], v8 offset:49152
	ds_read_b128 v[98:101], v8 offset:51200
	v_mfma_f32_16x16x32_f16 v[58:61], v[86:89], v[74:77], v[58:61]
	v_mfma_f32_16x16x32_f16 v[50:53], v[94:97], v[74:77], v[50:53]
	v_mfma_f32_16x16x32_f16 v[34:37], v[86:89], v[78:81], v[34:37]
	v_mfma_f32_16x16x32_f16 v[26:29], v[94:97], v[78:81], v[26:29]
	v_mfma_f32_16x16x32_f16 v[38:41], v[86:89], v[82:85], v[38:41]
	v_mfma_f32_16x16x32_f16 v[42:45], v[94:97], v[82:85], v[42:45]
	s_add_u32 s28, s2, 0xc80
	s_mov_b32 m0, s14
	s_waitcnt vmcnt(8) lgkmcnt(0)
	s_barrier
	s_addc_u32 s29, s3, 0
	s_add_u32 s30, s4, 0xc80
	global_load_lds_dwordx4 v3, s[28:29]
	s_mov_b32 m0, s6
	s_addc_u32 s31, s5, 0
	global_load_lds_dwordx4 v4, s[28:29]
	s_mov_b32 m0, s7
	s_nop 0
	global_load_lds_dwordx4 v3, s[30:31]
	s_mov_b32 m0, s10
	s_nop 0
	global_load_lds_dwordx4 v4, s[30:31]
	s_waitcnt lgkmcnt(0)
	v_mfma_f32_16x16x32_f16 v[54:57], v[90:93], v[46:49], v[54:57]
	v_mfma_f32_16x16x32_f16 v[30:33], v[98:101], v[46:49], v[30:33]
	ds_read_b128 v[46:49], v9
	ds_read_b128 v[74:77], v10
	ds_read_b128 v[78:81], v11
	ds_read_b128 v[82:85], v12
	ds_read_b128 v[86:89], v13
	ds_read_b128 v[94:97], v14
	v_mfma_f32_16x16x32_f16 v[58:61], v[90:93], v[62:65], v[58:61]
	v_mfma_f32_16x16x32_f16 v[50:53], v[98:101], v[62:65], v[50:53]
	v_mfma_f32_16x16x32_f16 v[34:37], v[90:93], v[66:69], v[34:37]
	v_mfma_f32_16x16x32_f16 v[26:29], v[98:101], v[66:69], v[26:29]
	v_mfma_f32_16x16x32_f16 v[38:41], v[90:93], v[70:73], v[38:41]
	v_mfma_f32_16x16x32_f16 v[42:45], v[98:101], v[70:73], v[42:45]
	s_waitcnt lgkmcnt(0)
	v_mfma_f32_16x16x32_f16 v[54:57], v[86:89], v[46:49], v[54:57]
	v_mfma_f32_16x16x32_f16 v[30:33], v[94:97], v[46:49], v[30:33]
	ds_read_b128 v[46:49], v15
	ds_read_b128 v[62:65], v15 offset:2048
	ds_read_b128 v[66:69], v15 offset:4096
	ds_read_b128 v[70:73], v15 offset:6144
	ds_read_b128 v[90:93], v16
	ds_read_b128 v[98:101], v16 offset:2048
	v_mfma_f32_16x16x32_f16 v[58:61], v[86:89], v[74:77], v[58:61]
	v_mfma_f32_16x16x32_f16 v[50:53], v[94:97], v[74:77], v[50:53]
	v_mfma_f32_16x16x32_f16 v[34:37], v[86:89], v[78:81], v[34:37]
	v_mfma_f32_16x16x32_f16 v[26:29], v[94:97], v[78:81], v[26:29]
	v_mfma_f32_16x16x32_f16 v[38:41], v[86:89], v[82:85], v[38:41]
	v_mfma_f32_16x16x32_f16 v[42:45], v[94:97], v[82:85], v[42:45]
	s_add_u32 s28, s2, 0xd00
	s_mov_b32 m0, s22
	s_waitcnt vmcnt(8) lgkmcnt(0)
	s_barrier
	s_addc_u32 s29, s3, 0
	s_add_u32 s30, s4, 0xd00
	global_load_lds_dwordx4 v3, s[28:29]
	s_mov_b32 m0, s19
	s_addc_u32 s31, s5, 0
	global_load_lds_dwordx4 v4, s[28:29]
	s_mov_b32 m0, s20
	s_nop 0
	global_load_lds_dwordx4 v3, s[30:31]
	s_mov_b32 m0, s21
	s_nop 0
	global_load_lds_dwordx4 v4, s[30:31]
	s_waitcnt lgkmcnt(0)
	v_mfma_f32_16x16x32_f16 v[54:57], v[90:93], v[46:49], v[54:57]
	v_mfma_f32_16x16x32_f16 v[30:33], v[98:101], v[46:49], v[30:33]
	ds_read_b128 v[46:49], v17
	ds_read_b128 v[74:77], v18
	ds_read_b128 v[78:81], v19
	ds_read_b128 v[82:85], v20
	ds_read_b128 v[86:89], v21
	ds_read_b128 v[94:97], v22
	v_mfma_f32_16x16x32_f16 v[58:61], v[90:93], v[62:65], v[58:61]
	v_mfma_f32_16x16x32_f16 v[50:53], v[98:101], v[62:65], v[50:53]
	v_mfma_f32_16x16x32_f16 v[34:37], v[90:93], v[66:69], v[34:37]
	v_mfma_f32_16x16x32_f16 v[26:29], v[98:101], v[66:69], v[26:29]
	v_mfma_f32_16x16x32_f16 v[38:41], v[90:93], v[70:73], v[38:41]
	v_mfma_f32_16x16x32_f16 v[42:45], v[98:101], v[70:73], v[42:45]
	s_waitcnt lgkmcnt(0)
	v_mfma_f32_16x16x32_f16 v[54:57], v[86:89], v[46:49], v[54:57]
	v_mfma_f32_16x16x32_f16 v[30:33], v[94:97], v[46:49], v[30:33]
	ds_read_b128 v[46:49], v23
	ds_read_b128 v[62:65], v23 offset:2048
	ds_read_b128 v[66:69], v23 offset:4096
	ds_read_b128 v[70:73], v23 offset:6144
	ds_read_b128 v[90:93], v24
	ds_read_b128 v[98:101], v24 offset:2048
	v_mfma_f32_16x16x32_f16 v[58:61], v[86:89], v[74:77], v[58:61]
	v_mfma_f32_16x16x32_f16 v[50:53], v[94:97], v[74:77], v[50:53]
	v_mfma_f32_16x16x32_f16 v[34:37], v[86:89], v[78:81], v[34:37]
	v_mfma_f32_16x16x32_f16 v[26:29], v[94:97], v[78:81], v[26:29]
	v_mfma_f32_16x16x32_f16 v[38:41], v[86:89], v[82:85], v[38:41]
	v_mfma_f32_16x16x32_f16 v[42:45], v[94:97], v[82:85], v[42:45]
	s_add_u32 s28, s2, 0xd80
	s_mov_b32 m0, s26
	s_waitcnt vmcnt(8) lgkmcnt(0)
	s_barrier
	s_addc_u32 s29, s3, 0
	s_add_u32 s30, s4, 0xd80
	global_load_lds_dwordx4 v3, s[28:29]
	s_mov_b32 m0, s23
	s_addc_u32 s31, s5, 0
	global_load_lds_dwordx4 v4, s[28:29]
	s_mov_b32 m0, s24
	s_nop 0
	global_load_lds_dwordx4 v3, s[30:31]
	s_mov_b32 m0, s25
	s_nop 0
	global_load_lds_dwordx4 v4, s[30:31]
	s_waitcnt lgkmcnt(0)
	v_mfma_f32_16x16x32_f16 v[54:57], v[90:93], v[46:49], v[54:57]
	v_mfma_f32_16x16x32_f16 v[30:33], v[98:101], v[46:49], v[30:33]
	ds_read_b128 v[46:49], v7
	ds_read_b128 v[74:77], v7 offset:2048
	ds_read_b128 v[78:81], v7 offset:4096
	ds_read_b128 v[82:85], v7 offset:6144
	ds_read_b128 v[86:89], v5 offset:16384
	ds_read_b128 v[94:97], v5 offset:18432
	v_mfma_f32_16x16x32_f16 v[58:61], v[90:93], v[62:65], v[58:61]
	v_mfma_f32_16x16x32_f16 v[50:53], v[98:101], v[62:65], v[50:53]
	v_mfma_f32_16x16x32_f16 v[34:37], v[90:93], v[66:69], v[34:37]
	v_mfma_f32_16x16x32_f16 v[26:29], v[98:101], v[66:69], v[26:29]
	v_mfma_f32_16x16x32_f16 v[38:41], v[90:93], v[70:73], v[38:41]
	v_mfma_f32_16x16x32_f16 v[42:45], v[98:101], v[70:73], v[42:45]
	s_waitcnt lgkmcnt(0)
	v_mfma_f32_16x16x32_f16 v[54:57], v[86:89], v[46:49], v[54:57]
	v_mfma_f32_16x16x32_f16 v[30:33], v[94:97], v[46:49], v[30:33]
	ds_read_b128 v[46:49], v6
	ds_read_b128 v[62:65], v6 offset:2048
	ds_read_b128 v[66:69], v6 offset:4096
	ds_read_b128 v[70:73], v6 offset:6144
	ds_read_b128 v[90:93], v8 offset:16384
	ds_read_b128 v[98:101], v8 offset:18432
	v_mfma_f32_16x16x32_f16 v[58:61], v[86:89], v[74:77], v[58:61]
	v_mfma_f32_16x16x32_f16 v[50:53], v[94:97], v[74:77], v[50:53]
	v_mfma_f32_16x16x32_f16 v[34:37], v[86:89], v[78:81], v[34:37]
	v_mfma_f32_16x16x32_f16 v[26:29], v[94:97], v[78:81], v[26:29]
	v_mfma_f32_16x16x32_f16 v[38:41], v[86:89], v[82:85], v[38:41]
	v_mfma_f32_16x16x32_f16 v[42:45], v[94:97], v[82:85], v[42:45]
	s_add_u32 s28, s2, 0xe00
	s_mov_b32 m0, s18
	s_waitcnt vmcnt(8) lgkmcnt(0)
	s_barrier
	s_addc_u32 s29, s3, 0
	s_add_u32 s30, s4, 0xe00
	global_load_lds_dwordx4 v3, s[28:29]
	s_mov_b32 m0, s15
	s_addc_u32 s31, s5, 0
	global_load_lds_dwordx4 v4, s[28:29]
	s_mov_b32 m0, s16
	s_nop 0
	global_load_lds_dwordx4 v3, s[30:31]
	s_mov_b32 m0, s17
	s_nop 0
	global_load_lds_dwordx4 v4, s[30:31]
	s_waitcnt lgkmcnt(0)
	v_mfma_f32_16x16x32_f16 v[54:57], v[90:93], v[46:49], v[54:57]
	v_mfma_f32_16x16x32_f16 v[30:33], v[98:101], v[46:49], v[30:33]
	ds_read_b128 v[46:49], v7 offset:32768
	ds_read_b128 v[74:77], v7 offset:34816
	ds_read_b128 v[78:81], v7 offset:36864
	ds_read_b128 v[82:85], v7 offset:38912
	ds_read_b128 v[86:89], v5 offset:49152
	ds_read_b128 v[94:97], v5 offset:51200
	v_mfma_f32_16x16x32_f16 v[58:61], v[90:93], v[62:65], v[58:61]
	v_mfma_f32_16x16x32_f16 v[50:53], v[98:101], v[62:65], v[50:53]
	v_mfma_f32_16x16x32_f16 v[34:37], v[90:93], v[66:69], v[34:37]
	v_mfma_f32_16x16x32_f16 v[26:29], v[98:101], v[66:69], v[26:29]
	v_mfma_f32_16x16x32_f16 v[38:41], v[90:93], v[70:73], v[38:41]
	v_mfma_f32_16x16x32_f16 v[42:45], v[98:101], v[70:73], v[42:45]
	s_waitcnt lgkmcnt(0)
	v_mfma_f32_16x16x32_f16 v[54:57], v[86:89], v[46:49], v[54:57]
	v_mfma_f32_16x16x32_f16 v[30:33], v[94:97], v[46:49], v[30:33]
	ds_read_b128 v[46:49], v6 offset:32768
	ds_read_b128 v[62:65], v6 offset:34816
	ds_read_b128 v[66:69], v6 offset:36864
	ds_read_b128 v[70:73], v6 offset:38912
	ds_read_b128 v[90:93], v8 offset:49152
	ds_read_b128 v[98:101], v8 offset:51200
	v_mfma_f32_16x16x32_f16 v[58:61], v[86:89], v[74:77], v[58:61]
	v_mfma_f32_16x16x32_f16 v[50:53], v[94:97], v[74:77], v[50:53]
	v_mfma_f32_16x16x32_f16 v[34:37], v[86:89], v[78:81], v[34:37]
	v_mfma_f32_16x16x32_f16 v[26:29], v[94:97], v[78:81], v[26:29]
	v_mfma_f32_16x16x32_f16 v[38:41], v[86:89], v[82:85], v[38:41]
	v_mfma_f32_16x16x32_f16 v[42:45], v[94:97], v[82:85], v[42:45]
	s_mov_b32 m0, s14
	s_add_u32 s14, s2, 0xe80
	s_waitcnt vmcnt(8) lgkmcnt(0)
	s_barrier
	s_addc_u32 s15, s3, 0
	s_add_u32 s16, s4, 0xe80
	global_load_lds_dwordx4 v3, s[14:15]
	s_mov_b32 m0, s6
	s_addc_u32 s17, s5, 0
	global_load_lds_dwordx4 v4, s[14:15]
	s_mov_b32 m0, s7
	s_nop 0
	global_load_lds_dwordx4 v3, s[16:17]
	s_mov_b32 m0, s10
	s_nop 0
	global_load_lds_dwordx4 v4, s[16:17]
	s_waitcnt lgkmcnt(0)
	v_mfma_f32_16x16x32_f16 v[54:57], v[90:93], v[46:49], v[54:57]
	v_mfma_f32_16x16x32_f16 v[30:33], v[98:101], v[46:49], v[30:33]
	ds_read_b128 v[46:49], v9
	ds_read_b128 v[74:77], v10
	ds_read_b128 v[78:81], v11
	ds_read_b128 v[82:85], v12
	ds_read_b128 v[86:89], v13
	ds_read_b128 v[94:97], v14
	v_mfma_f32_16x16x32_f16 v[58:61], v[90:93], v[62:65], v[58:61]
	v_mfma_f32_16x16x32_f16 v[50:53], v[98:101], v[62:65], v[50:53]
	v_mfma_f32_16x16x32_f16 v[34:37], v[90:93], v[66:69], v[34:37]
	v_mfma_f32_16x16x32_f16 v[26:29], v[98:101], v[66:69], v[26:29]
	v_mfma_f32_16x16x32_f16 v[38:41], v[90:93], v[70:73], v[38:41]
	v_mfma_f32_16x16x32_f16 v[42:45], v[98:101], v[70:73], v[42:45]
	s_waitcnt lgkmcnt(0)
	v_mfma_f32_16x16x32_f16 v[54:57], v[86:89], v[46:49], v[54:57]
	v_mfma_f32_16x16x32_f16 v[30:33], v[94:97], v[46:49], v[30:33]
	ds_read_b128 v[46:49], v15
	ds_read_b128 v[62:65], v15 offset:2048
	ds_read_b128 v[66:69], v15 offset:4096
	ds_read_b128 v[70:73], v15 offset:6144
	ds_read_b128 v[90:93], v16
	ds_read_b128 v[98:101], v16 offset:2048
	v_mfma_f32_16x16x32_f16 v[58:61], v[86:89], v[74:77], v[58:61]
	v_mfma_f32_16x16x32_f16 v[50:53], v[94:97], v[74:77], v[50:53]
	v_mfma_f32_16x16x32_f16 v[34:37], v[86:89], v[78:81], v[34:37]
	v_mfma_f32_16x16x32_f16 v[26:29], v[94:97], v[78:81], v[26:29]
	v_mfma_f32_16x16x32_f16 v[38:41], v[86:89], v[82:85], v[38:41]
	v_mfma_f32_16x16x32_f16 v[42:45], v[94:97], v[82:85], v[42:45]
	s_add_u32 s6, s2, 0xf00
	s_mov_b32 m0, s22
	s_waitcnt vmcnt(8) lgkmcnt(0)
	s_barrier
	s_addc_u32 s7, s3, 0
	s_add_u32 s14, s4, 0xf00
	global_load_lds_dwordx4 v3, s[6:7]
	s_mov_b32 m0, s19
	s_addc_u32 s15, s5, 0
	global_load_lds_dwordx4 v4, s[6:7]
	s_mov_b32 m0, s20
	s_nop 0
	global_load_lds_dwordx4 v3, s[14:15]
	s_mov_b32 m0, s21
	s_nop 0
	global_load_lds_dwordx4 v4, s[14:15]
	s_waitcnt lgkmcnt(0)
	v_mfma_f32_16x16x32_f16 v[54:57], v[90:93], v[46:49], v[54:57]
	v_mfma_f32_16x16x32_f16 v[30:33], v[98:101], v[46:49], v[30:33]
	ds_read_b128 v[46:49], v17
	ds_read_b128 v[74:77], v18
	ds_read_b128 v[78:81], v19
	ds_read_b128 v[82:85], v20
	ds_read_b128 v[86:89], v21
	ds_read_b128 v[94:97], v22
	v_mfma_f32_16x16x32_f16 v[58:61], v[90:93], v[62:65], v[58:61]
	v_mfma_f32_16x16x32_f16 v[50:53], v[98:101], v[62:65], v[50:53]
	v_mfma_f32_16x16x32_f16 v[34:37], v[90:93], v[66:69], v[34:37]
	v_mfma_f32_16x16x32_f16 v[26:29], v[98:101], v[66:69], v[26:29]
	v_mfma_f32_16x16x32_f16 v[38:41], v[90:93], v[70:73], v[38:41]
	v_mfma_f32_16x16x32_f16 v[42:45], v[98:101], v[70:73], v[42:45]
	s_waitcnt lgkmcnt(0)
	v_mfma_f32_16x16x32_f16 v[54:57], v[86:89], v[46:49], v[54:57]
	v_mfma_f32_16x16x32_f16 v[30:33], v[94:97], v[46:49], v[30:33]
	ds_read_b128 v[46:49], v23
	ds_read_b128 v[62:65], v23 offset:2048
	ds_read_b128 v[66:69], v23 offset:4096
	ds_read_b128 v[70:73], v23 offset:6144
	ds_read_b128 v[90:93], v24
	ds_read_b128 v[98:101], v24 offset:2048
	v_mfma_f32_16x16x32_f16 v[58:61], v[86:89], v[74:77], v[58:61]
	v_mfma_f32_16x16x32_f16 v[50:53], v[94:97], v[74:77], v[50:53]
	v_mfma_f32_16x16x32_f16 v[34:37], v[86:89], v[78:81], v[34:37]
	v_mfma_f32_16x16x32_f16 v[26:29], v[94:97], v[78:81], v[26:29]
	v_mfma_f32_16x16x32_f16 v[38:41], v[86:89], v[82:85], v[38:41]
	v_mfma_f32_16x16x32_f16 v[42:45], v[94:97], v[82:85], v[42:45]
	s_add_u32 s2, s2, 0xf80
	s_mov_b32 m0, s26
	s_waitcnt vmcnt(8) lgkmcnt(0)
	s_barrier
	s_addc_u32 s3, s3, 0
	s_add_u32 s4, s4, 0xf80
	global_load_lds_dwordx4 v3, s[2:3]
	s_mov_b32 m0, s23
	s_addc_u32 s5, s5, 0
	global_load_lds_dwordx4 v4, s[2:3]
	s_mov_b32 m0, s24
	s_nop 0
	global_load_lds_dwordx4 v3, s[4:5]
	s_mov_b32 m0, s25
	s_nop 0
	global_load_lds_dwordx4 v4, s[4:5]
	s_waitcnt lgkmcnt(0)
	v_mfma_f32_16x16x32_f16 v[54:57], v[90:93], v[46:49], v[54:57]
	v_mfma_f32_16x16x32_f16 v[30:33], v[98:101], v[46:49], v[30:33]
	ds_read_b128 v[46:49], v7
	ds_read_b128 v[74:77], v7 offset:2048
	ds_read_b128 v[78:81], v7 offset:4096
	ds_read_b128 v[82:85], v7 offset:6144
	ds_read_b128 v[86:89], v5 offset:16384
	ds_read_b128 v[94:97], v5 offset:18432
	v_mfma_f32_16x16x32_f16 v[58:61], v[90:93], v[62:65], v[58:61]
	v_mfma_f32_16x16x32_f16 v[50:53], v[98:101], v[62:65], v[50:53]
	v_mfma_f32_16x16x32_f16 v[34:37], v[90:93], v[66:69], v[34:37]
	v_mfma_f32_16x16x32_f16 v[26:29], v[98:101], v[66:69], v[26:29]
	v_mfma_f32_16x16x32_f16 v[38:41], v[90:93], v[70:73], v[38:41]
	v_mfma_f32_16x16x32_f16 v[42:45], v[98:101], v[70:73], v[42:45]
	s_waitcnt lgkmcnt(0)
	v_mfma_f32_16x16x32_f16 v[54:57], v[86:89], v[46:49], v[54:57]
	v_mfma_f32_16x16x32_f16 v[30:33], v[94:97], v[46:49], v[30:33]
	ds_read_b128 v[46:49], v6
	ds_read_b128 v[62:65], v6 offset:2048
	ds_read_b128 v[66:69], v6 offset:4096
	ds_read_b128 v[70:73], v6 offset:6144
	ds_read_b128 v[90:93], v8 offset:16384
	ds_read_b128 v[98:101], v8 offset:18432
	v_mfma_f32_16x16x32_f16 v[58:61], v[86:89], v[74:77], v[58:61]
	v_mfma_f32_16x16x32_f16 v[50:53], v[94:97], v[74:77], v[50:53]
	v_mfma_f32_16x16x32_f16 v[34:37], v[86:89], v[78:81], v[34:37]
	v_mfma_f32_16x16x32_f16 v[26:29], v[94:97], v[78:81], v[26:29]
	v_mfma_f32_16x16x32_f16 v[38:41], v[86:89], v[82:85], v[38:41]
	v_mfma_f32_16x16x32_f16 v[42:45], v[94:97], v[82:85], v[42:45]
	s_waitcnt vmcnt(8) lgkmcnt(0)
	s_barrier
	s_waitcnt lgkmcnt(0)
	v_mfma_f32_16x16x32_f16 v[54:57], v[90:93], v[46:49], v[54:57]
	v_mfma_f32_16x16x32_f16 v[30:33], v[98:101], v[46:49], v[30:33]
	ds_read_b128 v[46:49], v7 offset:32768
	ds_read_b128 v[74:77], v7 offset:34816
	ds_read_b128 v[78:81], v7 offset:36864
	ds_read_b128 v[82:85], v7 offset:38912
	ds_read_b128 v[86:89], v5 offset:49152
	ds_read_b128 v[94:97], v5 offset:51200
	v_mfma_f32_16x16x32_f16 v[58:61], v[90:93], v[62:65], v[58:61]
	v_mfma_f32_16x16x32_f16 v[50:53], v[98:101], v[62:65], v[50:53]
	v_mfma_f32_16x16x32_f16 v[34:37], v[90:93], v[66:69], v[34:37]
	v_mfma_f32_16x16x32_f16 v[26:29], v[98:101], v[66:69], v[26:29]
	v_mfma_f32_16x16x32_f16 v[38:41], v[90:93], v[70:73], v[38:41]
	v_mfma_f32_16x16x32_f16 v[42:45], v[98:101], v[70:73], v[42:45]
	s_waitcnt lgkmcnt(0)
	v_mfma_f32_16x16x32_f16 v[54:57], v[86:89], v[46:49], v[54:57]
	v_mfma_f32_16x16x32_f16 v[30:33], v[94:97], v[46:49], v[30:33]
	ds_read_b128 v[46:49], v6 offset:32768
	ds_read_b128 v[62:65], v6 offset:34816
	ds_read_b128 v[66:69], v6 offset:36864
	ds_read_b128 v[4:7], v6 offset:38912
	ds_read_b128 v[70:73], v8 offset:49152
	ds_read_b128 v[90:93], v8 offset:51200
	v_mfma_f32_16x16x32_f16 v[58:61], v[86:89], v[74:77], v[58:61]
	v_mfma_f32_16x16x32_f16 v[50:53], v[94:97], v[74:77], v[50:53]
	v_mfma_f32_16x16x32_f16 v[34:37], v[86:89], v[78:81], v[34:37]
	v_mfma_f32_16x16x32_f16 v[26:29], v[94:97], v[78:81], v[26:29]
	v_mfma_f32_16x16x32_f16 v[38:41], v[86:89], v[82:85], v[38:41]
	v_mfma_f32_16x16x32_f16 v[42:45], v[94:97], v[82:85], v[42:45]
	s_waitcnt vmcnt(0) lgkmcnt(0)
	s_barrier
	s_waitcnt lgkmcnt(0)
	v_mfma_f32_16x16x32_f16 v[54:57], v[70:73], v[46:49], v[54:57]
	v_mfma_f32_16x16x32_f16 v[30:33], v[90:93], v[46:49], v[30:33]
	ds_read_b128 v[46:49], v9
	ds_read_b128 v[74:77], v10
	ds_read_b128 v[8:11], v11
	ds_read_b128 v[78:81], v12
	ds_read_b128 v[82:85], v13
	ds_read_b128 v[86:89], v14
	v_mfma_f32_16x16x32_f16 v[58:61], v[70:73], v[62:65], v[58:61]
	v_mfma_f32_16x16x32_f16 v[50:53], v[90:93], v[62:65], v[50:53]
	v_mfma_f32_16x16x32_f16 v[34:37], v[70:73], v[66:69], v[34:37]
	v_mfma_f32_16x16x32_f16 v[26:29], v[90:93], v[66:69], v[26:29]
	v_mfma_f32_16x16x32_f16 v[38:41], v[70:73], v[4:7], v[38:41]
	v_mfma_f32_16x16x32_f16 v[4:7], v[90:93], v[4:7], v[42:45]
	s_waitcnt lgkmcnt(0)
	v_mfma_f32_16x16x32_f16 v[42:45], v[82:85], v[46:49], v[54:57]
	v_mfma_f32_16x16x32_f16 v[30:33], v[86:89], v[46:49], v[30:33]
	ds_read_b128 v[46:49], v15
	s_nop 0
	ds_read_b128 v[54:57], v15 offset:2048
	ds_read_b128 v[62:65], v15 offset:4096
	ds_read_b128 v[12:15], v15 offset:6144
	ds_read_b128 v[66:69], v16
	ds_read_b128 v[70:73], v16 offset:2048
	v_mfma_f32_16x16x32_f16 v[58:61], v[82:85], v[74:77], v[58:61]
	v_mfma_f32_16x16x32_f16 v[50:53], v[86:89], v[74:77], v[50:53]
	v_mfma_f32_16x16x32_f16 v[34:37], v[82:85], v[8:11], v[34:37]
	v_mfma_f32_16x16x32_f16 v[8:11], v[86:89], v[8:11], v[26:29]
	v_mfma_f32_16x16x32_f16 v[26:29], v[82:85], v[78:81], v[38:41]
	v_mfma_f32_16x16x32_f16 v[4:7], v[86:89], v[78:81], v[4:7]
	s_waitcnt vmcnt(0) lgkmcnt(0)
	s_barrier
	s_waitcnt lgkmcnt(0)
	v_mfma_f32_16x16x32_f16 v[38:41], v[66:69], v[46:49], v[42:45]
	v_mfma_f32_16x16x32_f16 v[30:33], v[70:73], v[46:49], v[30:33]
	s_nop 1
	ds_read_b128 v[42:45], v17
	ds_read_b128 v[46:49], v18
	ds_read_b128 v[16:19], v19
	ds_read_b128 v[74:77], v20
	ds_read_b128 v[78:81], v21
	ds_read_b128 v[82:85], v22
	v_mfma_f32_16x16x32_f16 v[58:61], v[66:69], v[54:57], v[58:61]
	v_mfma_f32_16x16x32_f16 v[50:53], v[70:73], v[54:57], v[50:53]
	v_mfma_f32_16x16x32_f16 v[34:37], v[66:69], v[62:65], v[34:37]
	v_mfma_f32_16x16x32_f16 v[8:11], v[70:73], v[62:65], v[8:11]
	v_mfma_f32_16x16x32_f16 v[26:29], v[66:69], v[12:15], v[26:29]
	v_mfma_f32_16x16x32_f16 v[4:7], v[70:73], v[12:15], v[4:7]
	s_waitcnt lgkmcnt(0)
	v_mfma_f32_16x16x32_f16 v[12:15], v[78:81], v[42:45], v[38:41]
	v_mfma_f32_16x16x32_f16 v[30:33], v[82:85], v[42:45], v[30:33]
	s_nop 1
	ds_read_b128 v[38:41], v23
	ds_read_b128 v[42:45], v23 offset:2048
	ds_read_b128 v[54:57], v23 offset:4096
	ds_read_b128 v[20:23], v23 offset:6144
	ds_read_b128 v[62:65], v24
	ds_read_b128 v[66:69], v24 offset:2048
	v_mfma_f32_16x16x32_f16 v[58:61], v[78:81], v[46:49], v[58:61]
	v_mfma_f32_16x16x32_f16 v[46:49], v[82:85], v[46:49], v[50:53]
	v_mfma_f32_16x16x32_f16 v[34:37], v[78:81], v[16:19], v[34:37]
	v_mfma_f32_16x16x32_f16 v[8:11], v[82:85], v[16:19], v[8:11]
	v_mfma_f32_16x16x32_f16 v[16:19], v[78:81], v[74:77], v[26:29]
	v_mfma_f32_16x16x32_f16 v[4:7], v[82:85], v[74:77], v[4:7]
	s_waitcnt lgkmcnt(0)
	v_mfma_f32_16x16x32_f16 v[12:15], v[62:65], v[38:41], v[12:15]
	v_mfma_f32_16x16x32_f16 v[24:27], v[66:69], v[38:41], v[30:33]
	v_mfma_f32_16x16x32_f16 v[28:31], v[62:65], v[42:45], v[58:61]
	v_mfma_f32_16x16x32_f16 v[38:41], v[66:69], v[42:45], v[46:49]
	v_mfma_f32_16x16x32_f16 v[32:35], v[62:65], v[54:57], v[34:37]
	v_mfma_f32_16x16x32_f16 v[8:11], v[66:69], v[54:57], v[8:11]
	v_mfma_f32_16x16x32_f16 v[16:19], v[62:65], v[20:23], v[16:19]
	v_mfma_f32_16x16x32_f16 v[4:7], v[66:69], v[20:23], v[4:7]
	s_mul_i32 s4, s8, s12
	s_ashr_i32 s3, s9, 31
	s_mul_hi_i32 s2, s8, s12
	s_mul_i32 s3, s4, s3
	s_mul_hi_u32 s5, s4, s9
	s_add_i32 s3, s5, s3
	s_mul_i32 s2, s2, s9
	s_add_i32 s3, s3, s2
	s_mul_i32 s2, s4, s9
	s_lshl_b64 s[2:3], s[2:3], 1
	v_or_b32_e32 v20, s13, v1
	v_lshlrev_b32_e32 v0, 2, v0
	s_add_u32 s0, s0, s2
	v_or3_b32 v21, v0, v2, s11
	s_addc_u32 s1, s1, s3
	v_mad_i64_i32 v[0:1], s[2:3], v20, s9, 0
	v_lshl_add_u64 v[0:1], v[0:1], 1, s[0:1]
	v_cvt_pk_f16_f32 v2, v12, v13
	v_lshlrev_b32_e32 v12, 1, v21
	v_mov_b32_e32 v13, 0
	v_cvt_pk_f16_f32 v3, v14, v15
	v_lshl_add_u64 v[0:1], v[0:1], 0, v[12:13]
	global_store_dwordx2 v[0:1], v[2:3], off
	v_cvt_pk_f16_f32 v3, v26, v27
	v_cvt_pk_f16_f32 v2, v24, v25
	global_store_dwordx2 v[0:1], v[2:3], off offset:32
	v_or_b32_e32 v0, 16, v20
	v_mad_i64_i32 v[0:1], s[2:3], v0, s9, 0
	v_lshl_add_u64 v[0:1], v[0:1], 1, s[0:1]
	v_cvt_pk_f16_f32 v3, v30, v31
	v_cvt_pk_f16_f32 v2, v28, v29
	v_lshl_add_u64 v[0:1], v[0:1], 0, v[12:13]
	global_store_dwordx2 v[0:1], v[2:3], off
	v_cvt_pk_f16_f32 v3, v40, v41
	v_cvt_pk_f16_f32 v2, v38, v39
	global_store_dwordx2 v[0:1], v[2:3], off offset:32
	v_or_b32_e32 v0, 32, v20
	v_mad_i64_i32 v[0:1], s[2:3], v0, s9, 0
	v_lshl_add_u64 v[0:1], v[0:1], 1, s[0:1]
	v_cvt_pk_f16_f32 v3, v34, v35
	v_cvt_pk_f16_f32 v2, v32, v33
	v_lshl_add_u64 v[0:1], v[0:1], 0, v[12:13]
	global_store_dwordx2 v[0:1], v[2:3], off
	v_cvt_pk_f16_f32 v3, v10, v11
	v_cvt_pk_f16_f32 v2, v8, v9
	global_store_dwordx2 v[0:1], v[2:3], off offset:32
	v_or_b32_e32 v0, 48, v20
	v_mad_i64_i32 v[0:1], s[2:3], v0, s9, 0
	v_lshl_add_u64 v[0:1], v[0:1], 1, s[0:1]
	v_cvt_pk_f16_f32 v3, v18, v19
	v_cvt_pk_f16_f32 v2, v16, v17
	v_lshl_add_u64 v[0:1], v[0:1], 0, v[12:13]
	global_store_dwordx2 v[0:1], v[2:3], off
	v_cvt_pk_f16_f32 v3, v6, v7
	v_cvt_pk_f16_f32 v2, v4, v5
	global_store_dwordx2 v[0:1], v[2:3], off offset:32
	s_endpgm
	s_endpgm
	s_endpgm
	s_endpgm
	s_endpgm
	s_endpgm
	s_endpgm
	s_endpgm
	s_endpgm
	s_endpgm
	s_endpgm
	s_endpgm
	s_endpgm
	s_endpgm
	s_endpgm
	s_endpgm
	s_endpgm
	s_endpgm
	s_endpgm
	s_endpgm
	s_endpgm
	s_endpgm
	s_endpgm
	s_endpgm
	s_endpgm
	s_endpgm
	s_endpgm
	s_endpgm
	s_endpgm
	s_endpgm
	s_endpgm
	s_endpgm
	s_endpgm
	s_endpgm
	s_endpgm
	s_endpgm
	s_endpgm
	s_endpgm
	s_endpgm
	s_endpgm
	s_endpgm
	s_endpgm
	s_endpgm
	s_endpgm
	s_endpgm
	s_endpgm
	s_endpgm
	s_endpgm
	s_endpgm

	.amdhsa_kernel _Z5gemm8ILi128ELi2ELi4ELi4ELi2ELi32EEvPKDF16_S1_iiiPDF16_PfPKf
		.amdhsa_group_segment_fixed_size 0
		.amdhsa_private_segment_fixed_size 0
		.amdhsa_kernarg_size 56
		.amdhsa_user_sgpr_count 2
		.amdhsa_user_sgpr_dispatch_ptr 0
		.amdhsa_user_sgpr_queue_ptr 0
		.amdhsa_user_sgpr_kernarg_segment_ptr 1
		.amdhsa_user_sgpr_dispatch_id 0
		.amdhsa_user_sgpr_kernarg_preload_length 0
		.amdhsa_user_sgpr_kernarg_preload_offset 0
		.amdhsa_user_sgpr_private_segment_size 0
		.amdhsa_uses_dynamic_stack 0
		.amdhsa_enable_private_segment 0
		.amdhsa_system_sgpr_workgroup_id_x 1
		.amdhsa_system_sgpr_workgroup_id_y 0
		.amdhsa_system_sgpr_workgroup_id_z 0
		.amdhsa_system_sgpr_workgroup_info 0
		.amdhsa_system_vgpr_workitem_id 0
		.amdhsa_next_free_vgpr 107
		.amdhsa_next_free_sgpr 36
		.amdhsa_accum_offset 108
		.amdhsa_reserve_vcc 0
		.amdhsa_float_round_mode_32 0
		.amdhsa_float_round_mode_16_64 0
		.amdhsa_float_denorm_mode_32 3
		.amdhsa_float_denorm_mode_16_64 3
		.amdhsa_dx10_clamp 1
		.amdhsa_ieee_mode 1
		.amdhsa_fp16_overflow 0
		.amdhsa_tg_split 0
		.amdhsa_exception_fp_ieee_invalid_op 0
		.amdhsa_exception_fp_denorm_src 0
		.amdhsa_exception_fp_ieee_div_zero 0
		.amdhsa_exception_fp_ieee_overflow 0
		.amdhsa_exception_fp_ieee_underflow 0
		.amdhsa_exception_fp_ieee_inexact 0
		.amdhsa_exception_int_div_zero 0
	.end_amdhsa_kernel

amdhsa.kernels:
  - .agpr_count:     0
    .args:
      - .offset:         0
        .size:           400
        .value_kind:     by_value
    .group_segment_fixed_size: 33280
    .kernarg_segment_align: 8
    .kernarg_segment_size: 400
    .language:       OpenCL C
    .language_version:
      - 2
      - 0
    .max_flat_workgroup_size: 256
    .name:           _Z10wt_convert7CvtJobs
    .private_segment_fixed_size: 0
    .sgpr_count:     54
    .sgpr_spill_count: 0
    .symbol:         _Z10wt_convert7CvtJobs.kd
    .uniform_work_group_size: 1
    .uses_dynamic_stack: false
    .vgpr_count:     45
    .vgpr_spill_count: 0
    .wavefront_size: 64
  - .agpr_count:     0
    .args:
      - .actual_access:  read_only
        .address_space:  global
        .offset:         0
        .size:           8
        .value_kind:     global_buffer
      - .actual_access:  read_only
        .address_space:  global
        .offset:         8
        .size:           8
        .value_kind:     global_buffer
      - .actual_access:  read_only
        .address_space:  global
        .offset:         16
        .size:           8
        .value_kind:     global_buffer
      - .actual_access:  write_only
        .address_space:  global
        .offset:         24
        .size:           8
        .value_kind:     global_buffer
      - .actual_access:  read_only
        .address_space:  global
        .offset:         32
        .size:           8
        .value_kind:     global_buffer
      - .actual_access:  read_only
        .address_space:  global
        .offset:         40
        .size:           8
        .value_kind:     global_buffer
      - .actual_access:  write_only
        .address_space:  global
        .offset:         48
        .size:           8
        .value_kind:     global_buffer
      - .offset:         56
        .size:           400
        .value_kind:     by_value
    .group_segment_fixed_size: 33280
    .kernarg_segment_align: 8
    .kernarg_segment_size: 456
    .language:       OpenCL C
    .language_version:
      - 2
      - 0
    .max_flat_workgroup_size: 256
    .name:           _Z13embed_ln_convPKiPKfS2_PfS2_S2_PDF16_7CvtJobs
    .private_segment_fixed_size: 0
    .sgpr_count:     36
    .sgpr_spill_count: 0
    .symbol:         _Z13embed_ln_convPKiPKfS2_PfS2_S2_PDF16_7CvtJobs.kd
    .uniform_work_group_size: 1
    .uses_dynamic_stack: false
    .vgpr_count:     79
    .vgpr_spill_count: 0
    .wavefront_size: 64
  - .agpr_count:     0
    .args:
      - .address_space:  global
        .offset:         0
        .size:           8
        .value_kind:     global_buffer
      - .address_space:  global
        .offset:         8
        .size:           8
        .value_kind:     global_buffer
      - .actual_access:  write_only
        .address_space:  global
        .offset:         16
        .size:           8
        .value_kind:     global_buffer
      - .actual_access:  read_only
        .address_space:  global
        .offset:         24
        .size:           8
        .value_kind:     global_buffer
      - .offset:         32
        .size:           4
        .value_kind:     by_value
      - .offset:         36
        .size:           4
        .value_kind:     by_value
      - .offset:         40
        .size:           4
        .value_kind:     by_value
    .group_segment_fixed_size: 0
    .kernarg_segment_align: 8
    .kernarg_segment_size: 44
    .language:       OpenCL C
    .language_version:
      - 2
      - 0
    .max_flat_workgroup_size: 512
    .name:           _Z17gemm_256sq_8phasePKDF16_S0_PfPKfiii
    .private_segment_fixed_size: 0
    .sgpr_count:     47
    .sgpr_spill_count: 0
    .symbol:         _Z17gemm_256sq_8phasePKDF16_S0_PfPKfiii.kd
    .uniform_work_group_size: 1
    .uses_dynamic_stack: false
    .vgpr_count:     244
    .vgpr_spill_count: 0
    .wavefront_size: 64
  - .agpr_count:     0
    .args:
      - .actual_access:  read_only
        .address_space:  global
        .offset:         0
        .size:           8
        .value_kind:     global_buffer
      - .actual_access:  read_only
        .address_space:  global
        .offset:         8
        .size:           8
        .value_kind:     global_buffer
      - .actual_access:  read_only
        .address_space:  global
        .offset:         16
        .size:           8
        .value_kind:     global_buffer
      - .actual_access:  write_only
        .address_space:  global
        .offset:         24
        .size:           8
        .value_kind:     global_buffer
      - .offset:         32
        .size:           400
        .value_kind:     by_value
    .group_segment_fixed_size: 33280
    .kernarg_segment_align: 8
    .kernarg_segment_size: 432
    .language:       OpenCL C
    .language_version:
      - 2
      - 0
    .max_flat_workgroup_size: 256
    .name:           _Z11attn_kernelPKDF16_S0_S0_PDF16_7CvtJobs
    .private_segment_fixed_size: 0
    .sgpr_count:     36
    .sgpr_spill_count: 0
    .symbol:         _Z11attn_kernelPKDF16_S0_S0_PDF16_7CvtJobs.kd
    .uniform_work_group_size: 1
    .uses_dynamic_stack: false
    .vgpr_count:     116
    .vgpr_spill_count: 0
    .wavefront_size: 64
  - .agpr_count:     0
    .args:
      - .address_space:  global
        .offset:         0
        .size:           8
        .value_kind:     global_buffer
      - .address_space:  global
        .offset:         8
        .size:           8
        .value_kind:     global_buffer
      - .offset:         16
        .size:           4
        .value_kind:     by_value
      - .offset:         20
        .size:           4
        .value_kind:     by_value
      - .offset:         24
        .size:           4
        .value_kind:     by_value
      - .actual_access:  write_only
        .address_space:  global
        .offset:         32
        .size:           8
        .value_kind:     global_buffer
      - .actual_access:  read_only
        .address_space:  global
        .offset:         40
        .size:           8
        .value_kind:     global_buffer
      - .actual_access:  read_only
        .address_space:  global
        .offset:         48
        .size:           8
        .value_kind:     global_buffer
      - .offset:         56
        .size:           4
        .value_kind:     hidden_block_count_x
      - .offset:         60
        .size:           4
        .value_kind:     hidden_block_count_y
      - .offset:         64
        .size:           4
        .value_kind:     hidden_block_count_z
      - .offset:         68
        .size:           2
        .value_kind:     hidden_group_size_x
      - .offset:         70
        .size:           2
        .value_kind:     hidden_group_size_y
      - .offset:         72
        .size:           2
        .value_kind:     hidden_group_size_z
      - .offset:         74
        .size:           2
        .value_kind:     hidden_remainder_x
      - .offset:         76
        .size:           2
        .value_kind:     hidden_remainder_y
      - .offset:         78
        .size:           2
        .value_kind:     hidden_remainder_z
      - .offset:         96
        .size:           8
        .value_kind:     hidden_global_offset_x
      - .offset:         104
        .size:           8
        .value_kind:     hidden_global_offset_y
      - .offset:         112
        .size:           8
        .value_kind:     hidden_global_offset_z
      - .offset:         120
        .size:           2
        .value_kind:     hidden_grid_dims
      - .offset:         176
        .size:           4
        .value_kind:     hidden_dynamic_lds_size
    .group_segment_fixed_size: 0
    .kernarg_segment_align: 8
    .kernarg_segment_size: 312
    .language:       OpenCL C
    .language_version:
      - 2
      - 0
    .max_flat_workgroup_size: 512
    .name:           _Z5gemm8ILi192ELi2ELi3ELi0ELi1ELi16EEvPKDF16_S1_iiiPDF16_PfPKf
    .private_segment_fixed_size: 0
    .sgpr_count:     38
    .sgpr_spill_count: 0
    .symbol:         _Z5gemm8ILi192ELi2ELi3ELi0ELi1ELi16EEvPKDF16_S1_iiiPDF16_PfPKf.kd
    .uniform_work_group_size: 1
    .uses_dynamic_stack: false
    .vgpr_count:     125
    .vgpr_spill_count: 0
    .wavefront_size: 64
  - .agpr_count:     0
    .args:
      - .address_space:  global
        .offset:         0
        .size:           8
        .value_kind:     global_buffer
      - .address_space:  global
        .offset:         8
        .size:           8
        .value_kind:     global_buffer
      - .offset:         16
        .size:           4
        .value_kind:     by_value
      - .offset:         20
        .size:           4
        .value_kind:     by_value
      - .offset:         24
        .size:           4
        .value_kind:     by_value
      - .actual_access:  write_only
        .address_space:  global
        .offset:         32
        .size:           8
        .value_kind:     global_buffer
      - .actual_access:  read_only
        .address_space:  global
        .offset:         40
        .size:           8
        .value_kind:     global_buffer
      - .actual_access:  read_only
        .address_space:  global
        .offset:         48
        .size:           8
        .value_kind:     global_buffer
      - .offset:         56
        .size:           4
        .value_kind:     hidden_block_count_x
      - .offset:         60
        .size:           4
        .value_kind:     hidden_block_count_y
      - .offset:         64
        .size:           4
        .value_kind:     hidden_block_count_z
      - .offset:         68
        .size:           2
        .value_kind:     hidden_group_size_x
      - .offset:         70
        .size:           2
        .value_kind:     hidden_group_size_y
      - .offset:         72
        .size:           2
        .value_kind:     hidden_group_size_z
      - .offset:         74
        .size:           2
        .value_kind:     hidden_remainder_x
      - .offset:         76
        .size:           2
        .value_kind:     hidden_remainder_y
      - .offset:         78
        .size:           2
        .value_kind:     hidden_remainder_z
      - .offset:         96
        .size:           8
        .value_kind:     hidden_global_offset_x
      - .offset:         104
        .size:           8
        .value_kind:     hidden_global_offset_y
      - .offset:         112
        .size:           8
        .value_kind:     hidden_global_offset_z
      - .offset:         120
        .size:           2
        .value_kind:     hidden_grid_dims
      - .offset:         176
        .size:           4
        .value_kind:     hidden_dynamic_lds_size
    .group_segment_fixed_size: 0
    .kernarg_segment_align: 8
    .kernarg_segment_size: 312
    .language:       OpenCL C
    .language_version:
      - 2
      - 0
    .max_flat_workgroup_size: 512
    .name:           _Z5gemm8ILi128ELi2ELi2ELi2ELi1ELi16EEvPKDF16_S1_iiiPDF16_PfPKf
    .private_segment_fixed_size: 0
    .sgpr_count:     34
    .sgpr_spill_count: 0
    .symbol:         _Z5gemm8ILi128ELi2ELi2ELi2ELi1ELi16EEvPKDF16_S1_iiiPDF16_PfPKf.kd
    .uniform_work_group_size: 1
    .uses_dynamic_stack: false
    .vgpr_count:     90
    .vgpr_spill_count: 0
    .wavefront_size: 64
  - .agpr_count:     0
    .args:
      - .address_space:  global
        .offset:         0
        .size:           8
        .value_kind:     global_buffer
      - .address_space:  global
        .offset:         8
        .size:           8
        .value_kind:     global_buffer
      - .offset:         16
        .size:           4
        .value_kind:     by_value
      - .offset:         20
        .size:           4
        .value_kind:     by_value
      - .offset:         24
        .size:           4
        .value_kind:     by_value
      - .actual_access:  read_only
        .address_space:  global
        .offset:         32
        .size:           8
        .value_kind:     global_buffer
      - .address_space:  global
        .offset:         40
        .size:           8
        .value_kind:     global_buffer
      - .actual_access:  read_only
        .address_space:  global
        .offset:         48
        .size:           8
        .value_kind:     global_buffer
      - .offset:         56
        .size:           4
        .value_kind:     hidden_block_count_x
      - .offset:         60
        .size:           4
        .value_kind:     hidden_block_count_y
      - .offset:         64
        .size:           4
        .value_kind:     hidden_block_count_z
      - .offset:         68
        .size:           2
        .value_kind:     hidden_group_size_x
      - .offset:         70
        .size:           2
        .value_kind:     hidden_group_size_y
      - .offset:         72
        .size:           2
        .value_kind:     hidden_group_size_z
      - .offset:         74
        .size:           2
        .value_kind:     hidden_remainder_x
      - .offset:         76
        .size:           2
        .value_kind:     hidden_remainder_y
      - .offset:         78
        .size:           2
        .value_kind:     hidden_remainder_z
      - .offset:         96
        .size:           8
        .value_kind:     hidden_global_offset_x
      - .offset:         104
        .size:           8
        .value_kind:     hidden_global_offset_y
      - .offset:         112
        .size:           8
        .value_kind:     hidden_global_offset_z
      - .offset:         120
        .size:           2
        .value_kind:     hidden_grid_dims
      - .offset:         176
        .size:           4
        .value_kind:     hidden_dynamic_lds_size
    .group_segment_fixed_size: 0
    .kernarg_segment_align: 8
    .kernarg_segment_size: 312
    .language:       OpenCL C
    .language_version:
      - 2
      - 0
    .max_flat_workgroup_size: 512
    .name:           _Z5gemm8ILi64ELi4ELi6ELi1ELi1ELi16EEvPKDF16_S1_iiiPDF16_PfPKf
    .private_segment_fixed_size: 0
    .sgpr_count:     38
    .sgpr_spill_count: 0
    .symbol:         _Z5gemm8ILi64ELi4ELi6ELi1ELi1ELi16EEvPKDF16_S1_iiiPDF16_PfPKf.kd
    .uniform_work_group_size: 1
    .uses_dynamic_stack: false
    .vgpr_count:     104
    .vgpr_spill_count: 0
    .wavefront_size: 64
  - .agpr_count:     0
    .args:
      - .address_space:  global
        .offset:         0
        .size:           8
        .value_kind:     global_buffer
      - .address_space:  global
        .offset:         8
        .size:           8
        .value_kind:     global_buffer
      - .offset:         16
        .size:           4
        .value_kind:     by_value
      - .offset:         20
        .size:           4
        .value_kind:     by_value
      - .offset:         24
        .size:           4
        .value_kind:     by_value
      - .actual_access:  write_only
        .address_space:  global
        .offset:         32
        .size:           8
        .value_kind:     global_buffer
      - .actual_access:  read_only
        .address_space:  global
        .offset:         40
        .size:           8
        .value_kind:     global_buffer
      - .actual_access:  read_only
        .address_space:  global
        .offset:         48
        .size:           8
        .value_kind:     global_buffer
    .group_segment_fixed_size: 0
    .kernarg_segment_align: 8
    .kernarg_segment_size: 56
    .language:       OpenCL C
    .language_version:
      - 2
      - 0
    .max_flat_workgroup_size: 512
    .name:           _Z5gemm8ILi128ELi2ELi4ELi4ELi2ELi32EEvPKDF16_S1_iiiPDF16_PfPKf
    .private_segment_fixed_size: 0
    .sgpr_count:     42
    .sgpr_spill_count: 0
    .symbol:         _Z5gemm8ILi128ELi2ELi4ELi4ELi2ELi32EEvPKDF16_S1_iiiPDF16_PfPKf.kd
    .uniform_work_group_size: 1
    .uses_dynamic_stack: false
    .vgpr_count:     107
    .vgpr_spill_count: 0
    .wavefront_size: 64
  - .agpr_count:     0
    .args:
      - .actual_access:  read_only
        .address_space:  global
        .offset:         0
        .size:           8
        .value_kind:     global_buffer
      - .actual_access:  read_only
        .address_space:  global
        .offset:         8
        .size:           8
        .value_kind:     global_buffer
      - .actual_access:  read_only
        .address_space:  global
        .offset:         16
        .size:           8
        .value_kind:     global_buffer
      - .address_space:  global
        .offset:         24
        .size:           8
        .value_kind:     global_buffer
      - .actual_access:  read_only
        .address_space:  global
        .offset:         32
        .size:           8
        .value_kind:     global_buffer
      - .actual_access:  read_only
        .address_space:  global
        .offset:         40
        .size:           8
        .value_kind:     global_buffer
      - .actual_access:  write_only
        .address_space:  global
        .offset:         48
        .size:           8
        .value_kind:     global_buffer
    .group_segment_fixed_size: 0
    .kernarg_segment_align: 8
    .kernarg_segment_size: 56
    .language:       OpenCL C
    .language_version:
      - 2
      - 0
    .max_flat_workgroup_size: 256
    .name:           _Z9ln_kernelILi2EEvPKiPKfS3_PfS3_S3_PDF16_
    .private_segment_fixed_size: 0
    .sgpr_count:     18
    .sgpr_spill_count: 0
    .symbol:         _Z9ln_kernelILi2EEvPKiPKfS3_PfS3_S3_PDF16_.kd
    .uniform_work_group_size: 1
    .uses_dynamic_stack: false
    .vgpr_count:     58
    .vgpr_spill_count: 0
    .wavefront_size: 64
  - .agpr_count:     0
    .args:
      - .actual_access:  read_only
        .address_space:  global
        .offset:         0
        .size:           8
        .value_kind:     global_buffer
      - .actual_access:  read_only
        .address_space:  global
        .offset:         8
        .size:           8
        .value_kind:     global_buffer
      - .actual_access:  read_only
        .address_space:  global
        .offset:         16
        .size:           8
        .value_kind:     global_buffer
      - .actual_access:  read_only
        .address_space:  global
        .offset:         24
        .size:           8
        .value_kind:     global_buffer
      - .actual_access:  read_only
        .address_space:  global
        .offset:         32
        .size:           8
        .value_kind:     global_buffer
      - .actual_access:  read_only
        .address_space:  global
        .offset:         40
        .size:           8
        .value_kind:     global_buffer
      - .actual_access:  write_only
        .address_space:  global
        .offset:         48
        .size:           8
        .value_kind:     global_buffer
    .group_segment_fixed_size: 0
    .kernarg_segment_align: 8
    .kernarg_segment_size: 56
    .language:       OpenCL C
    .language_version:
      - 2
      - 0
    .max_flat_workgroup_size: 256
    .name:           _Z9ln_kernelILi0EEvPKiPKfS3_PfS3_S3_PDF16_
    .private_segment_fixed_size: 0
    .sgpr_count:     18
    .sgpr_spill_count: 0
    .symbol:         _Z9ln_kernelILi0EEvPKiPKfS3_PfS3_S3_PDF16_.kd
    .uniform_work_group_size: 1
    .uses_dynamic_stack: false
    .vgpr_count:     60
    .vgpr_spill_count: 0
    .wavefront_size: 64
  - .agpr_count:     0
    .args:
      - .actual_access:  read_only
        .address_space:  global
        .offset:         0
        .size:           8
        .value_kind:     global_buffer
      - .actual_access:  read_only
        .address_space:  global
        .offset:         8
        .size:           8
        .value_kind:     global_buffer
      - .actual_access:  read_only
        .address_space:  global
        .offset:         16
        .size:           8
        .value_kind:     global_buffer
      - .actual_access:  read_only
        .address_space:  global
        .offset:         24
        .size:           8
        .value_kind:     global_buffer
      - .actual_access:  read_only
        .address_space:  global
        .offset:         32
        .size:           8
        .value_kind:     global_buffer
      - .actual_access:  read_only
        .address_space:  global
        .offset:         40
        .size:           8
        .value_kind:     global_buffer
      - .actual_access:  write_only
        .address_space:  global
        .offset:         48
        .size:           8
        .value_kind:     global_buffer
    .group_segment_fixed_size: 0
    .kernarg_segment_align: 8
    .kernarg_segment_size: 56
    .language:       OpenCL C
    .language_version:
      - 2
      - 0
    .max_flat_workgroup_size: 256
    .name:           _Z9ln_kernelILi4EEvPKiPKfS3_PfS3_S3_PDF16_
    .private_segment_fixed_size: 0
    .sgpr_count:     18
    .sgpr_spill_count: 0
    .symbol:         _Z9ln_kernelILi4EEvPKiPKfS3_PfS3_S3_PDF16_.kd
    .uniform_work_group_size: 1
    .uses_dynamic_stack: false
    .vgpr_count:     64
    .vgpr_spill_count: 0
    .wavefront_size: 64
